# defer last MFMA group of each main-loop K tile past the tile barrier (fills LDS-latency bubble), plus P6 epilogue load hoist
# speedup vs baseline: 1.0115x; 1.0115x over previous
;     ...
;     for (int ui = 0;; ++ui) {
; #pragma unroll
;         for (int m = 0; m < MF; ++m)
; #pragma unroll
;             for (int n = 0; n < 4; ++n) acc[m][n] = (f32x4){0.f, 0.f, 0.f, 0.f};
;         for (int t = 0; t < nt - 2; t += 2) {
;             G_TILE(G_A0, G_B0, true, G_B1, G_A1, t + 1, true, t + 2, (void)0);
.LBB0_69:
	s_andn2_b64 vcc, exec, s[30:31]
	v_mov_b32_e32 v159, 0
	s_cbranch_vccnz .LBB0_72
	v_mov_b32_e32 v32, 0
	s_mov_b32 s8, 0
	s_mov_b32 s9, 0x5a0000
	s_movk_i32 s24, 0x100
	v_mov_b32_e32 v33, v32
	v_mov_b32_e32 v34, v32
	v_mov_b32_e32 v35, v32
	v_mov_b32_e32 v36, v32
	v_mov_b32_e32 v37, v32
	v_mov_b32_e32 v38, v32
	v_mov_b32_e32 v39, v32
	v_mov_b32_e32 v40, v32
	v_mov_b32_e32 v41, v32
	v_mov_b32_e32 v42, v32
	v_mov_b32_e32 v43, v32
	v_mov_b32_e32 v44, v32
	v_mov_b32_e32 v45, v32
	v_mov_b32_e32 v46, v32
	v_mov_b32_e32 v47, v32
	v_mov_b32_e32 v48, v32
	v_mov_b32_e32 v49, v32
	v_mov_b32_e32 v50, v32
	v_mov_b32_e32 v51, v32
	v_mov_b32_e32 v52, v32
	v_mov_b32_e32 v53, v32
	v_mov_b32_e32 v54, v32
	v_mov_b32_e32 v55, v32
	v_mov_b32_e32 v56, v32
	v_mov_b32_e32 v57, v32
	v_mov_b32_e32 v58, v32
	v_mov_b32_e32 v59, v32
	v_mov_b32_e32 v60, v32
	v_mov_b32_e32 v61, v32
	v_mov_b32_e32 v62, v32
	v_mov_b32_e32 v63, v32
	v_mov_b32_e32 v64, v32
	v_mov_b32_e32 v65, v32
	v_mov_b32_e32 v66, v32
	v_mov_b32_e32 v67, v32
	v_mov_b32_e32 v68, v32
	v_mov_b32_e32 v69, v32
	v_mov_b32_e32 v70, v32
	v_mov_b32_e32 v71, v32
	v_mov_b32_e32 v72, v32
	v_mov_b32_e32 v73, v32
	v_mov_b32_e32 v74, v32
	v_mov_b32_e32 v75, v32
	v_mov_b32_e32 v76, v32
	v_mov_b32_e32 v77, v32
	v_mov_b32_e32 v78, v32
	v_mov_b32_e32 v79, v32
	v_mov_b32_e32 v80, v32
	v_mov_b32_e32 v81, v32
	v_mov_b32_e32 v82, v32
	v_mov_b32_e32 v83, v32
	v_mov_b32_e32 v84, v32
	v_mov_b32_e32 v85, v32
	v_mov_b32_e32 v86, v32
	v_mov_b32_e32 v87, v32
	v_mov_b32_e32 v88, v32
	v_mov_b32_e32 v89, v32
	v_mov_b32_e32 v90, v32
	v_mov_b32_e32 v91, v32
	v_mov_b32_e32 v92, v32
	v_mov_b32_e32 v93, v32
	v_mov_b32_e32 v94, v32
	v_mov_b32_e32 v95, v32
	v_mov_b32_e32 v96, v32
	v_mov_b32_e32 v97, v32
	v_mov_b32_e32 v98, v32
	v_mov_b32_e32 v99, v32
	v_mov_b32_e32 v100, v32
	v_mov_b32_e32 v101, v32
	v_mov_b32_e32 v102, v32
	v_mov_b32_e32 v103, v32
	v_mov_b32_e32 v104, v32
	v_mov_b32_e32 v105, v32
	v_mov_b32_e32 v106, v32
	v_mov_b32_e32 v107, v32
	v_mov_b32_e32 v108, v32
	v_mov_b32_e32 v109, v32
	v_mov_b32_e32 v110, v32
	v_mov_b32_e32 v111, v32
	v_mov_b32_e32 v112, v32
	v_mov_b32_e32 v113, v32
	v_mov_b32_e32 v114, v32
	v_mov_b32_e32 v115, v32
	v_mov_b32_e32 v116, v32
	v_mov_b32_e32 v117, v32
	v_mov_b32_e32 v118, v32
	v_mov_b32_e32 v119, v32
	v_mov_b32_e32 v120, v32
	v_mov_b32_e32 v121, v32
	v_mov_b32_e32 v122, v32
	v_mov_b32_e32 v123, v32
	v_mov_b32_e32 v124, v32
	v_mov_b32_e32 v125, v32
	v_mov_b32_e32 v126, v32
	v_mov_b32_e32 v127, v32
	v_mov_b32_e32 v128, v32
	v_mov_b32_e32 v129, v32
	v_mov_b32_e32 v130, v32
	v_mov_b32_e32 v131, v32
	v_mov_b32_e32 v132, v32
	v_mov_b32_e32 v133, v32
	v_mov_b32_e32 v134, v32
	v_mov_b32_e32 v135, v32
	v_mov_b32_e32 v136, v32
	v_mov_b32_e32 v137, v32
	v_mov_b32_e32 v138, v32
	v_mov_b32_e32 v139, v32
	v_mov_b32_e32 v140, v32
	v_mov_b32_e32 v141, v32
	v_mov_b32_e32 v142, v32
	v_mov_b32_e32 v143, v32
	v_mov_b32_e32 v144, v32
	v_mov_b32_e32 v145, v32
	v_mov_b32_e32 v146, v32
	v_mov_b32_e32 v147, v32
	v_mov_b32_e32 v148, v32
	v_mov_b32_e32 v149, v32
	v_mov_b32_e32 v150, v32
	v_mov_b32_e32 v151, v32
	v_mov_b32_e32 v152, v32
	v_mov_b32_e32 v153, v32
	v_mov_b32_e32 v154, v32
	v_mov_b32_e32 v155, v32
	v_mov_b32_e32 v156, v32
	v_mov_b32_e32 v157, v32
	v_mov_b32_e32 v158, v32
	v_mov_b32_e32 v159, v32
	v_mov_b32_e32 v198, 0
	v_mov_b32_e32 v199, 0
	v_mov_b32_e32 v200, 0
	v_mov_b32_e32 v201, 0
	v_mov_b32_e32 v202, 0
	v_mov_b32_e32 v203, 0
	v_mov_b32_e32 v204, 0
	v_mov_b32_e32 v205, 0
	v_mov_b32_e32 v244, 0
	v_mov_b32_e32 v245, 0
	v_mov_b32_e32 v246, 0
	v_mov_b32_e32 v247, 0
	v_mov_b32_e32 v248, 0
	v_mov_b32_e32 v249, 0
	v_mov_b32_e32 v250, 0
	v_mov_b32_e32 v251, 0
	v_mov_b32_e32 v252, 0
	v_mov_b32_e32 v253, 0
	v_mov_b32_e32 v254, 0
	v_mov_b32_e32 v255, 0
.LBB0_71:
	s_mov_b32 m0, s68
	s_add_i32 s25, s24, 0xffffff80
	ds_read_b64_tr_b16 v[170:171], v166
	ds_read_b64_tr_b16 v[172:173], v167
	ds_read_b64_tr_b16 v[176:177], v167 offset:32
	ds_read_b128 v[178:181], v162
	ds_read_b64_tr_b16 v[174:175], v166 offset:32
	ds_read_b64_tr_b16 v[182:183], v166 offset:64
	ds_read_b64_tr_b16 v[186:187], v166 offset:96
	ds_read_b64_tr_b16 v[184:185], v167 offset:64
	ds_read_b64_tr_b16 v[188:189], v167 offset:96
	ds_read_b128 v[190:193], v162 offset:2048
	ds_read_b128 v[194:197], v162 offset:4096
	buffer_load_dwordx4 v163, s[20:23], s25 offen lds
	s_mov_b32 m0, s67
	v_mfma_f32_16x16x32_bf16 v[44:47], v[244:247], v[252:255], v[44:47]
	v_mfma_f32_16x16x32_bf16 v[40:43], v[248:251], v[252:255], v[40:43]
	v_mfma_f32_16x16x32_bf16 v[36:39], v[198:201], v[252:255], v[36:39]
	v_mfma_f32_16x16x32_bf16 v[32:35], v[202:205], v[252:255], v[32:35]
	s_waitcnt lgkmcnt(7)
	v_mfma_f32_16x16x32_bf16 v[156:159], v[170:173], v[178:181], v[156:159]
	buffer_load_dwordx4 v165, s[20:23], s25 offen lds
	s_mov_b32 m0, s66
	s_nop 0
	buffer_load_dwordx4 v164, s[20:23], s25 offen lds
	s_mov_b32 m0, s65
	s_waitcnt lgkmcnt(6)
	v_mfma_f32_16x16x32_bf16 v[152:155], v[174:177], v[178:181], v[152:155]
	buffer_load_dwordx4 v168, s[20:23], s25 offen lds
	s_add_i32 s25, s9, 0xffd60000
	s_waitcnt lgkmcnt(3)
	v_mfma_f32_16x16x32_bf16 v[148:151], v[182:185], v[178:181], v[148:151]
	s_waitcnt lgkmcnt(2)
	v_mfma_f32_16x16x32_bf16 v[144:147], v[186:189], v[178:181], v[144:147]
	s_waitcnt lgkmcnt(1)
	v_mfma_f32_16x16x32_bf16 v[140:143], v[170:173], v[190:193], v[140:143]
	ds_read_b128 v[178:181], v162 offset:6144
	s_waitcnt vmcnt(11)
	v_cvt_pk_bf16_f32 v15, v14, v15
	v_cvt_pk_bf16_f32 v14, v12, v13
	v_mfma_f32_16x16x32_bf16 v[136:139], v[174:177], v[190:193], v[136:139]
	ds_write_b64 v161, v[14:15] offset:34816
	v_mfma_f32_16x16x32_bf16 v[132:135], v[182:185], v[190:193], v[132:135]
	v_mfma_f32_16x16x32_bf16 v[128:131], v[186:189], v[190:193], v[128:131]
	buffer_load_dwordx4 v[12:15], v160, s[12:15], s25 offen
	s_waitcnt lgkmcnt(2)
	v_mfma_f32_16x16x32_bf16 v[124:127], v[170:173], v[194:197], v[124:127]
	ds_read_b128 v[190:193], v162 offset:8192
	v_mfma_f32_16x16x32_bf16 v[120:123], v[174:177], v[194:197], v[120:123]
	v_mfma_f32_16x16x32_bf16 v[116:119], v[182:185], v[194:197], v[116:119]
	v_mfma_f32_16x16x32_bf16 v[112:115], v[186:189], v[194:197], v[112:115]
	s_waitcnt lgkmcnt(2)
	v_mfma_f32_16x16x32_bf16 v[108:111], v[170:173], v[178:181], v[108:111]
	ds_read_b128 v[194:197], v162 offset:10240
	s_waitcnt vmcnt(11)
	v_cvt_pk_bf16_f32 v3, v2, v3
	v_cvt_pk_bf16_f32 v2, v0, v1
	v_mfma_f32_16x16x32_bf16 v[104:107], v[174:177], v[178:181], v[104:107]
	ds_write_b64 v161, v[2:3] offset:43520
	v_mfma_f32_16x16x32_bf16 v[100:103], v[182:185], v[178:181], v[100:103]
	v_mfma_f32_16x16x32_bf16 v[96:99], v[186:189], v[178:181], v[96:99]
	s_add_i32 s26, s9, 0xffdc0000
	buffer_load_dwordx4 v[0:3], v160, s[12:15], s26 offen
	s_waitcnt lgkmcnt(2)
	v_mfma_f32_16x16x32_bf16 v[92:95], v[170:173], v[190:193], v[92:95]
	ds_read_b128 v[178:181], v162 offset:12288
	v_mfma_f32_16x16x32_bf16 v[88:91], v[174:177], v[190:193], v[88:91]
	v_mfma_f32_16x16x32_bf16 v[84:87], v[182:185], v[190:193], v[84:87]
	v_mfma_f32_16x16x32_bf16 v[80:83], v[186:189], v[190:193], v[80:83]
	s_waitcnt lgkmcnt(2)
	v_mfma_f32_16x16x32_bf16 v[76:79], v[170:173], v[194:197], v[76:79]
	ds_read_b128 v[190:193], v162 offset:14336
	s_waitcnt vmcnt(11)
	v_cvt_pk_bf16_f32 v31, v30, v31
	v_cvt_pk_bf16_f32 v30, v28, v29
	v_mfma_f32_16x16x32_bf16 v[72:75], v[174:177], v[194:197], v[72:75]
	ds_write_b64 v161, v[30:31] offset:52224
	v_mfma_f32_16x16x32_bf16 v[68:71], v[182:185], v[194:197], v[68:71]
	v_mfma_f32_16x16x32_bf16 v[64:67], v[186:189], v[194:197], v[64:67]
	s_add_i32 s27, s9, 0xffe20000
	buffer_load_dwordx4 v[28:31], v160, s[12:15], s27 offen
	s_waitcnt lgkmcnt(2)
	v_mfma_f32_16x16x32_bf16 v[60:63], v[170:173], v[178:181], v[60:63]
	ds_read_b128 v[194:197], v162 offset:1024
	v_mfma_f32_16x16x32_bf16 v[56:59], v[174:177], v[178:181], v[56:59]
	v_mfma_f32_16x16x32_bf16 v[52:55], v[182:185], v[178:181], v[52:55]
	v_mfma_f32_16x16x32_bf16 v[48:51], v[186:189], v[178:181], v[48:51]
	s_waitcnt lgkmcnt(2)
	v_mfma_f32_16x16x32_bf16 v[44:47], v[170:173], v[190:193], v[44:47]
	ds_read_b128 v[170:173], v162 offset:3072
	s_waitcnt vmcnt(11)
	v_cvt_pk_bf16_f32 v27, v26, v27
	v_cvt_pk_bf16_f32 v26, v24, v25
	v_mfma_f32_16x16x32_bf16 v[40:43], v[174:177], v[190:193], v[40:43]
	ds_read_b64_tr_b16 v[244:245], v166 offset:17408
	ds_read_b64_tr_b16 v[248:249], v166 offset:17440
	ds_read_b64_tr_b16 v[198:199], v166 offset:17472
	ds_read_b64_tr_b16 v[202:203], v166 offset:17504
	ds_read_b64_tr_b16 v[246:247], v167 offset:17408
	ds_read_b64_tr_b16 v[250:251], v167 offset:17440
	ds_read_b64_tr_b16 v[200:201], v167 offset:17472
	ds_read_b64_tr_b16 v[204:205], v167 offset:17504
	ds_write_b64 v161, v[26:27] offset:60928
	v_mfma_f32_16x16x32_bf16 v[36:39], v[182:185], v[190:193], v[36:39]
	v_mfma_f32_16x16x32_bf16 v[32:35], v[186:189], v[190:193], v[32:35]
	s_add_i32 s42, s9, 0xffe80000
	buffer_load_dwordx4 v[24:27], v160, s[12:15], s42 offen
	s_waitcnt lgkmcnt(4)
	v_mfma_f32_16x16x32_bf16 v[156:159], v[244:247], v[194:197], v[156:159]
	ds_read_b128 v[182:185], v162 offset:5120
	s_waitcnt lgkmcnt(4)
	v_mfma_f32_16x16x32_bf16 v[152:155], v[248:251], v[194:197], v[152:155]
	s_waitcnt lgkmcnt(3)
	v_mfma_f32_16x16x32_bf16 v[148:151], v[198:201], v[194:197], v[148:151]
	s_waitcnt lgkmcnt(2)
	v_mfma_f32_16x16x32_bf16 v[144:147], v[202:205], v[194:197], v[144:147]
	v_mfma_f32_16x16x32_bf16 v[140:143], v[244:247], v[170:173], v[140:143]
	ds_read_b128 v[186:189], v162 offset:7168
	s_waitcnt vmcnt(11)
	v_cvt_pk_bf16_f32 v23, v22, v23
	v_cvt_pk_bf16_f32 v22, v20, v21
	v_mfma_f32_16x16x32_bf16 v[136:139], v[248:251], v[170:173], v[136:139]
	ds_write_b64 v161, v[22:23] offset:35072
	v_mfma_f32_16x16x32_bf16 v[132:135], v[198:201], v[170:173], v[132:135]
	v_mfma_f32_16x16x32_bf16 v[128:131], v[202:205], v[170:173], v[128:131]
	buffer_load_dwordx4 v[20:23], v160, s[16:19], s25 offen
	s_waitcnt lgkmcnt(2)
	v_mfma_f32_16x16x32_bf16 v[124:127], v[244:247], v[182:185], v[124:127]
	ds_read_b128 v[170:173], v162 offset:9216
	v_mfma_f32_16x16x32_bf16 v[120:123], v[248:251], v[182:185], v[120:123]
	v_mfma_f32_16x16x32_bf16 v[116:119], v[198:201], v[182:185], v[116:119]
	v_mfma_f32_16x16x32_bf16 v[112:115], v[202:205], v[182:185], v[112:115]
	s_waitcnt lgkmcnt(2)
	v_mfma_f32_16x16x32_bf16 v[108:111], v[244:247], v[186:189], v[108:111]
	ds_read_b128 v[182:185], v162 offset:11264
	s_waitcnt vmcnt(11)
	v_cvt_pk_bf16_f32 v7, v6, v7
	v_cvt_pk_bf16_f32 v6, v4, v5
	v_mfma_f32_16x16x32_bf16 v[104:107], v[248:251], v[186:189], v[104:107]
	ds_write_b64 v161, v[6:7] offset:43776
	v_mfma_f32_16x16x32_bf16 v[100:103], v[198:201], v[186:189], v[100:103]
	v_mfma_f32_16x16x32_bf16 v[96:99], v[202:205], v[186:189], v[96:99]
	buffer_load_dwordx4 v[4:7], v160, s[16:19], s26 offen
	s_waitcnt lgkmcnt(2)
	v_mfma_f32_16x16x32_bf16 v[92:95], v[244:247], v[170:173], v[92:95]
	ds_read_b128 v[186:189], v162 offset:13312
	v_mfma_f32_16x16x32_bf16 v[88:91], v[248:251], v[170:173], v[88:91]
	v_mfma_f32_16x16x32_bf16 v[84:87], v[198:201], v[170:173], v[84:87]
	v_mfma_f32_16x16x32_bf16 v[80:83], v[202:205], v[170:173], v[80:83]
	s_waitcnt lgkmcnt(2)
	v_mfma_f32_16x16x32_bf16 v[76:79], v[244:247], v[182:185], v[76:79]
	ds_read_b128 v[252:255], v162 offset:15360
	s_waitcnt vmcnt(11)
	v_cvt_pk_bf16_f32 v11, v10, v11
	v_cvt_pk_bf16_f32 v10, v8, v9
	v_mfma_f32_16x16x32_bf16 v[72:75], v[248:251], v[182:185], v[72:75]
	ds_write_b64 v161, v[10:11] offset:52480
	v_mfma_f32_16x16x32_bf16 v[68:71], v[198:201], v[182:185], v[68:71]
	v_mfma_f32_16x16x32_bf16 v[64:67], v[202:205], v[182:185], v[64:67]
	buffer_load_dwordx4 v[8:11], v160, s[16:19], s27 offen
	s_waitcnt lgkmcnt(2)
	v_mfma_f32_16x16x32_bf16 v[60:63], v[244:247], v[186:189], v[60:63]
	v_mfma_f32_16x16x32_bf16 v[56:59], v[248:251], v[186:189], v[56:59]
	v_mfma_f32_16x16x32_bf16 v[52:55], v[198:201], v[186:189], v[52:55]
	v_mfma_f32_16x16x32_bf16 v[48:51], v[202:205], v[186:189], v[48:51]
	s_waitcnt lgkmcnt(1)
	s_waitcnt vmcnt(11)
	v_cvt_pk_bf16_f32 v19, v18, v19
	v_cvt_pk_bf16_f32 v18, v16, v17
	ds_write_b64 v161, v[18:19] offset:61184
	buffer_load_dwordx4 v[16:19], v160, s[16:19], s42 offen
	s_waitcnt vmcnt(8)
	s_mov_b32 m0, s55
	s_waitcnt lgkmcnt(0)
	s_barrier
;     ...
;             G_TILE(G_A1, G_B1, true, G_B0, G_A0, t + 2, true, t + 3, (void)0);
	ds_read_b64_tr_b16 v[170:171], v166 offset:34816
	ds_read_b64_tr_b16 v[172:173], v167 offset:34816
	ds_read_b64_tr_b16 v[176:177], v167 offset:34848
	ds_read_b128 v[178:181], v162 offset:32768
	ds_read_b64_tr_b16 v[174:175], v166 offset:34848
	ds_read_b64_tr_b16 v[182:183], v166 offset:34880
	ds_read_b64_tr_b16 v[186:187], v166 offset:34912
	ds_read_b64_tr_b16 v[184:185], v167 offset:34880
	ds_read_b64_tr_b16 v[188:189], v167 offset:34912
	ds_read_b128 v[190:193], v162 offset:34816
	ds_read_b128 v[194:197], v162 offset:36864
	buffer_load_dwordx4 v163, s[20:23], s24 offen lds
	s_mov_b32 m0, s56
	v_mfma_f32_16x16x32_bf16 v[44:47], v[244:247], v[252:255], v[44:47]
	v_mfma_f32_16x16x32_bf16 v[40:43], v[248:251], v[252:255], v[40:43]
	v_mfma_f32_16x16x32_bf16 v[36:39], v[198:201], v[252:255], v[36:39]
	v_mfma_f32_16x16x32_bf16 v[32:35], v[202:205], v[252:255], v[32:35]
	s_waitcnt lgkmcnt(7)
	v_mfma_f32_16x16x32_bf16 v[156:159], v[170:173], v[178:181], v[156:159]
	buffer_load_dwordx4 v165, s[20:23], s24 offen lds
	s_mov_b32 m0, s57
	s_add_i32 s25, s9, 0xffee0000
	buffer_load_dwordx4 v164, s[20:23], s24 offen lds
	s_mov_b32 m0, s59
	s_waitcnt lgkmcnt(6)
	v_mfma_f32_16x16x32_bf16 v[152:155], v[174:177], v[178:181], v[152:155]
	buffer_load_dwordx4 v168, s[20:23], s24 offen lds
	s_waitcnt lgkmcnt(3)
	v_mfma_f32_16x16x32_bf16 v[148:151], v[182:185], v[178:181], v[148:151]
	s_waitcnt lgkmcnt(2)
	v_mfma_f32_16x16x32_bf16 v[144:147], v[186:189], v[178:181], v[144:147]
	s_waitcnt lgkmcnt(1)
	v_mfma_f32_16x16x32_bf16 v[140:143], v[170:173], v[190:193], v[140:143]
	ds_read_b128 v[178:181], v162 offset:38912
	s_waitcnt vmcnt(11)
	v_cvt_pk_bf16_f32 v15, v14, v15
	v_cvt_pk_bf16_f32 v14, v12, v13
	v_mfma_f32_16x16x32_bf16 v[136:139], v[174:177], v[190:193], v[136:139]
	ds_write_b64 v161, v[14:15]
	v_mfma_f32_16x16x32_bf16 v[132:135], v[182:185], v[190:193], v[132:135]
	v_mfma_f32_16x16x32_bf16 v[128:131], v[186:189], v[190:193], v[128:131]
	buffer_load_dwordx4 v[12:15], v160, s[12:15], s25 offen
	s_waitcnt lgkmcnt(2)
	v_mfma_f32_16x16x32_bf16 v[124:127], v[170:173], v[194:197], v[124:127]
	ds_read_b128 v[190:193], v162 offset:40960
	v_mfma_f32_16x16x32_bf16 v[120:123], v[174:177], v[194:197], v[120:123]
	v_mfma_f32_16x16x32_bf16 v[116:119], v[182:185], v[194:197], v[116:119]
	v_mfma_f32_16x16x32_bf16 v[112:115], v[186:189], v[194:197], v[112:115]
	s_waitcnt lgkmcnt(2)
	v_mfma_f32_16x16x32_bf16 v[108:111], v[170:173], v[178:181], v[108:111]
	ds_read_b128 v[194:197], v162 offset:43008
	s_waitcnt vmcnt(11)
	v_cvt_pk_bf16_f32 v3, v2, v3
	v_cvt_pk_bf16_f32 v2, v0, v1
	v_mfma_f32_16x16x32_bf16 v[104:107], v[174:177], v[178:181], v[104:107]
	ds_write_b64 v161, v[2:3] offset:8704
	v_mfma_f32_16x16x32_bf16 v[100:103], v[182:185], v[178:181], v[100:103]
	v_mfma_f32_16x16x32_bf16 v[96:99], v[186:189], v[178:181], v[96:99]
	s_add_i32 s26, s9, 0xfff40000
	buffer_load_dwordx4 v[0:3], v160, s[12:15], s26 offen
	s_waitcnt lgkmcnt(2)
	v_mfma_f32_16x16x32_bf16 v[92:95], v[170:173], v[190:193], v[92:95]
	ds_read_b128 v[178:181], v162 offset:45056
	v_mfma_f32_16x16x32_bf16 v[88:91], v[174:177], v[190:193], v[88:91]
	v_mfma_f32_16x16x32_bf16 v[84:87], v[182:185], v[190:193], v[84:87]
	v_mfma_f32_16x16x32_bf16 v[80:83], v[186:189], v[190:193], v[80:83]
	s_waitcnt lgkmcnt(2)
	v_mfma_f32_16x16x32_bf16 v[76:79], v[170:173], v[194:197], v[76:79]
	ds_read_b128 v[190:193], v162 offset:47104
	s_waitcnt vmcnt(11)
	v_cvt_pk_bf16_f32 v31, v30, v31
	v_cvt_pk_bf16_f32 v30, v28, v29
	v_mfma_f32_16x16x32_bf16 v[72:75], v[174:177], v[194:197], v[72:75]
	ds_write_b64 v161, v[30:31] offset:17408
	v_mfma_f32_16x16x32_bf16 v[68:71], v[182:185], v[194:197], v[68:71]
	v_mfma_f32_16x16x32_bf16 v[64:67], v[186:189], v[194:197], v[64:67]
	s_add_i32 s27, s9, 0xfffa0000
	buffer_load_dwordx4 v[28:31], v160, s[12:15], s27 offen
	s_waitcnt lgkmcnt(2)
	v_mfma_f32_16x16x32_bf16 v[60:63], v[170:173], v[178:181], v[60:63]
	ds_read_b128 v[194:197], v162 offset:33792
	v_mfma_f32_16x16x32_bf16 v[56:59], v[174:177], v[178:181], v[56:59]
	v_mfma_f32_16x16x32_bf16 v[52:55], v[182:185], v[178:181], v[52:55]
	v_mfma_f32_16x16x32_bf16 v[48:51], v[186:189], v[178:181], v[48:51]
	s_waitcnt lgkmcnt(2)
	v_mfma_f32_16x16x32_bf16 v[44:47], v[170:173], v[190:193], v[44:47]
	ds_read_b128 v[170:173], v162 offset:35840
	s_waitcnt vmcnt(11)
; #define G_ENDTILE(VM) do { asm volatile("s_waitcnt vmcnt(" #VM ")" ::: "memory"); \
;         asm volatile("s_waitcnt lgkmcnt(0)" ::: "memory"); __builtin_amdgcn_s_barrier(); asm volatile("" ::: "memory"); } while (0)
;     ...
;         for (int t = 0; t < nt - 2; t += 2) {
;             G_TILE(G_A0, G_B0, true, G_B1, G_A1, t + 1, true, t + 2, (void)0);
;             G_ENDTILE(8);
;             G_TILE(G_A1, G_B1, true, G_B0, G_A0, t + 2, true, t + 3, (void)0);
;             G_ENDTILE(8);
;         }
	v_cvt_pk_bf16_f32 v27, v26, v27
	v_cvt_pk_bf16_f32 v26, v24, v25
	v_mfma_f32_16x16x32_bf16 v[40:43], v[174:177], v[190:193], v[40:43]
	ds_read_b64_tr_b16 v[244:245], v166 offset:52224
	ds_read_b64_tr_b16 v[248:249], v166 offset:52256
	ds_read_b64_tr_b16 v[198:199], v166 offset:52288
	ds_read_b64_tr_b16 v[202:203], v166 offset:52320
	ds_read_b64_tr_b16 v[246:247], v167 offset:52224
	ds_read_b64_tr_b16 v[250:251], v167 offset:52256
	ds_read_b64_tr_b16 v[200:201], v167 offset:52288
	ds_read_b64_tr_b16 v[204:205], v167 offset:52320
	ds_write_b64 v161, v[26:27] offset:26112
	v_mfma_f32_16x16x32_bf16 v[36:39], v[182:185], v[190:193], v[36:39]
	v_mfma_f32_16x16x32_bf16 v[32:35], v[186:189], v[190:193], v[32:35]
	buffer_load_dwordx4 v[24:27], v160, s[12:15], s9 offen
	s_waitcnt lgkmcnt(4)
	v_mfma_f32_16x16x32_bf16 v[156:159], v[244:247], v[194:197], v[156:159]
	ds_read_b128 v[182:185], v162 offset:37888
	s_waitcnt lgkmcnt(4)
	v_mfma_f32_16x16x32_bf16 v[152:155], v[248:251], v[194:197], v[152:155]
	s_waitcnt lgkmcnt(3)
	v_mfma_f32_16x16x32_bf16 v[148:151], v[198:201], v[194:197], v[148:151]
	s_waitcnt lgkmcnt(2)
	v_mfma_f32_16x16x32_bf16 v[144:147], v[202:205], v[194:197], v[144:147]
	v_mfma_f32_16x16x32_bf16 v[140:143], v[244:247], v[170:173], v[140:143]
	ds_read_b128 v[186:189], v162 offset:39936
	s_waitcnt vmcnt(11)
	v_cvt_pk_bf16_f32 v23, v22, v23
	v_cvt_pk_bf16_f32 v22, v20, v21
	v_mfma_f32_16x16x32_bf16 v[136:139], v[248:251], v[170:173], v[136:139]
	ds_write_b64 v161, v[22:23] offset:256
	v_mfma_f32_16x16x32_bf16 v[132:135], v[198:201], v[170:173], v[132:135]
	v_mfma_f32_16x16x32_bf16 v[128:131], v[202:205], v[170:173], v[128:131]
	buffer_load_dwordx4 v[20:23], v160, s[16:19], s25 offen
	s_waitcnt lgkmcnt(2)
	v_mfma_f32_16x16x32_bf16 v[124:127], v[244:247], v[182:185], v[124:127]
	ds_read_b128 v[170:173], v162 offset:41984
	v_mfma_f32_16x16x32_bf16 v[120:123], v[248:251], v[182:185], v[120:123]
	v_mfma_f32_16x16x32_bf16 v[116:119], v[198:201], v[182:185], v[116:119]
	v_mfma_f32_16x16x32_bf16 v[112:115], v[202:205], v[182:185], v[112:115]
	s_waitcnt lgkmcnt(2)
	v_mfma_f32_16x16x32_bf16 v[108:111], v[244:247], v[186:189], v[108:111]
	ds_read_b128 v[182:185], v162 offset:44032
	s_waitcnt vmcnt(11)
	v_cvt_pk_bf16_f32 v7, v6, v7
	v_cvt_pk_bf16_f32 v6, v4, v5
	v_mfma_f32_16x16x32_bf16 v[104:107], v[248:251], v[186:189], v[104:107]
	ds_write_b64 v161, v[6:7] offset:8960
	v_mfma_f32_16x16x32_bf16 v[100:103], v[198:201], v[186:189], v[100:103]
	v_mfma_f32_16x16x32_bf16 v[96:99], v[202:205], v[186:189], v[96:99]
	buffer_load_dwordx4 v[4:7], v160, s[16:19], s26 offen
	s_waitcnt lgkmcnt(2)
	v_mfma_f32_16x16x32_bf16 v[92:95], v[244:247], v[170:173], v[92:95]
	ds_read_b128 v[186:189], v162 offset:46080
	v_mfma_f32_16x16x32_bf16 v[88:91], v[248:251], v[170:173], v[88:91]
	v_mfma_f32_16x16x32_bf16 v[84:87], v[198:201], v[170:173], v[84:87]
	v_mfma_f32_16x16x32_bf16 v[80:83], v[202:205], v[170:173], v[80:83]
	s_waitcnt lgkmcnt(2)
	v_mfma_f32_16x16x32_bf16 v[76:79], v[244:247], v[182:185], v[76:79]
	ds_read_b128 v[252:255], v162 offset:48128
	s_waitcnt vmcnt(11)
	v_cvt_pk_bf16_f32 v11, v10, v11
	v_cvt_pk_bf16_f32 v10, v8, v9
	v_mfma_f32_16x16x32_bf16 v[72:75], v[248:251], v[182:185], v[72:75]
	ds_write_b64 v161, v[10:11] offset:17664
	v_mfma_f32_16x16x32_bf16 v[68:71], v[198:201], v[182:185], v[68:71]
	v_mfma_f32_16x16x32_bf16 v[64:67], v[202:205], v[182:185], v[64:67]
	buffer_load_dwordx4 v[8:11], v160, s[16:19], s27 offen
	s_waitcnt lgkmcnt(2)
	v_mfma_f32_16x16x32_bf16 v[60:63], v[244:247], v[186:189], v[60:63]
	v_mfma_f32_16x16x32_bf16 v[56:59], v[248:251], v[186:189], v[56:59]
	v_mfma_f32_16x16x32_bf16 v[52:55], v[198:201], v[186:189], v[52:55]
	v_mfma_f32_16x16x32_bf16 v[48:51], v[202:205], v[186:189], v[48:51]
	s_waitcnt lgkmcnt(1)
	s_waitcnt vmcnt(11)
	v_cvt_pk_bf16_f32 v19, v18, v19
	v_cvt_pk_bf16_f32 v18, v16, v17
	ds_write_b64 v161, v[18:19] offset:26368
	buffer_load_dwordx4 v[16:19], v160, s[16:19], s9 offen
	s_waitcnt vmcnt(8)
	s_waitcnt lgkmcnt(0)
	s_barrier
	s_add_i32 s8, s8, 2
	s_add_i32 s9, s9, 0x300000
	s_addk_i32 s24, 0x100
	s_cmp_ge_i32 s8, s64
	s_cbranch_scc0 .LBB0_71
	v_mfma_f32_16x16x32_bf16 v[44:47], v[244:247], v[252:255], v[44:47]
	v_mfma_f32_16x16x32_bf16 v[40:43], v[248:251], v[252:255], v[40:43]
	v_mfma_f32_16x16x32_bf16 v[36:39], v[198:201], v[252:255], v[36:39]
	v_mfma_f32_16x16x32_bf16 v[32:35], v[202:205], v[252:255], v[32:35]
	s_branch .LBB0_73

;     ...
;     for (int ui = 0;; ++ui) {
; #pragma unroll
;         for (int m = 0; m < MF; ++m)
; #pragma unroll
;             for (int n = 0; n < 4; ++n) acc[m][n] = (f32x4){0.f, 0.f, 0.f, 0.f};
;         for (int t = 0; t < nt - 2; t += 2) {
;             G_TILE(G_A0, G_B0, true, G_B1, G_A1, t + 1, true, t + 2, (void)0);
.LBB0_376:
	s_andn2_b64 vcc, exec, s[30:31]
	v_mov_b32_e32 v159, 0
	s_cbranch_vccnz .LBB0_379
	v_mov_b32_e32 v32, 0
	s_mov_b32 s8, 0
	s_mov_b32 s9, 0x1e0000
	s_movk_i32 s24, 0x100
	v_mov_b32_e32 v33, v32
	v_mov_b32_e32 v34, v32
	v_mov_b32_e32 v35, v32
	v_mov_b32_e32 v36, v32
	v_mov_b32_e32 v37, v32
	v_mov_b32_e32 v38, v32
	v_mov_b32_e32 v39, v32
	v_mov_b32_e32 v40, v32
	v_mov_b32_e32 v41, v32
	v_mov_b32_e32 v42, v32
	v_mov_b32_e32 v43, v32
	v_mov_b32_e32 v44, v32
	v_mov_b32_e32 v45, v32
	v_mov_b32_e32 v46, v32
	v_mov_b32_e32 v47, v32
	v_mov_b32_e32 v48, v32
	v_mov_b32_e32 v49, v32
	v_mov_b32_e32 v50, v32
	v_mov_b32_e32 v51, v32
	v_mov_b32_e32 v52, v32
	v_mov_b32_e32 v53, v32
	v_mov_b32_e32 v54, v32
	v_mov_b32_e32 v55, v32
	v_mov_b32_e32 v56, v32
	v_mov_b32_e32 v57, v32
	v_mov_b32_e32 v58, v32
	v_mov_b32_e32 v59, v32
	v_mov_b32_e32 v60, v32
	v_mov_b32_e32 v61, v32
	v_mov_b32_e32 v62, v32
	v_mov_b32_e32 v63, v32
	v_mov_b32_e32 v64, v32
	v_mov_b32_e32 v65, v32
	v_mov_b32_e32 v66, v32
	v_mov_b32_e32 v67, v32
	v_mov_b32_e32 v68, v32
	v_mov_b32_e32 v69, v32
	v_mov_b32_e32 v70, v32
	v_mov_b32_e32 v71, v32
	v_mov_b32_e32 v72, v32
	v_mov_b32_e32 v73, v32
	v_mov_b32_e32 v74, v32
	v_mov_b32_e32 v75, v32
	v_mov_b32_e32 v76, v32
	v_mov_b32_e32 v77, v32
	v_mov_b32_e32 v78, v32
	v_mov_b32_e32 v79, v32
	v_mov_b32_e32 v80, v32
	v_mov_b32_e32 v81, v32
	v_mov_b32_e32 v82, v32
	v_mov_b32_e32 v83, v32
	v_mov_b32_e32 v84, v32
	v_mov_b32_e32 v85, v32
	v_mov_b32_e32 v86, v32
	v_mov_b32_e32 v87, v32
	v_mov_b32_e32 v88, v32
	v_mov_b32_e32 v89, v32
	v_mov_b32_e32 v90, v32
	v_mov_b32_e32 v91, v32
	v_mov_b32_e32 v92, v32
	v_mov_b32_e32 v93, v32
	v_mov_b32_e32 v94, v32
	v_mov_b32_e32 v95, v32
	v_mov_b32_e32 v96, v32
	v_mov_b32_e32 v97, v32
	v_mov_b32_e32 v98, v32
	v_mov_b32_e32 v99, v32
	v_mov_b32_e32 v100, v32
	v_mov_b32_e32 v101, v32
	v_mov_b32_e32 v102, v32
	v_mov_b32_e32 v103, v32
	v_mov_b32_e32 v104, v32
	v_mov_b32_e32 v105, v32
	v_mov_b32_e32 v106, v32
	v_mov_b32_e32 v107, v32
	v_mov_b32_e32 v108, v32
	v_mov_b32_e32 v109, v32
	v_mov_b32_e32 v110, v32
	v_mov_b32_e32 v111, v32
	v_mov_b32_e32 v112, v32
	v_mov_b32_e32 v113, v32
	v_mov_b32_e32 v114, v32
	v_mov_b32_e32 v115, v32
	v_mov_b32_e32 v116, v32
	v_mov_b32_e32 v117, v32
	v_mov_b32_e32 v118, v32
	v_mov_b32_e32 v119, v32
	v_mov_b32_e32 v120, v32
	v_mov_b32_e32 v121, v32
	v_mov_b32_e32 v122, v32
	v_mov_b32_e32 v123, v32
	v_mov_b32_e32 v124, v32
	v_mov_b32_e32 v125, v32
	v_mov_b32_e32 v126, v32
	v_mov_b32_e32 v127, v32
	v_mov_b32_e32 v128, v32
	v_mov_b32_e32 v129, v32
	v_mov_b32_e32 v130, v32
	v_mov_b32_e32 v131, v32
	v_mov_b32_e32 v132, v32
	v_mov_b32_e32 v133, v32
	v_mov_b32_e32 v134, v32
	v_mov_b32_e32 v135, v32
	v_mov_b32_e32 v136, v32
	v_mov_b32_e32 v137, v32
	v_mov_b32_e32 v138, v32
	v_mov_b32_e32 v139, v32
	v_mov_b32_e32 v140, v32
	v_mov_b32_e32 v141, v32
	v_mov_b32_e32 v142, v32
	v_mov_b32_e32 v143, v32
	v_mov_b32_e32 v144, v32
	v_mov_b32_e32 v145, v32
	v_mov_b32_e32 v146, v32
	v_mov_b32_e32 v147, v32
	v_mov_b32_e32 v148, v32
	v_mov_b32_e32 v149, v32
	v_mov_b32_e32 v150, v32
	v_mov_b32_e32 v151, v32
	v_mov_b32_e32 v152, v32
	v_mov_b32_e32 v153, v32
	v_mov_b32_e32 v154, v32
	v_mov_b32_e32 v155, v32
	v_mov_b32_e32 v156, v32
	v_mov_b32_e32 v157, v32
	v_mov_b32_e32 v158, v32
	v_mov_b32_e32 v159, v32
	v_mov_b32_e32 v202, 0
	v_mov_b32_e32 v203, 0
	v_mov_b32_e32 v204, 0
	v_mov_b32_e32 v205, 0
	v_mov_b32_e32 v206, 0
	v_mov_b32_e32 v207, 0
	v_mov_b32_e32 v208, 0
	v_mov_b32_e32 v209, 0
	v_mov_b32_e32 v244, 0
	v_mov_b32_e32 v245, 0
	v_mov_b32_e32 v246, 0
	v_mov_b32_e32 v247, 0
	v_mov_b32_e32 v248, 0
	v_mov_b32_e32 v249, 0
	v_mov_b32_e32 v250, 0
	v_mov_b32_e32 v251, 0
	v_mov_b32_e32 v252, 0
	v_mov_b32_e32 v253, 0
	v_mov_b32_e32 v254, 0
	v_mov_b32_e32 v255, 0
.LBB0_378:
	s_mov_b32 m0, s72
	s_add_i32 s25, s24, 0xffffff80
	ds_read_b64_tr_b16 v[170:171], v165
	ds_read_b64_tr_b16 v[172:173], v166
	ds_read_b64_tr_b16 v[176:177], v166 offset:32
	ds_read_b128 v[178:181], v162
	ds_read_b64_tr_b16 v[174:175], v165 offset:32
	ds_read_b64_tr_b16 v[182:183], v165 offset:64
	ds_read_b64_tr_b16 v[186:187], v165 offset:96
	ds_read_b64_tr_b16 v[184:185], v166 offset:64
	ds_read_b64_tr_b16 v[188:189], v166 offset:96
	ds_read_b128 v[190:193], v162 offset:2048
	ds_read_b128 v[198:201], v162 offset:4096
	buffer_load_dwordx4 v163, s[20:23], s25 offen lds
	s_mov_b32 m0, s71
	v_mfma_f32_16x16x32_bf16 v[44:47], v[244:247], v[252:255], v[44:47]
	v_mfma_f32_16x16x32_bf16 v[40:43], v[248:251], v[252:255], v[40:43]
	v_mfma_f32_16x16x32_bf16 v[36:39], v[202:205], v[252:255], v[36:39]
	v_mfma_f32_16x16x32_bf16 v[32:35], v[206:209], v[252:255], v[32:35]
	s_waitcnt lgkmcnt(7)
	v_mfma_f32_16x16x32_bf16 v[156:159], v[170:173], v[178:181], v[156:159]
	buffer_load_dwordx4 v164, s[20:23], s25 offen lds
	s_mov_b32 m0, s70
	s_nop 0
	buffer_load_dwordx4 v167, s[20:23], s25 offen lds
	s_mov_b32 m0, s68
	s_waitcnt lgkmcnt(6)
	v_mfma_f32_16x16x32_bf16 v[152:155], v[174:177], v[178:181], v[152:155]
	buffer_load_dwordx4 v168, s[20:23], s25 offen lds
	s_add_i32 s25, s9, 0xfff20000
	s_waitcnt lgkmcnt(3)
	v_mfma_f32_16x16x32_bf16 v[148:151], v[182:185], v[178:181], v[148:151]
	s_waitcnt lgkmcnt(2)
	v_mfma_f32_16x16x32_bf16 v[144:147], v[186:189], v[178:181], v[144:147]
	s_waitcnt lgkmcnt(1)
	v_mfma_f32_16x16x32_bf16 v[140:143], v[170:173], v[190:193], v[140:143]
	ds_read_b128 v[178:181], v162 offset:6144
	s_waitcnt vmcnt(11)
	v_cvt_pk_bf16_f32 v15, v14, v15
	v_cvt_pk_bf16_f32 v14, v12, v13
	v_mfma_f32_16x16x32_bf16 v[136:139], v[174:177], v[190:193], v[136:139]
	ds_write_b64 v161, v[14:15] offset:34816
	v_mfma_f32_16x16x32_bf16 v[132:135], v[182:185], v[190:193], v[132:135]
	v_mfma_f32_16x16x32_bf16 v[128:131], v[186:189], v[190:193], v[128:131]
	buffer_load_dwordx4 v[12:15], v160, s[12:15], s25 offen
	s_waitcnt lgkmcnt(2)
	v_mfma_f32_16x16x32_bf16 v[124:127], v[170:173], v[198:201], v[124:127]
	ds_read_b128 v[190:193], v162 offset:8192
	v_mfma_f32_16x16x32_bf16 v[120:123], v[174:177], v[198:201], v[120:123]
	v_mfma_f32_16x16x32_bf16 v[116:119], v[182:185], v[198:201], v[116:119]
	v_mfma_f32_16x16x32_bf16 v[112:115], v[186:189], v[198:201], v[112:115]
	s_waitcnt lgkmcnt(2)
	v_mfma_f32_16x16x32_bf16 v[108:111], v[170:173], v[178:181], v[108:111]
	ds_read_b128 v[198:201], v162 offset:10240
	s_waitcnt vmcnt(10)
	v_cvt_pk_bf16_f32 v31, v30, v31
	v_cvt_pk_bf16_f32 v30, v28, v29
	v_mfma_f32_16x16x32_bf16 v[104:107], v[174:177], v[178:181], v[104:107]
	ds_write_b64 v161, v[30:31] offset:43520
	v_mfma_f32_16x16x32_bf16 v[100:103], v[182:185], v[178:181], v[100:103]
	v_mfma_f32_16x16x32_bf16 v[96:99], v[186:189], v[178:181], v[96:99]
	s_add_i32 s26, s9, 0xfff40000
	buffer_load_dwordx4 v[28:31], v160, s[12:15], s26 offen
	s_waitcnt lgkmcnt(2)
	v_mfma_f32_16x16x32_bf16 v[92:95], v[170:173], v[190:193], v[92:95]
	ds_read_b128 v[178:181], v162 offset:12288
	v_mfma_f32_16x16x32_bf16 v[88:91], v[174:177], v[190:193], v[88:91]
	v_mfma_f32_16x16x32_bf16 v[84:87], v[182:185], v[190:193], v[84:87]
	v_mfma_f32_16x16x32_bf16 v[80:83], v[186:189], v[190:193], v[80:83]
	s_waitcnt lgkmcnt(2)
	v_mfma_f32_16x16x32_bf16 v[76:79], v[170:173], v[198:201], v[76:79]
	ds_read_b128 v[190:193], v162 offset:14336
	v_cvt_pk_bf16_f32 v7, v6, v7
	v_cvt_pk_bf16_f32 v6, v4, v5
	v_mfma_f32_16x16x32_bf16 v[72:75], v[174:177], v[198:201], v[72:75]
	ds_write_b64 v161, v[6:7] offset:52224
	v_mfma_f32_16x16x32_bf16 v[68:71], v[182:185], v[198:201], v[68:71]
	v_mfma_f32_16x16x32_bf16 v[64:67], v[186:189], v[198:201], v[64:67]
	s_add_i32 s27, s9, 0xfff60000
	buffer_load_dwordx4 v[4:7], v160, s[12:15], s27 offen
	s_waitcnt lgkmcnt(2)
	v_mfma_f32_16x16x32_bf16 v[60:63], v[170:173], v[178:181], v[60:63]
	ds_read_b128 v[198:201], v162 offset:1024
	v_mfma_f32_16x16x32_bf16 v[56:59], v[174:177], v[178:181], v[56:59]
	v_mfma_f32_16x16x32_bf16 v[52:55], v[182:185], v[178:181], v[52:55]
	v_mfma_f32_16x16x32_bf16 v[48:51], v[186:189], v[178:181], v[48:51]
	s_waitcnt lgkmcnt(2)
	v_mfma_f32_16x16x32_bf16 v[44:47], v[170:173], v[190:193], v[44:47]
	ds_read_b128 v[170:173], v162 offset:3072
	s_waitcnt vmcnt(11)
	v_cvt_pk_bf16_f32 v27, v26, v27
	v_cvt_pk_bf16_f32 v26, v24, v25
	v_mfma_f32_16x16x32_bf16 v[40:43], v[174:177], v[190:193], v[40:43]
	ds_read_b64_tr_b16 v[244:245], v165 offset:17408
	ds_read_b64_tr_b16 v[248:249], v165 offset:17440
	ds_read_b64_tr_b16 v[202:203], v165 offset:17472
	ds_read_b64_tr_b16 v[206:207], v165 offset:17504
	ds_read_b64_tr_b16 v[246:247], v166 offset:17408
	ds_read_b64_tr_b16 v[250:251], v166 offset:17440
	ds_read_b64_tr_b16 v[204:205], v166 offset:17472
	ds_read_b64_tr_b16 v[208:209], v166 offset:17504
	ds_write_b64 v161, v[26:27] offset:60928
	v_mfma_f32_16x16x32_bf16 v[36:39], v[182:185], v[190:193], v[36:39]
	v_mfma_f32_16x16x32_bf16 v[32:35], v[186:189], v[190:193], v[32:35]
	s_add_i32 s45, s9, 0xfff80000
	buffer_load_dwordx4 v[24:27], v160, s[12:15], s45 offen
	s_waitcnt lgkmcnt(4)
	v_mfma_f32_16x16x32_bf16 v[156:159], v[244:247], v[198:201], v[156:159]
	ds_read_b128 v[182:185], v162 offset:5120
	s_waitcnt lgkmcnt(4)
	v_mfma_f32_16x16x32_bf16 v[152:155], v[248:251], v[198:201], v[152:155]
	s_waitcnt lgkmcnt(3)
	v_mfma_f32_16x16x32_bf16 v[148:151], v[202:205], v[198:201], v[148:151]
	s_waitcnt lgkmcnt(2)
	v_mfma_f32_16x16x32_bf16 v[144:147], v[206:209], v[198:201], v[144:147]
	v_mfma_f32_16x16x32_bf16 v[140:143], v[244:247], v[170:173], v[140:143]
	ds_read_b128 v[186:189], v162 offset:7168
	s_waitcnt vmcnt(11)
	v_cvt_pk_bf16_f32 v23, v22, v23
	v_cvt_pk_bf16_f32 v22, v20, v21
	v_mfma_f32_16x16x32_bf16 v[136:139], v[248:251], v[170:173], v[136:139]
	ds_write_b64 v161, v[22:23] offset:35072
	v_mfma_f32_16x16x32_bf16 v[132:135], v[202:205], v[170:173], v[132:135]
	v_mfma_f32_16x16x32_bf16 v[128:131], v[206:209], v[170:173], v[128:131]
	buffer_load_dwordx4 v[20:23], v160, s[16:19], s25 offen
	s_waitcnt lgkmcnt(2)
	v_mfma_f32_16x16x32_bf16 v[124:127], v[244:247], v[182:185], v[124:127]
	ds_read_b128 v[170:173], v162 offset:9216
	v_mfma_f32_16x16x32_bf16 v[120:123], v[248:251], v[182:185], v[120:123]
	v_mfma_f32_16x16x32_bf16 v[116:119], v[202:205], v[182:185], v[116:119]
	v_mfma_f32_16x16x32_bf16 v[112:115], v[206:209], v[182:185], v[112:115]
	s_waitcnt lgkmcnt(2)
	v_mfma_f32_16x16x32_bf16 v[108:111], v[244:247], v[186:189], v[108:111]
	ds_read_b128 v[182:185], v162 offset:11264
	s_waitcnt vmcnt(10)
	v_cvt_pk_bf16_f32 v11, v10, v11
	v_cvt_pk_bf16_f32 v10, v8, v9
	v_mfma_f32_16x16x32_bf16 v[104:107], v[248:251], v[186:189], v[104:107]
	ds_write_b64 v161, v[10:11] offset:43776
	v_mfma_f32_16x16x32_bf16 v[100:103], v[202:205], v[186:189], v[100:103]
	v_mfma_f32_16x16x32_bf16 v[96:99], v[206:209], v[186:189], v[96:99]
	buffer_load_dwordx4 v[8:11], v160, s[16:19], s26 offen
	s_waitcnt lgkmcnt(2)
	v_mfma_f32_16x16x32_bf16 v[92:95], v[244:247], v[170:173], v[92:95]
	ds_read_b128 v[186:189], v162 offset:13312
	v_mfma_f32_16x16x32_bf16 v[88:91], v[248:251], v[170:173], v[88:91]
	v_mfma_f32_16x16x32_bf16 v[84:87], v[202:205], v[170:173], v[84:87]
	v_mfma_f32_16x16x32_bf16 v[80:83], v[206:209], v[170:173], v[80:83]
	s_waitcnt lgkmcnt(2)
	v_mfma_f32_16x16x32_bf16 v[76:79], v[244:247], v[182:185], v[76:79]
	ds_read_b128 v[252:255], v162 offset:15360
	v_cvt_pk_bf16_f32 v3, v2, v3
	v_cvt_pk_bf16_f32 v2, v0, v1
	v_mfma_f32_16x16x32_bf16 v[72:75], v[248:251], v[182:185], v[72:75]
	ds_write_b64 v161, v[2:3] offset:52480
	v_mfma_f32_16x16x32_bf16 v[68:71], v[202:205], v[182:185], v[68:71]
	v_mfma_f32_16x16x32_bf16 v[64:67], v[206:209], v[182:185], v[64:67]
	buffer_load_dwordx4 v[0:3], v160, s[16:19], s27 offen
	s_waitcnt lgkmcnt(2)
	v_mfma_f32_16x16x32_bf16 v[60:63], v[244:247], v[186:189], v[60:63]
	v_mfma_f32_16x16x32_bf16 v[56:59], v[248:251], v[186:189], v[56:59]
	v_mfma_f32_16x16x32_bf16 v[52:55], v[202:205], v[186:189], v[52:55]
	v_mfma_f32_16x16x32_bf16 v[48:51], v[206:209], v[186:189], v[48:51]
	s_waitcnt lgkmcnt(1)
	s_waitcnt vmcnt(11)
	v_cvt_pk_bf16_f32 v19, v18, v19
	v_cvt_pk_bf16_f32 v18, v16, v17
	ds_write_b64 v161, v[18:19] offset:61184
	buffer_load_dwordx4 v[16:19], v160, s[16:19], s45 offen
	s_waitcnt vmcnt(8)
	s_mov_b32 m0, s59
	s_waitcnt lgkmcnt(0)
	s_barrier
;     ...
;             G_TILE(G_A1, G_B1, true, G_B0, G_A0, t + 2, true, t + 3, (void)0);
	ds_read_b64_tr_b16 v[170:171], v165 offset:34816
	ds_read_b64_tr_b16 v[172:173], v166 offset:34816
	ds_read_b64_tr_b16 v[176:177], v166 offset:34848
	ds_read_b128 v[178:181], v162 offset:32768
	ds_read_b64_tr_b16 v[174:175], v165 offset:34848
	ds_read_b64_tr_b16 v[182:183], v165 offset:34880
	ds_read_b64_tr_b16 v[186:187], v165 offset:34912
	ds_read_b64_tr_b16 v[184:185], v166 offset:34880
	ds_read_b64_tr_b16 v[188:189], v166 offset:34912
	ds_read_b128 v[190:193], v162 offset:34816
	ds_read_b128 v[198:201], v162 offset:36864
	buffer_load_dwordx4 v163, s[20:23], s24 offen lds
	s_mov_b32 m0, s60
	v_mfma_f32_16x16x32_bf16 v[44:47], v[244:247], v[252:255], v[44:47]
	v_mfma_f32_16x16x32_bf16 v[40:43], v[248:251], v[252:255], v[40:43]
	v_mfma_f32_16x16x32_bf16 v[36:39], v[202:205], v[252:255], v[36:39]
	v_mfma_f32_16x16x32_bf16 v[32:35], v[206:209], v[252:255], v[32:35]
	s_waitcnt lgkmcnt(7)
	v_mfma_f32_16x16x32_bf16 v[156:159], v[170:173], v[178:181], v[156:159]
	buffer_load_dwordx4 v164, s[20:23], s24 offen lds
	s_mov_b32 m0, s61
	s_add_i32 s25, s9, 0xfffa0000
	buffer_load_dwordx4 v167, s[20:23], s24 offen lds
	s_mov_b32 m0, s62
	s_waitcnt lgkmcnt(6)
	v_mfma_f32_16x16x32_bf16 v[152:155], v[174:177], v[178:181], v[152:155]
	buffer_load_dwordx4 v168, s[20:23], s24 offen lds
	s_waitcnt lgkmcnt(3)
	v_mfma_f32_16x16x32_bf16 v[148:151], v[182:185], v[178:181], v[148:151]
	s_waitcnt lgkmcnt(2)
	v_mfma_f32_16x16x32_bf16 v[144:147], v[186:189], v[178:181], v[144:147]
	s_waitcnt lgkmcnt(1)
	v_mfma_f32_16x16x32_bf16 v[140:143], v[170:173], v[190:193], v[140:143]
	ds_read_b128 v[178:181], v162 offset:38912
	s_waitcnt vmcnt(11)
	v_cvt_pk_bf16_f32 v15, v14, v15
	v_cvt_pk_bf16_f32 v14, v12, v13
	v_mfma_f32_16x16x32_bf16 v[136:139], v[174:177], v[190:193], v[136:139]
	ds_write_b64 v161, v[14:15]
	v_mfma_f32_16x16x32_bf16 v[132:135], v[182:185], v[190:193], v[132:135]
	v_mfma_f32_16x16x32_bf16 v[128:131], v[186:189], v[190:193], v[128:131]
	buffer_load_dwordx4 v[12:15], v160, s[12:15], s25 offen
	s_waitcnt lgkmcnt(2)
	v_mfma_f32_16x16x32_bf16 v[124:127], v[170:173], v[198:201], v[124:127]
	ds_read_b128 v[190:193], v162 offset:40960
	v_mfma_f32_16x16x32_bf16 v[120:123], v[174:177], v[198:201], v[120:123]
	v_mfma_f32_16x16x32_bf16 v[116:119], v[182:185], v[198:201], v[116:119]
	v_mfma_f32_16x16x32_bf16 v[112:115], v[186:189], v[198:201], v[112:115]
	s_waitcnt lgkmcnt(2)
	v_mfma_f32_16x16x32_bf16 v[108:111], v[170:173], v[178:181], v[108:111]
	ds_read_b128 v[198:201], v162 offset:43008
	s_waitcnt vmcnt(11)
	v_cvt_pk_bf16_f32 v31, v30, v31
	v_cvt_pk_bf16_f32 v30, v28, v29
	v_mfma_f32_16x16x32_bf16 v[104:107], v[174:177], v[178:181], v[104:107]
	ds_write_b64 v161, v[30:31] offset:8704
	v_mfma_f32_16x16x32_bf16 v[100:103], v[182:185], v[178:181], v[100:103]
	v_mfma_f32_16x16x32_bf16 v[96:99], v[186:189], v[178:181], v[96:99]
	s_add_i32 s26, s9, 0xfffc0000
	buffer_load_dwordx4 v[28:31], v160, s[12:15], s26 offen
	s_waitcnt lgkmcnt(2)
	v_mfma_f32_16x16x32_bf16 v[92:95], v[170:173], v[190:193], v[92:95]
	ds_read_b128 v[178:181], v162 offset:45056
	v_mfma_f32_16x16x32_bf16 v[88:91], v[174:177], v[190:193], v[88:91]
	v_mfma_f32_16x16x32_bf16 v[84:87], v[182:185], v[190:193], v[84:87]
	v_mfma_f32_16x16x32_bf16 v[80:83], v[186:189], v[190:193], v[80:83]
	s_waitcnt lgkmcnt(2)
	v_mfma_f32_16x16x32_bf16 v[76:79], v[170:173], v[198:201], v[76:79]
	ds_read_b128 v[190:193], v162 offset:47104
	s_waitcnt vmcnt(11)
	v_cvt_pk_bf16_f32 v7, v6, v7
	v_cvt_pk_bf16_f32 v6, v4, v5
	v_mfma_f32_16x16x32_bf16 v[72:75], v[174:177], v[198:201], v[72:75]
	ds_write_b64 v161, v[6:7] offset:17408
	v_mfma_f32_16x16x32_bf16 v[68:71], v[182:185], v[198:201], v[68:71]
	v_mfma_f32_16x16x32_bf16 v[64:67], v[186:189], v[198:201], v[64:67]
	s_add_i32 s27, s9, 0xfffe0000
	buffer_load_dwordx4 v[4:7], v160, s[12:15], s27 offen
	s_waitcnt lgkmcnt(2)
	v_mfma_f32_16x16x32_bf16 v[60:63], v[170:173], v[178:181], v[60:63]
	ds_read_b128 v[198:201], v162 offset:33792
	v_mfma_f32_16x16x32_bf16 v[56:59], v[174:177], v[178:181], v[56:59]
	v_mfma_f32_16x16x32_bf16 v[52:55], v[182:185], v[178:181], v[52:55]
	v_mfma_f32_16x16x32_bf16 v[48:51], v[186:189], v[178:181], v[48:51]
	s_waitcnt lgkmcnt(2)
	v_mfma_f32_16x16x32_bf16 v[44:47], v[170:173], v[190:193], v[44:47]
	ds_read_b128 v[170:173], v162 offset:35840
	s_waitcnt vmcnt(11)
; #define G_ENDTILE(VM) do { asm volatile("s_waitcnt vmcnt(" #VM ")" ::: "memory"); \
;         asm volatile("s_waitcnt lgkmcnt(0)" ::: "memory"); __builtin_amdgcn_s_barrier(); asm volatile("" ::: "memory"); } while (0)
;     ...
;         for (int t = 0; t < nt - 2; t += 2) {
;             G_TILE(G_A0, G_B0, true, G_B1, G_A1, t + 1, true, t + 2, (void)0);
;             G_ENDTILE(8);
;             G_TILE(G_A1, G_B1, true, G_B0, G_A0, t + 2, true, t + 3, (void)0);
;             G_ENDTILE(8);
;         }
	v_cvt_pk_bf16_f32 v27, v26, v27
	v_cvt_pk_bf16_f32 v26, v24, v25
	v_mfma_f32_16x16x32_bf16 v[40:43], v[174:177], v[190:193], v[40:43]
	ds_read_b64_tr_b16 v[244:245], v165 offset:52224
	ds_read_b64_tr_b16 v[248:249], v165 offset:52256
	ds_read_b64_tr_b16 v[202:203], v165 offset:52288
	ds_read_b64_tr_b16 v[206:207], v165 offset:52320
	ds_read_b64_tr_b16 v[246:247], v166 offset:52224
	ds_read_b64_tr_b16 v[250:251], v166 offset:52256
	ds_read_b64_tr_b16 v[204:205], v166 offset:52288
	ds_read_b64_tr_b16 v[208:209], v166 offset:52320
	ds_write_b64 v161, v[26:27] offset:26112
	v_mfma_f32_16x16x32_bf16 v[36:39], v[182:185], v[190:193], v[36:39]
	v_mfma_f32_16x16x32_bf16 v[32:35], v[186:189], v[190:193], v[32:35]
	buffer_load_dwordx4 v[24:27], v160, s[12:15], s9 offen
	s_waitcnt lgkmcnt(4)
	v_mfma_f32_16x16x32_bf16 v[156:159], v[244:247], v[198:201], v[156:159]
	ds_read_b128 v[182:185], v162 offset:37888
	s_waitcnt lgkmcnt(4)
	v_mfma_f32_16x16x32_bf16 v[152:155], v[248:251], v[198:201], v[152:155]
	s_waitcnt lgkmcnt(3)
	v_mfma_f32_16x16x32_bf16 v[148:151], v[202:205], v[198:201], v[148:151]
	s_waitcnt lgkmcnt(2)
	v_mfma_f32_16x16x32_bf16 v[144:147], v[206:209], v[198:201], v[144:147]
	v_mfma_f32_16x16x32_bf16 v[140:143], v[244:247], v[170:173], v[140:143]
	ds_read_b128 v[186:189], v162 offset:39936
	s_waitcnt vmcnt(11)
	v_cvt_pk_bf16_f32 v23, v22, v23
	v_cvt_pk_bf16_f32 v22, v20, v21
	v_mfma_f32_16x16x32_bf16 v[136:139], v[248:251], v[170:173], v[136:139]
	ds_write_b64 v161, v[22:23] offset:256
	v_mfma_f32_16x16x32_bf16 v[132:135], v[202:205], v[170:173], v[132:135]
	v_mfma_f32_16x16x32_bf16 v[128:131], v[206:209], v[170:173], v[128:131]
	buffer_load_dwordx4 v[20:23], v160, s[16:19], s25 offen
	s_waitcnt lgkmcnt(2)
	v_mfma_f32_16x16x32_bf16 v[124:127], v[244:247], v[182:185], v[124:127]
	ds_read_b128 v[170:173], v162 offset:41984
	v_mfma_f32_16x16x32_bf16 v[120:123], v[248:251], v[182:185], v[120:123]
	v_mfma_f32_16x16x32_bf16 v[116:119], v[202:205], v[182:185], v[116:119]
	v_mfma_f32_16x16x32_bf16 v[112:115], v[206:209], v[182:185], v[112:115]
	s_waitcnt lgkmcnt(2)
	v_mfma_f32_16x16x32_bf16 v[108:111], v[244:247], v[186:189], v[108:111]
	ds_read_b128 v[182:185], v162 offset:44032
	s_waitcnt vmcnt(11)
	v_cvt_pk_bf16_f32 v11, v10, v11
	v_cvt_pk_bf16_f32 v10, v8, v9
	v_mfma_f32_16x16x32_bf16 v[104:107], v[248:251], v[186:189], v[104:107]
	ds_write_b64 v161, v[10:11] offset:8960
	v_mfma_f32_16x16x32_bf16 v[100:103], v[202:205], v[186:189], v[100:103]
	v_mfma_f32_16x16x32_bf16 v[96:99], v[206:209], v[186:189], v[96:99]
	buffer_load_dwordx4 v[8:11], v160, s[16:19], s26 offen
	s_waitcnt lgkmcnt(2)
	v_mfma_f32_16x16x32_bf16 v[92:95], v[244:247], v[170:173], v[92:95]
	ds_read_b128 v[186:189], v162 offset:46080
	v_mfma_f32_16x16x32_bf16 v[88:91], v[248:251], v[170:173], v[88:91]
	v_mfma_f32_16x16x32_bf16 v[84:87], v[202:205], v[170:173], v[84:87]
	v_mfma_f32_16x16x32_bf16 v[80:83], v[206:209], v[170:173], v[80:83]
	s_waitcnt lgkmcnt(2)
	v_mfma_f32_16x16x32_bf16 v[76:79], v[244:247], v[182:185], v[76:79]
	ds_read_b128 v[252:255], v162 offset:48128
	s_waitcnt vmcnt(11)
	v_cvt_pk_bf16_f32 v3, v2, v3
	v_cvt_pk_bf16_f32 v2, v0, v1
	v_mfma_f32_16x16x32_bf16 v[72:75], v[248:251], v[182:185], v[72:75]
	ds_write_b64 v161, v[2:3] offset:17664
	v_mfma_f32_16x16x32_bf16 v[68:71], v[202:205], v[182:185], v[68:71]
	v_mfma_f32_16x16x32_bf16 v[64:67], v[206:209], v[182:185], v[64:67]
	buffer_load_dwordx4 v[0:3], v160, s[16:19], s27 offen
	s_waitcnt lgkmcnt(2)
	v_mfma_f32_16x16x32_bf16 v[60:63], v[244:247], v[186:189], v[60:63]
	v_mfma_f32_16x16x32_bf16 v[56:59], v[248:251], v[186:189], v[56:59]
	v_mfma_f32_16x16x32_bf16 v[52:55], v[202:205], v[186:189], v[52:55]
	v_mfma_f32_16x16x32_bf16 v[48:51], v[206:209], v[186:189], v[48:51]
	s_waitcnt lgkmcnt(1)
	s_waitcnt vmcnt(11)
	v_cvt_pk_bf16_f32 v19, v18, v19
	v_cvt_pk_bf16_f32 v18, v16, v17
	ds_write_b64 v161, v[18:19] offset:26368
	buffer_load_dwordx4 v[16:19], v160, s[16:19], s9 offen
	s_waitcnt vmcnt(8)
	s_waitcnt lgkmcnt(0)
	s_barrier
	s_add_i32 s8, s8, 2
	s_add_i32 s9, s9, 0x100000
	s_addk_i32 s24, 0x100
	s_cmp_ge_i32 s8, s67
	s_cbranch_scc0 .LBB0_378
	v_mfma_f32_16x16x32_bf16 v[44:47], v[244:247], v[252:255], v[44:47]
	v_mfma_f32_16x16x32_bf16 v[40:43], v[248:251], v[252:255], v[40:43]
	v_mfma_f32_16x16x32_bf16 v[36:39], v[202:205], v[252:255], v[36:39]
	v_mfma_f32_16x16x32_bf16 v[32:35], v[206:209], v[252:255], v[32:35]
	s_branch .LBB0_380

;     ...
;     for (int ui = 0;; ++ui) {
; #pragma unroll
;         for (int m = 0; m < MF; ++m)
; #pragma unroll
;             for (int n = 0; n < 4; ++n) acc[m][n] = (f32x4){0.f, 0.f, 0.f, 0.f};
;         for (int t = 0; t < nt - 2; t += 2) {
;             G_TILE(G_A0, G_B0, true, G_B1, G_A1, t + 1, true, t + 2, (void)0);
.LBB0_649:
	s_andn2_b64 vcc, exec, s[40:41]
	v_mov_b32_e32 v175, 0
	s_cbranch_vccnz .LBB0_652
	v_mov_b32_e32 v32, 0
	s_mov_b32 s16, 0
	s_mov_b32 s17, 0x1e0000
	s_movk_i32 s36, 0x100
	v_mov_b32_e32 v33, v32
	v_mov_b32_e32 v34, v32
	v_mov_b32_e32 v35, v32
	v_mov_b32_e32 v36, v32
	v_mov_b32_e32 v37, v32
	v_mov_b32_e32 v38, v32
	v_mov_b32_e32 v39, v32
	v_mov_b32_e32 v40, v32
	v_mov_b32_e32 v41, v32
	v_mov_b32_e32 v42, v32
	v_mov_b32_e32 v43, v32
	v_mov_b32_e32 v44, v32
	v_mov_b32_e32 v45, v32
	v_mov_b32_e32 v46, v32
	v_mov_b32_e32 v47, v32
	v_mov_b32_e32 v48, v32
	v_mov_b32_e32 v49, v32
	v_mov_b32_e32 v50, v32
	v_mov_b32_e32 v51, v32
	v_mov_b32_e32 v52, v32
	v_mov_b32_e32 v53, v32
	v_mov_b32_e32 v54, v32
	v_mov_b32_e32 v55, v32
	v_mov_b32_e32 v56, v32
	v_mov_b32_e32 v57, v32
	v_mov_b32_e32 v58, v32
	v_mov_b32_e32 v59, v32
	v_mov_b32_e32 v68, v32
	v_mov_b32_e32 v69, v32
	v_mov_b32_e32 v70, v32
	v_mov_b32_e32 v71, v32
	v_mov_b32_e32 v76, v32
	v_mov_b32_e32 v77, v32
	v_mov_b32_e32 v78, v32
	v_mov_b32_e32 v79, v32
	v_mov_b32_e32 v60, v32
	v_mov_b32_e32 v61, v32
	v_mov_b32_e32 v62, v32
	v_mov_b32_e32 v63, v32
	v_mov_b32_e32 v64, v32
	v_mov_b32_e32 v65, v32
	v_mov_b32_e32 v66, v32
	v_mov_b32_e32 v67, v32
	v_mov_b32_e32 v72, v32
	v_mov_b32_e32 v73, v32
	v_mov_b32_e32 v74, v32
	v_mov_b32_e32 v75, v32
	v_mov_b32_e32 v80, v32
	v_mov_b32_e32 v81, v32
	v_mov_b32_e32 v82, v32
	v_mov_b32_e32 v83, v32
	v_mov_b32_e32 v84, v32
	v_mov_b32_e32 v85, v32
	v_mov_b32_e32 v86, v32
	v_mov_b32_e32 v87, v32
	v_mov_b32_e32 v96, v32
	v_mov_b32_e32 v97, v32
	v_mov_b32_e32 v98, v32
	v_mov_b32_e32 v99, v32
	v_mov_b32_e32 v104, v32
	v_mov_b32_e32 v105, v32
	v_mov_b32_e32 v106, v32
	v_mov_b32_e32 v107, v32
	v_mov_b32_e32 v108, v32
	v_mov_b32_e32 v109, v32
	v_mov_b32_e32 v110, v32
	v_mov_b32_e32 v111, v32
	v_mov_b32_e32 v88, v32
	v_mov_b32_e32 v89, v32
	v_mov_b32_e32 v90, v32
	v_mov_b32_e32 v91, v32
	v_mov_b32_e32 v92, v32
	v_mov_b32_e32 v93, v32
	v_mov_b32_e32 v94, v32
	v_mov_b32_e32 v95, v32
	v_mov_b32_e32 v100, v32
	v_mov_b32_e32 v101, v32
	v_mov_b32_e32 v102, v32
	v_mov_b32_e32 v103, v32
	v_mov_b32_e32 v112, v32
	v_mov_b32_e32 v113, v32
	v_mov_b32_e32 v114, v32
	v_mov_b32_e32 v115, v32
	v_mov_b32_e32 v116, v32
	v_mov_b32_e32 v117, v32
	v_mov_b32_e32 v118, v32
	v_mov_b32_e32 v119, v32
	v_mov_b32_e32 v128, v32
	v_mov_b32_e32 v129, v32
	v_mov_b32_e32 v130, v32
	v_mov_b32_e32 v131, v32
	v_mov_b32_e32 v136, v32
	v_mov_b32_e32 v137, v32
	v_mov_b32_e32 v138, v32
	v_mov_b32_e32 v139, v32
	v_mov_b32_e32 v140, v32
	v_mov_b32_e32 v141, v32
	v_mov_b32_e32 v142, v32
	v_mov_b32_e32 v143, v32
	v_mov_b32_e32 v120, v32
	v_mov_b32_e32 v121, v32
	v_mov_b32_e32 v122, v32
	v_mov_b32_e32 v123, v32
	v_mov_b32_e32 v124, v32
	v_mov_b32_e32 v125, v32
	v_mov_b32_e32 v126, v32
	v_mov_b32_e32 v127, v32
	v_mov_b32_e32 v132, v32
	v_mov_b32_e32 v133, v32
	v_mov_b32_e32 v134, v32
	v_mov_b32_e32 v135, v32
	v_mov_b32_e32 v144, v32
	v_mov_b32_e32 v145, v32
	v_mov_b32_e32 v146, v32
	v_mov_b32_e32 v147, v32
	v_mov_b32_e32 v148, v32
	v_mov_b32_e32 v149, v32
	v_mov_b32_e32 v150, v32
	v_mov_b32_e32 v151, v32
	v_mov_b32_e32 v152, v32
	v_mov_b32_e32 v153, v32
	v_mov_b32_e32 v154, v32
	v_mov_b32_e32 v155, v32
	v_mov_b32_e32 v156, v32
	v_mov_b32_e32 v157, v32
	v_mov_b32_e32 v158, v32
	v_mov_b32_e32 v159, v32
	v_mov_b32_e32 v160, v32
	v_mov_b32_e32 v161, v32
	v_mov_b32_e32 v162, v32
	v_mov_b32_e32 v163, v32
	v_mov_b32_e32 v164, v32
	v_mov_b32_e32 v165, v32
	v_mov_b32_e32 v166, v32
	v_mov_b32_e32 v167, v32
	v_mov_b32_e32 v168, v32
	v_mov_b32_e32 v169, v32
	v_mov_b32_e32 v170, v32
	v_mov_b32_e32 v171, v32
	v_mov_b32_e32 v172, v32
	v_mov_b32_e32 v173, v32
	v_mov_b32_e32 v174, v32
	v_mov_b32_e32 v175, v32
	v_mov_b32_e32 v218, 0
	v_mov_b32_e32 v219, 0
	v_mov_b32_e32 v220, 0
	v_mov_b32_e32 v221, 0
	v_mov_b32_e32 v238, 0
	v_mov_b32_e32 v239, 0
	v_mov_b32_e32 v240, 0
	v_mov_b32_e32 v241, 0
	v_mov_b32_e32 v244, 0
	v_mov_b32_e32 v245, 0
	v_mov_b32_e32 v246, 0
	v_mov_b32_e32 v247, 0
	v_mov_b32_e32 v248, 0
	v_mov_b32_e32 v249, 0
	v_mov_b32_e32 v250, 0
	v_mov_b32_e32 v251, 0
	v_mov_b32_e32 v252, 0
	v_mov_b32_e32 v253, 0
	v_mov_b32_e32 v254, 0
	v_mov_b32_e32 v255, 0
.LBB0_651:
	s_mov_b32 m0, s85
	s_add_i32 s37, s36, 0xffffff80
	ds_read_b64_tr_b16 v[178:179], v188
	ds_read_b64_tr_b16 v[176:177], v187
	ds_read_b64_tr_b16 v[180:181], v187 offset:32
	ds_read_b64_tr_b16 v[198:199], v187 offset:64
	ds_read_b64_tr_b16 v[202:203], v187 offset:96
	ds_read_b128 v[206:209], v186
	ds_read_b64_tr_b16 v[182:183], v188 offset:32
	ds_read_b64_tr_b16 v[200:201], v188 offset:64
	ds_read_b64_tr_b16 v[204:205], v188 offset:96
	ds_read_b128 v[210:213], v186 offset:2048
	ds_read_b128 v[214:217], v186 offset:4096
	buffer_load_dwordx4 v189, s[20:23], s37 offen lds
	s_mov_b32 m0, s7
	v_mfma_f32_16x16x32_bf16 v[44:47], v[244:247], v[238:241], v[44:47]
	v_mfma_f32_16x16x32_bf16 v[40:43], v[218:221], v[238:241], v[40:43]
	v_mfma_f32_16x16x32_bf16 v[36:39], v[248:251], v[238:241], v[36:39]
	v_mfma_f32_16x16x32_bf16 v[32:35], v[252:255], v[238:241], v[32:35]
	s_waitcnt lgkmcnt(5)
	v_mfma_f32_16x16x32_bf16 v[172:175], v[176:179], v[206:209], v[172:175]
	buffer_load_dwordx4 v192, s[20:23], s37 offen lds
	s_mov_b32 m0, s6
	s_nop 0
	buffer_load_dwordx4 v191, s[20:23], s37 offen lds
	s_mov_b32 m0, s47
	s_waitcnt lgkmcnt(4)
	v_mfma_f32_16x16x32_bf16 v[168:171], v[180:183], v[206:209], v[168:171]
	buffer_load_dwordx4 v190, s[20:23], s37 offen lds
	s_mov_b32 m0, s48
	s_nop 0
	buffer_load_dwordx4 v193, s[20:23], s37 offen lds
	s_waitcnt lgkmcnt(3)
	v_mfma_f32_16x16x32_bf16 v[164:167], v[198:201], v[206:209], v[164:167]
	s_add_i32 s37, s17, 0xfff20000
	s_waitcnt lgkmcnt(2)
	v_mfma_f32_16x16x32_bf16 v[160:163], v[202:205], v[206:209], v[160:163]
	s_waitcnt lgkmcnt(1)
	v_mfma_f32_16x16x32_bf16 v[156:159], v[176:179], v[210:213], v[156:159]
	ds_read_b128 v[206:209], v186 offset:6144
	s_waitcnt vmcnt(12)
	v_cvt_pk_bf16_f32 v15, v14, v15
	v_cvt_pk_bf16_f32 v14, v12, v13
	v_mfma_f32_16x16x32_bf16 v[152:155], v[180:183], v[210:213], v[152:155]
	ds_write_b64 v185, v[14:15] offset:34816
	v_mfma_f32_16x16x32_bf16 v[148:151], v[198:201], v[210:213], v[148:151]
	v_mfma_f32_16x16x32_bf16 v[144:147], v[202:205], v[210:213], v[144:147]
	buffer_load_dwordx4 v[12:15], v184, s[24:27], s37 offen
	s_waitcnt lgkmcnt(2)
	v_mfma_f32_16x16x32_bf16 v[132:135], v[176:179], v[214:217], v[132:135]
	ds_read_b128 v[210:213], v186 offset:8192
	v_mfma_f32_16x16x32_bf16 v[124:127], v[180:183], v[214:217], v[124:127]
	v_mfma_f32_16x16x32_bf16 v[120:123], v[198:201], v[214:217], v[120:123]
	v_mfma_f32_16x16x32_bf16 v[140:143], v[202:205], v[214:217], v[140:143]
	s_waitcnt lgkmcnt(2)
	v_mfma_f32_16x16x32_bf16 v[136:139], v[176:179], v[206:209], v[136:139]
	ds_read_b128 v[214:217], v186 offset:10240
	s_waitcnt vmcnt(12)
	v_cvt_pk_bf16_f32 v3, v2, v3
	v_cvt_pk_bf16_f32 v2, v0, v1
	v_mfma_f32_16x16x32_bf16 v[128:131], v[180:183], v[206:209], v[128:131]
	ds_write_b64 v185, v[2:3] offset:43520
	v_mfma_f32_16x16x32_bf16 v[116:119], v[198:201], v[206:209], v[116:119]
	v_mfma_f32_16x16x32_bf16 v[112:115], v[202:205], v[206:209], v[112:115]
	s_add_i32 s38, s17, 0xfff40000
	buffer_load_dwordx4 v[0:3], v184, s[24:27], s38 offen
	s_waitcnt lgkmcnt(2)
	v_mfma_f32_16x16x32_bf16 v[100:103], v[176:179], v[210:213], v[100:103]
	ds_read_b128 v[206:209], v186 offset:12288
	v_mfma_f32_16x16x32_bf16 v[92:95], v[180:183], v[210:213], v[92:95]
	v_mfma_f32_16x16x32_bf16 v[88:91], v[198:201], v[210:213], v[88:91]
	v_mfma_f32_16x16x32_bf16 v[108:111], v[202:205], v[210:213], v[108:111]
	s_waitcnt lgkmcnt(2)
	v_mfma_f32_16x16x32_bf16 v[104:107], v[176:179], v[214:217], v[104:107]
	ds_read_b128 v[210:213], v186 offset:14336
	s_waitcnt vmcnt(12)
	v_cvt_pk_bf16_f32 v31, v30, v31
	v_cvt_pk_bf16_f32 v30, v28, v29
	v_mfma_f32_16x16x32_bf16 v[96:99], v[180:183], v[214:217], v[96:99]
	ds_write_b64 v185, v[30:31] offset:52224
	v_mfma_f32_16x16x32_bf16 v[84:87], v[198:201], v[214:217], v[84:87]
	v_mfma_f32_16x16x32_bf16 v[80:83], v[202:205], v[214:217], v[80:83]
	s_add_i32 s39, s17, 0xfff60000
	buffer_load_dwordx4 v[28:31], v184, s[24:27], s39 offen
	s_waitcnt lgkmcnt(2)
	v_mfma_f32_16x16x32_bf16 v[72:75], v[176:179], v[206:209], v[72:75]
	ds_read_b128 v[214:217], v186 offset:16384
	v_mfma_f32_16x16x32_bf16 v[64:67], v[180:183], v[206:209], v[64:67]
	v_mfma_f32_16x16x32_bf16 v[60:63], v[198:201], v[206:209], v[60:63]
	v_mfma_f32_16x16x32_bf16 v[76:79], v[202:205], v[206:209], v[76:79]
	s_waitcnt lgkmcnt(2)
	v_mfma_f32_16x16x32_bf16 v[68:71], v[176:179], v[210:213], v[68:71]
	ds_read_b128 v[206:209], v186 offset:1024
	s_waitcnt vmcnt(12)
	v_cvt_pk_bf16_f32 v27, v26, v27
	v_cvt_pk_bf16_f32 v26, v24, v25
	v_mfma_f32_16x16x32_bf16 v[56:59], v[180:183], v[210:213], v[56:59]
	ds_write_b64 v185, v[26:27] offset:60928
	v_mfma_f32_16x16x32_bf16 v[52:55], v[198:201], v[210:213], v[52:55]
	v_mfma_f32_16x16x32_bf16 v[48:51], v[202:205], v[210:213], v[48:51]
	s_add_i32 s42, s17, 0xfff80000
	buffer_load_dwordx4 v[24:27], v184, s[24:27], s42 offen
	ds_read_b128 v[210:213], v186 offset:3072
	s_waitcnt lgkmcnt(3)
	v_mfma_f32_16x16x32_bf16 v[44:47], v[176:179], v[214:217], v[44:47]
	ds_read_b64_tr_b16 v[246:247], v188 offset:17408
	ds_read_b64_tr_b16 v[220:221], v188 offset:17440
	ds_read_b64_tr_b16 v[244:245], v187 offset:17408
	ds_read_b64_tr_b16 v[218:219], v187 offset:17440
	v_mfma_f32_16x16x32_bf16 v[40:43], v[180:183], v[214:217], v[40:43]
	ds_read_b64_tr_b16 v[248:249], v187 offset:17472
	ds_read_b64_tr_b16 v[250:251], v188 offset:17472
	v_mfma_f32_16x16x32_bf16 v[36:39], v[198:201], v[214:217], v[36:39]
	ds_read_b64_tr_b16 v[252:253], v187 offset:17504
	ds_read_b64_tr_b16 v[254:255], v188 offset:17504
	v_mfma_f32_16x16x32_bf16 v[32:35], v[202:205], v[214:217], v[32:35]
	s_waitcnt lgkmcnt(5)
	v_mfma_f32_16x16x32_bf16 v[172:175], v[244:247], v[206:209], v[172:175]
	ds_read_b128 v[202:205], v186 offset:5120
	s_waitcnt vmcnt(12)
	v_cvt_pk_bf16_f32 v23, v22, v23
	v_cvt_pk_bf16_f32 v22, v20, v21
	s_waitcnt lgkmcnt(5)
	v_mfma_f32_16x16x32_bf16 v[168:171], v[218:221], v[206:209], v[168:171]
	ds_write_b64 v185, v[22:23] offset:34880
	s_waitcnt lgkmcnt(4)
	v_mfma_f32_16x16x32_bf16 v[164:167], v[248:251], v[206:209], v[164:167]
	s_waitcnt lgkmcnt(2)
	v_mfma_f32_16x16x32_bf16 v[160:163], v[252:255], v[206:209], v[160:163]
	buffer_load_dwordx4 v[20:23], v184, s[28:31], s37 offen
	v_mfma_f32_16x16x32_bf16 v[156:159], v[244:247], v[210:213], v[156:159]
	ds_read_b128 v[206:209], v186 offset:7168
	v_mfma_f32_16x16x32_bf16 v[152:155], v[218:221], v[210:213], v[152:155]
	v_mfma_f32_16x16x32_bf16 v[148:151], v[248:251], v[210:213], v[148:151]
	v_mfma_f32_16x16x32_bf16 v[144:147], v[252:255], v[210:213], v[144:147]
	s_waitcnt lgkmcnt(2)
	v_mfma_f32_16x16x32_bf16 v[132:135], v[244:247], v[202:205], v[132:135]
	ds_read_b128 v[210:213], v186 offset:9216
	s_waitcnt vmcnt(12)
	v_cvt_pk_bf16_f32 v7, v6, v7
	v_cvt_pk_bf16_f32 v6, v4, v5
	v_mfma_f32_16x16x32_bf16 v[124:127], v[218:221], v[202:205], v[124:127]
	ds_write_b64 v185, v[6:7] offset:43584
	v_mfma_f32_16x16x32_bf16 v[120:123], v[248:251], v[202:205], v[120:123]
	v_mfma_f32_16x16x32_bf16 v[140:143], v[252:255], v[202:205], v[140:143]
	buffer_load_dwordx4 v[4:7], v184, s[28:31], s38 offen
	s_waitcnt lgkmcnt(2)
;     ...
;             G_TILE(G_A1, G_B1, true, G_B0, G_A0, t + 2, true, t + 3, (void)0);
	v_mfma_f32_16x16x32_bf16 v[136:139], v[244:247], v[206:209], v[136:139]
	ds_read_b128 v[202:205], v186 offset:11264
	v_mfma_f32_16x16x32_bf16 v[128:131], v[218:221], v[206:209], v[128:131]
	v_mfma_f32_16x16x32_bf16 v[116:119], v[248:251], v[206:209], v[116:119]
	v_mfma_f32_16x16x32_bf16 v[112:115], v[252:255], v[206:209], v[112:115]
	s_waitcnt lgkmcnt(2)
	v_mfma_f32_16x16x32_bf16 v[100:103], v[244:247], v[210:213], v[100:103]
	ds_read_b128 v[206:209], v186 offset:13312
	s_waitcnt vmcnt(12)
	v_cvt_pk_bf16_f32 v11, v10, v11
	v_cvt_pk_bf16_f32 v10, v8, v9
	v_mfma_f32_16x16x32_bf16 v[92:95], v[218:221], v[210:213], v[92:95]
	ds_write_b64 v185, v[10:11] offset:52288
	v_mfma_f32_16x16x32_bf16 v[88:91], v[248:251], v[210:213], v[88:91]
	v_mfma_f32_16x16x32_bf16 v[108:111], v[252:255], v[210:213], v[108:111]
	buffer_load_dwordx4 v[8:11], v184, s[28:31], s39 offen
	s_waitcnt lgkmcnt(2)
	v_mfma_f32_16x16x32_bf16 v[104:107], v[244:247], v[202:205], v[104:107]
	ds_read_b128 v[210:213], v186 offset:15360
	v_mfma_f32_16x16x32_bf16 v[96:99], v[218:221], v[202:205], v[96:99]
	v_mfma_f32_16x16x32_bf16 v[84:87], v[248:251], v[202:205], v[84:87]
	v_mfma_f32_16x16x32_bf16 v[80:83], v[252:255], v[202:205], v[80:83]
	s_waitcnt lgkmcnt(2)
	v_mfma_f32_16x16x32_bf16 v[72:75], v[244:247], v[206:209], v[72:75]
	ds_read_b128 v[238:241], v186 offset:17408
	s_waitcnt vmcnt(12)
	v_cvt_pk_bf16_f32 v19, v18, v19
	v_cvt_pk_bf16_f32 v18, v16, v17
	v_mfma_f32_16x16x32_bf16 v[64:67], v[218:221], v[206:209], v[64:67]
	ds_write_b64 v185, v[18:19] offset:60992
	v_mfma_f32_16x16x32_bf16 v[60:63], v[248:251], v[206:209], v[60:63]
	v_mfma_f32_16x16x32_bf16 v[76:79], v[252:255], v[206:209], v[76:79]
	buffer_load_dwordx4 v[16:19], v184, s[28:31], s42 offen
	s_waitcnt lgkmcnt(2)
	v_mfma_f32_16x16x32_bf16 v[68:71], v[244:247], v[210:213], v[68:71]
	v_mfma_f32_16x16x32_bf16 v[56:59], v[218:221], v[210:213], v[56:59]
	v_mfma_f32_16x16x32_bf16 v[52:55], v[248:251], v[210:213], v[52:55]
	v_mfma_f32_16x16x32_bf16 v[48:51], v[252:255], v[210:213], v[48:51]
	s_waitcnt lgkmcnt(1)
	s_waitcnt vmcnt(8)
	s_mov_b32 m0, s46
	s_waitcnt lgkmcnt(0)
	s_barrier
	ds_read_b64_tr_b16 v[178:179], v188 offset:34816
	ds_read_b64_tr_b16 v[176:177], v187 offset:34816
	ds_read_b64_tr_b16 v[180:181], v187 offset:34848
	ds_read_b64_tr_b16 v[198:199], v187 offset:34880
	ds_read_b64_tr_b16 v[202:203], v187 offset:34912
	ds_read_b128 v[206:209], v186 offset:36864
	ds_read_b64_tr_b16 v[182:183], v188 offset:34848
	ds_read_b64_tr_b16 v[200:201], v188 offset:34880
	ds_read_b64_tr_b16 v[204:205], v188 offset:34912
	ds_read_b128 v[210:213], v186 offset:38912
	ds_read_b128 v[214:217], v186 offset:40960
	buffer_load_dwordx4 v189, s[20:23], s36 offen lds
	s_mov_b32 m0, s86
	v_mfma_f32_16x16x32_bf16 v[44:47], v[244:247], v[238:241], v[44:47]
	v_mfma_f32_16x16x32_bf16 v[40:43], v[218:221], v[238:241], v[40:43]
	v_mfma_f32_16x16x32_bf16 v[36:39], v[248:251], v[238:241], v[36:39]
	v_mfma_f32_16x16x32_bf16 v[32:35], v[252:255], v[238:241], v[32:35]
	s_waitcnt lgkmcnt(5)
	v_mfma_f32_16x16x32_bf16 v[172:175], v[176:179], v[206:209], v[172:175]
	buffer_load_dwordx4 v192, s[20:23], s36 offen lds
	s_mov_b32 m0, s89
	s_add_i32 s37, s17, 0xfffa0000
	buffer_load_dwordx4 v191, s[20:23], s36 offen lds
	s_mov_b32 m0, s90
	s_waitcnt lgkmcnt(4)
	v_mfma_f32_16x16x32_bf16 v[168:171], v[180:183], v[206:209], v[168:171]
	buffer_load_dwordx4 v190, s[20:23], s36 offen lds
	s_mov_b32 m0, s91
	s_nop 0
	buffer_load_dwordx4 v193, s[20:23], s36 offen lds
	s_waitcnt lgkmcnt(3)
	v_mfma_f32_16x16x32_bf16 v[164:167], v[198:201], v[206:209], v[164:167]
	s_waitcnt lgkmcnt(2)
	v_mfma_f32_16x16x32_bf16 v[160:163], v[202:205], v[206:209], v[160:163]
	s_waitcnt lgkmcnt(1)
	v_mfma_f32_16x16x32_bf16 v[156:159], v[176:179], v[210:213], v[156:159]
	ds_read_b128 v[206:209], v186 offset:43008
	s_waitcnt vmcnt(12)
	v_cvt_pk_bf16_f32 v15, v14, v15
	v_cvt_pk_bf16_f32 v14, v12, v13
	v_mfma_f32_16x16x32_bf16 v[152:155], v[180:183], v[210:213], v[152:155]
	ds_write_b64 v185, v[14:15]
	v_mfma_f32_16x16x32_bf16 v[148:151], v[198:201], v[210:213], v[148:151]
	v_mfma_f32_16x16x32_bf16 v[144:147], v[202:205], v[210:213], v[144:147]
	buffer_load_dwordx4 v[12:15], v184, s[24:27], s37 offen
	s_waitcnt lgkmcnt(2)
	v_mfma_f32_16x16x32_bf16 v[132:135], v[176:179], v[214:217], v[132:135]
	ds_read_b128 v[210:213], v186 offset:45056
	v_mfma_f32_16x16x32_bf16 v[124:127], v[180:183], v[214:217], v[124:127]
	v_mfma_f32_16x16x32_bf16 v[120:123], v[198:201], v[214:217], v[120:123]
	v_mfma_f32_16x16x32_bf16 v[140:143], v[202:205], v[214:217], v[140:143]
	s_waitcnt lgkmcnt(2)
	v_mfma_f32_16x16x32_bf16 v[136:139], v[176:179], v[206:209], v[136:139]
	ds_read_b128 v[214:217], v186 offset:47104
	s_waitcnt vmcnt(12)
	v_cvt_pk_bf16_f32 v3, v2, v3
	v_cvt_pk_bf16_f32 v2, v0, v1
	v_mfma_f32_16x16x32_bf16 v[128:131], v[180:183], v[206:209], v[128:131]
	ds_write_b64 v185, v[2:3] offset:8704
	v_mfma_f32_16x16x32_bf16 v[116:119], v[198:201], v[206:209], v[116:119]
	v_mfma_f32_16x16x32_bf16 v[112:115], v[202:205], v[206:209], v[112:115]
	s_add_i32 s38, s17, 0xfffc0000
	buffer_load_dwordx4 v[0:3], v184, s[24:27], s38 offen
	s_waitcnt lgkmcnt(2)
	v_mfma_f32_16x16x32_bf16 v[100:103], v[176:179], v[210:213], v[100:103]
	ds_read_b128 v[206:209], v186 offset:49152
	v_mfma_f32_16x16x32_bf16 v[92:95], v[180:183], v[210:213], v[92:95]
	v_mfma_f32_16x16x32_bf16 v[88:91], v[198:201], v[210:213], v[88:91]
	v_mfma_f32_16x16x32_bf16 v[108:111], v[202:205], v[210:213], v[108:111]
	s_waitcnt lgkmcnt(2)
	v_mfma_f32_16x16x32_bf16 v[104:107], v[176:179], v[214:217], v[104:107]
	ds_read_b128 v[210:213], v186 offset:51200
	s_waitcnt vmcnt(12)
; #define G_ENDTILE(VM) do { asm volatile("s_waitcnt vmcnt(" #VM ")" ::: "memory"); \
;         asm volatile("s_waitcnt lgkmcnt(0)" ::: "memory"); __builtin_amdgcn_s_barrier(); asm volatile("" ::: "memory"); } while (0)
;     ...
;         for (int t = 0; t < nt - 2; t += 2) {
;             G_TILE(G_A0, G_B0, true, G_B1, G_A1, t + 1, true, t + 2, (void)0);
;             G_ENDTILE(8);
;             G_TILE(G_A1, G_B1, true, G_B0, G_A0, t + 2, true, t + 3, (void)0);
;             G_ENDTILE(8);
;         }
	v_cvt_pk_bf16_f32 v31, v30, v31
	v_cvt_pk_bf16_f32 v30, v28, v29
	v_mfma_f32_16x16x32_bf16 v[96:99], v[180:183], v[214:217], v[96:99]
	ds_write_b64 v185, v[30:31] offset:17408
	v_mfma_f32_16x16x32_bf16 v[84:87], v[198:201], v[214:217], v[84:87]
	v_mfma_f32_16x16x32_bf16 v[80:83], v[202:205], v[214:217], v[80:83]
	s_add_i32 s39, s17, 0xfffe0000
	buffer_load_dwordx4 v[28:31], v184, s[24:27], s39 offen
	s_waitcnt lgkmcnt(2)
	v_mfma_f32_16x16x32_bf16 v[72:75], v[176:179], v[206:209], v[72:75]
	ds_read_b128 v[214:217], v186 offset:53248
	v_mfma_f32_16x16x32_bf16 v[64:67], v[180:183], v[206:209], v[64:67]
	v_mfma_f32_16x16x32_bf16 v[60:63], v[198:201], v[206:209], v[60:63]
	v_mfma_f32_16x16x32_bf16 v[76:79], v[202:205], v[206:209], v[76:79]
	s_waitcnt lgkmcnt(2)
	v_mfma_f32_16x16x32_bf16 v[68:71], v[176:179], v[210:213], v[68:71]
	ds_read_b128 v[206:209], v186 offset:37888
	s_waitcnt vmcnt(12)
	v_cvt_pk_bf16_f32 v27, v26, v27
	v_cvt_pk_bf16_f32 v26, v24, v25
	v_mfma_f32_16x16x32_bf16 v[56:59], v[180:183], v[210:213], v[56:59]
	ds_write_b64 v185, v[26:27] offset:26112
	v_mfma_f32_16x16x32_bf16 v[52:55], v[198:201], v[210:213], v[52:55]
	v_mfma_f32_16x16x32_bf16 v[48:51], v[202:205], v[210:213], v[48:51]
	buffer_load_dwordx4 v[24:27], v184, s[24:27], s17 offen
	ds_read_b128 v[210:213], v186 offset:39936
	s_waitcnt lgkmcnt(3)
	v_mfma_f32_16x16x32_bf16 v[44:47], v[176:179], v[214:217], v[44:47]
	ds_read_b64_tr_b16 v[246:247], v188 offset:52224
	ds_read_b64_tr_b16 v[220:221], v188 offset:52256
	ds_read_b64_tr_b16 v[244:245], v187 offset:52224
	ds_read_b64_tr_b16 v[218:219], v187 offset:52256
	v_mfma_f32_16x16x32_bf16 v[40:43], v[180:183], v[214:217], v[40:43]
	ds_read_b64_tr_b16 v[248:249], v187 offset:52288
	ds_read_b64_tr_b16 v[250:251], v188 offset:52288
	v_mfma_f32_16x16x32_bf16 v[36:39], v[198:201], v[214:217], v[36:39]
	ds_read_b64_tr_b16 v[252:253], v187 offset:52320
	ds_read_b64_tr_b16 v[254:255], v188 offset:52320
	v_mfma_f32_16x16x32_bf16 v[32:35], v[202:205], v[214:217], v[32:35]
	s_waitcnt lgkmcnt(5)
	v_mfma_f32_16x16x32_bf16 v[172:175], v[244:247], v[206:209], v[172:175]
	ds_read_b128 v[202:205], v186 offset:41984
	s_waitcnt vmcnt(12)
	v_cvt_pk_bf16_f32 v23, v22, v23
	v_cvt_pk_bf16_f32 v22, v20, v21
	s_waitcnt lgkmcnt(5)
	v_mfma_f32_16x16x32_bf16 v[168:171], v[218:221], v[206:209], v[168:171]
	ds_write_b64 v185, v[22:23] offset:64
	s_waitcnt lgkmcnt(4)
	v_mfma_f32_16x16x32_bf16 v[164:167], v[248:251], v[206:209], v[164:167]
	s_waitcnt lgkmcnt(2)
	v_mfma_f32_16x16x32_bf16 v[160:163], v[252:255], v[206:209], v[160:163]
	buffer_load_dwordx4 v[20:23], v184, s[28:31], s37 offen
	v_mfma_f32_16x16x32_bf16 v[156:159], v[244:247], v[210:213], v[156:159]
	ds_read_b128 v[206:209], v186 offset:44032
	v_mfma_f32_16x16x32_bf16 v[152:155], v[218:221], v[210:213], v[152:155]
	v_mfma_f32_16x16x32_bf16 v[148:151], v[248:251], v[210:213], v[148:151]
	v_mfma_f32_16x16x32_bf16 v[144:147], v[252:255], v[210:213], v[144:147]
	s_waitcnt lgkmcnt(2)
	v_mfma_f32_16x16x32_bf16 v[132:135], v[244:247], v[202:205], v[132:135]
	ds_read_b128 v[210:213], v186 offset:46080
	s_waitcnt vmcnt(12)
	v_cvt_pk_bf16_f32 v7, v6, v7
	v_cvt_pk_bf16_f32 v6, v4, v5
	v_mfma_f32_16x16x32_bf16 v[124:127], v[218:221], v[202:205], v[124:127]
	ds_write_b64 v185, v[6:7] offset:8768
	v_mfma_f32_16x16x32_bf16 v[120:123], v[248:251], v[202:205], v[120:123]
	v_mfma_f32_16x16x32_bf16 v[140:143], v[252:255], v[202:205], v[140:143]
	buffer_load_dwordx4 v[4:7], v184, s[28:31], s38 offen
	s_waitcnt lgkmcnt(2)
	v_mfma_f32_16x16x32_bf16 v[136:139], v[244:247], v[206:209], v[136:139]
	ds_read_b128 v[202:205], v186 offset:48128
	v_mfma_f32_16x16x32_bf16 v[128:131], v[218:221], v[206:209], v[128:131]
	v_mfma_f32_16x16x32_bf16 v[116:119], v[248:251], v[206:209], v[116:119]
	v_mfma_f32_16x16x32_bf16 v[112:115], v[252:255], v[206:209], v[112:115]
	s_waitcnt lgkmcnt(2)
	v_mfma_f32_16x16x32_bf16 v[100:103], v[244:247], v[210:213], v[100:103]
	ds_read_b128 v[206:209], v186 offset:50176
	s_waitcnt vmcnt(12)
	v_cvt_pk_bf16_f32 v11, v10, v11
	v_cvt_pk_bf16_f32 v10, v8, v9
	v_mfma_f32_16x16x32_bf16 v[92:95], v[218:221], v[210:213], v[92:95]
	ds_write_b64 v185, v[10:11] offset:17472
	v_mfma_f32_16x16x32_bf16 v[88:91], v[248:251], v[210:213], v[88:91]
	v_mfma_f32_16x16x32_bf16 v[108:111], v[252:255], v[210:213], v[108:111]
	buffer_load_dwordx4 v[8:11], v184, s[28:31], s39 offen
	s_waitcnt lgkmcnt(2)
	v_mfma_f32_16x16x32_bf16 v[104:107], v[244:247], v[202:205], v[104:107]
	ds_read_b128 v[210:213], v186 offset:52224
	v_mfma_f32_16x16x32_bf16 v[96:99], v[218:221], v[202:205], v[96:99]
	v_mfma_f32_16x16x32_bf16 v[84:87], v[248:251], v[202:205], v[84:87]
	v_mfma_f32_16x16x32_bf16 v[80:83], v[252:255], v[202:205], v[80:83]
	s_waitcnt lgkmcnt(2)
	v_mfma_f32_16x16x32_bf16 v[72:75], v[244:247], v[206:209], v[72:75]
	ds_read_b128 v[238:241], v186 offset:54272
	s_waitcnt vmcnt(12)
	v_cvt_pk_bf16_f32 v19, v18, v19
	v_cvt_pk_bf16_f32 v18, v16, v17
	v_mfma_f32_16x16x32_bf16 v[64:67], v[218:221], v[206:209], v[64:67]
	ds_write_b64 v185, v[18:19] offset:26176
	v_mfma_f32_16x16x32_bf16 v[60:63], v[248:251], v[206:209], v[60:63]
	v_mfma_f32_16x16x32_bf16 v[76:79], v[252:255], v[206:209], v[76:79]
	buffer_load_dwordx4 v[16:19], v184, s[28:31], s17 offen
	s_waitcnt lgkmcnt(2)
	v_mfma_f32_16x16x32_bf16 v[68:71], v[244:247], v[210:213], v[68:71]
	v_mfma_f32_16x16x32_bf16 v[56:59], v[218:221], v[210:213], v[56:59]
	v_mfma_f32_16x16x32_bf16 v[52:55], v[248:251], v[210:213], v[52:55]
	v_mfma_f32_16x16x32_bf16 v[48:51], v[252:255], v[210:213], v[48:51]
	s_waitcnt lgkmcnt(1)
	s_waitcnt vmcnt(8)
	s_waitcnt lgkmcnt(0)
	s_barrier
	s_add_i32 s16, s16, 2
	s_add_i32 s17, s17, 0x100000
	s_addk_i32 s36, 0x100
	s_cmp_ge_i32 s16, s97
	s_cbranch_scc0 .LBB0_651
	v_mfma_f32_16x16x32_bf16 v[44:47], v[244:247], v[238:241], v[44:47]
	v_mfma_f32_16x16x32_bf16 v[40:43], v[218:221], v[238:241], v[40:43]
	v_mfma_f32_16x16x32_bf16 v[36:39], v[248:251], v[238:241], v[36:39]
	v_mfma_f32_16x16x32_bf16 v[32:35], v[252:255], v[238:241], v[32:35]
	s_branch .LBB0_653

;     ...
;     for (int ui = 0;; ++ui) {
; #pragma unroll
;         for (int m = 0; m < MF; ++m)
; #pragma unroll
;             for (int n = 0; n < 4; ++n) acc[m][n] = (f32x4){0.f, 0.f, 0.f, 0.f};
;         for (int t = 0; t < nt - 2; t += 2) {
;             G_TILE(G_A0, G_B0, true, G_B1, G_A1, t + 1, true, t + 2, (void)0);
.LBB0_861:
	s_andn2_b64 vcc, exec, s[28:29]
	v_mov_b32_e32 v175, 0
	s_cbranch_vccnz .LBB0_864
	v_mov_b32_e32 v32, 0
	s_mov_b32 s8, 0
	s_mov_b32 s9, 0x1e0000
	s_movk_i32 s36, 0x100
	v_mov_b32_e32 v33, v32
	v_mov_b32_e32 v34, v32
	v_mov_b32_e32 v35, v32
	v_mov_b32_e32 v36, v32
	v_mov_b32_e32 v37, v32
	v_mov_b32_e32 v38, v32
	v_mov_b32_e32 v39, v32
	v_mov_b32_e32 v40, v32
	v_mov_b32_e32 v41, v32
	v_mov_b32_e32 v42, v32
	v_mov_b32_e32 v43, v32
	s_waitcnt vmcnt(1)
	v_mov_b32_e32 v44, v32
	v_mov_b32_e32 v45, v32
	v_mov_b32_e32 v46, v32
	v_mov_b32_e32 v47, v32
	v_mov_b32_e32 v48, v32
	v_mov_b32_e32 v49, v32
	v_mov_b32_e32 v50, v32
	v_mov_b32_e32 v51, v32
	s_waitcnt vmcnt(0)
	v_mov_b32_e32 v52, v32
	v_mov_b32_e32 v53, v32
	v_mov_b32_e32 v54, v32
	v_mov_b32_e32 v55, v32
	v_mov_b32_e32 v56, v32
	v_mov_b32_e32 v57, v32
	v_mov_b32_e32 v58, v32
	v_mov_b32_e32 v59, v32
	v_mov_b32_e32 v68, v32
	v_mov_b32_e32 v69, v32
	v_mov_b32_e32 v70, v32
	v_mov_b32_e32 v71, v32
	v_mov_b32_e32 v76, v32
	v_mov_b32_e32 v77, v32
	v_mov_b32_e32 v78, v32
	v_mov_b32_e32 v79, v32
	v_mov_b32_e32 v60, v32
	v_mov_b32_e32 v61, v32
	v_mov_b32_e32 v62, v32
	v_mov_b32_e32 v63, v32
	v_mov_b32_e32 v64, v32
	v_mov_b32_e32 v65, v32
	v_mov_b32_e32 v66, v32
	v_mov_b32_e32 v67, v32
	v_mov_b32_e32 v72, v32
	v_mov_b32_e32 v73, v32
	v_mov_b32_e32 v74, v32
	v_mov_b32_e32 v75, v32
	v_mov_b32_e32 v80, v32
	v_mov_b32_e32 v81, v32
	v_mov_b32_e32 v82, v32
	v_mov_b32_e32 v83, v32
	v_mov_b32_e32 v84, v32
	v_mov_b32_e32 v85, v32
	v_mov_b32_e32 v86, v32
	v_mov_b32_e32 v87, v32
	v_mov_b32_e32 v96, v32
	v_mov_b32_e32 v97, v32
	v_mov_b32_e32 v98, v32
	v_mov_b32_e32 v99, v32
	v_mov_b32_e32 v104, v32
	v_mov_b32_e32 v105, v32
	v_mov_b32_e32 v106, v32
	v_mov_b32_e32 v107, v32
	v_mov_b32_e32 v108, v32
	v_mov_b32_e32 v109, v32
	v_mov_b32_e32 v110, v32
	v_mov_b32_e32 v111, v32
	v_mov_b32_e32 v88, v32
	v_mov_b32_e32 v89, v32
	v_mov_b32_e32 v90, v32
	v_mov_b32_e32 v91, v32
	v_mov_b32_e32 v92, v32
	v_mov_b32_e32 v93, v32
	v_mov_b32_e32 v94, v32
	v_mov_b32_e32 v95, v32
	v_mov_b32_e32 v100, v32
	v_mov_b32_e32 v101, v32
	v_mov_b32_e32 v102, v32
	v_mov_b32_e32 v103, v32
	v_mov_b32_e32 v112, v32
	v_mov_b32_e32 v113, v32
	v_mov_b32_e32 v114, v32
	v_mov_b32_e32 v115, v32
	v_mov_b32_e32 v116, v32
	v_mov_b32_e32 v117, v32
	v_mov_b32_e32 v118, v32
	v_mov_b32_e32 v119, v32
	v_mov_b32_e32 v128, v32
	v_mov_b32_e32 v129, v32
	v_mov_b32_e32 v130, v32
	v_mov_b32_e32 v131, v32
	v_mov_b32_e32 v136, v32
	v_mov_b32_e32 v137, v32
	v_mov_b32_e32 v138, v32
	v_mov_b32_e32 v139, v32
	v_mov_b32_e32 v140, v32
	v_mov_b32_e32 v141, v32
	v_mov_b32_e32 v142, v32
	v_mov_b32_e32 v143, v32
	v_mov_b32_e32 v120, v32
	v_mov_b32_e32 v121, v32
	v_mov_b32_e32 v122, v32
	v_mov_b32_e32 v123, v32
	v_mov_b32_e32 v124, v32
	v_mov_b32_e32 v125, v32
	v_mov_b32_e32 v126, v32
	v_mov_b32_e32 v127, v32
	v_mov_b32_e32 v132, v32
	v_mov_b32_e32 v133, v32
	v_mov_b32_e32 v134, v32
	v_mov_b32_e32 v135, v32
	v_mov_b32_e32 v144, v32
	v_mov_b32_e32 v145, v32
	v_mov_b32_e32 v146, v32
	v_mov_b32_e32 v147, v32
	v_mov_b32_e32 v148, v32
	v_mov_b32_e32 v149, v32
	v_mov_b32_e32 v150, v32
	v_mov_b32_e32 v151, v32
	v_mov_b32_e32 v152, v32
	v_mov_b32_e32 v153, v32
	v_mov_b32_e32 v154, v32
	v_mov_b32_e32 v155, v32
	v_mov_b32_e32 v156, v32
	v_mov_b32_e32 v157, v32
	v_mov_b32_e32 v158, v32
	v_mov_b32_e32 v159, v32
	v_mov_b32_e32 v160, v32
	v_mov_b32_e32 v161, v32
	v_mov_b32_e32 v162, v32
	v_mov_b32_e32 v163, v32
	v_mov_b32_e32 v164, v32
	v_mov_b32_e32 v165, v32
	v_mov_b32_e32 v166, v32
	v_mov_b32_e32 v167, v32
	v_mov_b32_e32 v168, v32
	v_mov_b32_e32 v169, v32
	v_mov_b32_e32 v170, v32
	v_mov_b32_e32 v171, v32
	v_mov_b32_e32 v172, v32
	v_mov_b32_e32 v173, v32
	v_mov_b32_e32 v174, v32
	v_mov_b32_e32 v175, v32
	v_mov_b32_e32 v216, 0
	v_mov_b32_e32 v217, 0
	v_mov_b32_e32 v218, 0
	v_mov_b32_e32 v219, 0
	v_mov_b32_e32 v220, 0
	v_mov_b32_e32 v221, 0
	v_mov_b32_e32 v222, 0
	v_mov_b32_e32 v223, 0
	v_mov_b32_e32 v244, 0
	v_mov_b32_e32 v245, 0
	v_mov_b32_e32 v246, 0
	v_mov_b32_e32 v247, 0
	v_mov_b32_e32 v248, 0
	v_mov_b32_e32 v249, 0
	v_mov_b32_e32 v250, 0
	v_mov_b32_e32 v251, 0
	v_mov_b32_e32 v252, 0
	v_mov_b32_e32 v253, 0
	v_mov_b32_e32 v254, 0
	v_mov_b32_e32 v255, 0
.LBB0_863:
	s_mov_b32 m0, s85
	s_add_i32 s38, s36, 0xffffff80
	ds_read_b64_tr_b16 v[178:179], v206
	ds_read_b64_tr_b16 v[176:177], v205
	ds_read_b64_tr_b16 v[180:181], v205 offset:32
	ds_read_b64_tr_b16 v[184:185], v205 offset:64
	ds_read_b64_tr_b16 v[188:189], v205 offset:96
	ds_read_b128 v[192:195], v199
	ds_read_b64_tr_b16 v[182:183], v206 offset:32
	ds_read_b64_tr_b16 v[186:187], v206 offset:64
	ds_read_b64_tr_b16 v[190:191], v206 offset:96
	ds_read_b128 v[208:211], v199 offset:2048
	ds_read_b128 v[212:215], v199 offset:4096
	buffer_load_dwordx4 v200, s[20:23], s38 offen lds
	s_mov_b32 m0, s86
	v_mfma_f32_16x16x32_bf16 v[44:47], v[244:247], v[252:255], v[44:47]
	v_mfma_f32_16x16x32_bf16 v[40:43], v[248:251], v[252:255], v[40:43]
	v_mfma_f32_16x16x32_bf16 v[36:39], v[216:219], v[252:255], v[36:39]
	v_mfma_f32_16x16x32_bf16 v[32:35], v[220:223], v[252:255], v[32:35]
	s_waitcnt lgkmcnt(0)
	v_mfma_f32_16x16x32_bf16 v[172:175], v[176:179], v[192:195], v[172:175]
	buffer_load_dwordx4 v201, s[20:23], s38 offen lds
	s_mov_b32 m0, s87
	s_nop 0
	buffer_load_dwordx4 v202, s[20:23], s38 offen lds
	s_mov_b32 m0, s88
	v_mfma_f32_16x16x32_bf16 v[168:171], v[180:183], v[192:195], v[168:171]
	buffer_load_dwordx4 v203, s[20:23], s38 offen lds
	s_mov_b32 m0, s89
	s_nop 0
	buffer_load_dwordx4 v204, s[20:23], s38 offen lds
	v_mfma_f32_16x16x32_bf16 v[164:167], v[184:187], v[192:195], v[164:167]
	s_add_i32 s38, s9, 0xfff20000
	v_mfma_f32_16x16x32_bf16 v[160:163], v[188:191], v[192:195], v[160:163]
	v_mfma_f32_16x16x32_bf16 v[156:159], v[176:179], v[208:211], v[156:159]
	ds_read_b128 v[192:195], v199 offset:6144
	s_waitcnt vmcnt(12)
	v_cvt_pk_bf16_f32 v23, v22, v23
	v_cvt_pk_bf16_f32 v22, v20, v21
	v_mfma_f32_16x16x32_bf16 v[152:155], v[180:183], v[208:211], v[152:155]
	ds_write_b64 v198, v[22:23] offset:34816
	v_mfma_f32_16x16x32_bf16 v[148:151], v[184:187], v[208:211], v[148:151]
	v_mfma_f32_16x16x32_bf16 v[144:147], v[188:191], v[208:211], v[144:147]
	buffer_load_dwordx4 v[20:23], v197, s[24:27], s38 offen
	v_mfma_f32_16x16x32_bf16 v[132:135], v[176:179], v[212:215], v[132:135]
	ds_read_b128 v[208:211], v199 offset:8192
	v_mfma_f32_16x16x32_bf16 v[124:127], v[180:183], v[212:215], v[124:127]
	v_mfma_f32_16x16x32_bf16 v[120:123], v[184:187], v[212:215], v[120:123]
	v_mfma_f32_16x16x32_bf16 v[140:143], v[188:191], v[212:215], v[140:143]
	s_waitcnt lgkmcnt(2)
	v_mfma_f32_16x16x32_bf16 v[136:139], v[176:179], v[192:195], v[136:139]
	ds_read_b128 v[212:215], v199 offset:10240
	s_waitcnt vmcnt(11)
	v_cvt_pk_bf16_f32 v31, v30, v31
	v_cvt_pk_bf16_f32 v30, v28, v29
	v_mfma_f32_16x16x32_bf16 v[128:131], v[180:183], v[192:195], v[128:131]
	ds_write_b64 v198, v[30:31] offset:43520
	v_mfma_f32_16x16x32_bf16 v[116:119], v[184:187], v[192:195], v[116:119]
	v_mfma_f32_16x16x32_bf16 v[112:115], v[188:191], v[192:195], v[112:115]
	s_add_i32 s39, s9, 0xfff40000
	buffer_load_dwordx4 v[28:31], v197, s[24:27], s39 offen
	s_waitcnt lgkmcnt(2)
	v_mfma_f32_16x16x32_bf16 v[100:103], v[176:179], v[208:211], v[100:103]
	ds_read_b128 v[192:195], v199 offset:12288
	v_mfma_f32_16x16x32_bf16 v[92:95], v[180:183], v[208:211], v[92:95]
	v_mfma_f32_16x16x32_bf16 v[88:91], v[184:187], v[208:211], v[88:91]
	v_mfma_f32_16x16x32_bf16 v[108:111], v[188:191], v[208:211], v[108:111]
	s_waitcnt lgkmcnt(2)
	v_mfma_f32_16x16x32_bf16 v[104:107], v[176:179], v[212:215], v[104:107]
	ds_read_b128 v[208:211], v199 offset:14336
	v_cvt_pk_bf16_f32 v19, v18, v19
	v_cvt_pk_bf16_f32 v18, v16, v17
	v_mfma_f32_16x16x32_bf16 v[96:99], v[180:183], v[212:215], v[96:99]
	ds_write_b64 v198, v[18:19] offset:52224
	v_mfma_f32_16x16x32_bf16 v[84:87], v[184:187], v[212:215], v[84:87]
	v_mfma_f32_16x16x32_bf16 v[80:83], v[188:191], v[212:215], v[80:83]
	s_add_i32 s43, s9, 0xfff60000
	buffer_load_dwordx4 v[16:19], v197, s[24:27], s43 offen
	s_waitcnt lgkmcnt(2)
	v_mfma_f32_16x16x32_bf16 v[72:75], v[176:179], v[192:195], v[72:75]
	ds_read_b128 v[212:215], v199 offset:16384
	v_mfma_f32_16x16x32_bf16 v[64:67], v[180:183], v[192:195], v[64:67]
	v_mfma_f32_16x16x32_bf16 v[60:63], v[184:187], v[192:195], v[60:63]
	v_mfma_f32_16x16x32_bf16 v[76:79], v[188:191], v[192:195], v[76:79]
	s_waitcnt lgkmcnt(2)
	v_mfma_f32_16x16x32_bf16 v[68:71], v[176:179], v[208:211], v[68:71]
	ds_read_b128 v[192:195], v199 offset:1024
	s_waitcnt vmcnt(12)
	v_cvt_pk_bf16_f32 v27, v26, v27
	v_cvt_pk_bf16_f32 v26, v24, v25
	v_mfma_f32_16x16x32_bf16 v[56:59], v[180:183], v[208:211], v[56:59]
	ds_write_b64 v198, v[26:27] offset:60928
	v_mfma_f32_16x16x32_bf16 v[52:55], v[184:187], v[208:211], v[52:55]
	v_mfma_f32_16x16x32_bf16 v[48:51], v[188:191], v[208:211], v[48:51]
	s_add_i32 s45, s9, 0xfff80000
	buffer_load_dwordx4 v[24:27], v197, s[24:27], s45 offen
	ds_read_b128 v[208:211], v199 offset:3072
	s_waitcnt lgkmcnt(3)
	v_mfma_f32_16x16x32_bf16 v[44:47], v[176:179], v[212:215], v[44:47]
	ds_read_b64_tr_b16 v[246:247], v206 offset:17408
	ds_read_b64_tr_b16 v[218:219], v206 offset:17440
	ds_read_b64_tr_b16 v[244:245], v205 offset:17408
	ds_read_b64_tr_b16 v[216:217], v205 offset:17440
	v_mfma_f32_16x16x32_bf16 v[40:43], v[180:183], v[212:215], v[40:43]
	ds_read_b64_tr_b16 v[248:249], v205 offset:17472
	ds_read_b64_tr_b16 v[250:251], v206 offset:17472
	v_mfma_f32_16x16x32_bf16 v[36:39], v[184:187], v[212:215], v[36:39]
	ds_read_b64_tr_b16 v[252:253], v205 offset:17504
	ds_read_b64_tr_b16 v[254:255], v206 offset:17504
	v_mfma_f32_16x16x32_bf16 v[32:35], v[188:191], v[212:215], v[32:35]
	s_waitcnt lgkmcnt(5)
	v_mfma_f32_16x16x32_bf16 v[172:175], v[244:247], v[192:195], v[172:175]
	ds_read_b128 v[188:191], v199 offset:5120
	s_waitcnt vmcnt(12)
	v_cvt_pk_bf16_f32 v15, v14, v15
	v_cvt_pk_bf16_f32 v14, v12, v13
	s_waitcnt lgkmcnt(5)
	v_mfma_f32_16x16x32_bf16 v[168:171], v[216:219], v[192:195], v[168:171]
	ds_write_b64 v198, v[14:15] offset:35072
	s_waitcnt lgkmcnt(4)
	v_mfma_f32_16x16x32_bf16 v[164:167], v[248:251], v[192:195], v[164:167]
	s_waitcnt lgkmcnt(2)
	v_mfma_f32_16x16x32_bf16 v[160:163], v[252:255], v[192:195], v[160:163]
	buffer_load_dwordx4 v[12:15], v197, s[16:19], s38 offen
	v_mfma_f32_16x16x32_bf16 v[156:159], v[244:247], v[208:211], v[156:159]
	ds_read_b128 v[192:195], v199 offset:7168
	v_mfma_f32_16x16x32_bf16 v[152:155], v[216:219], v[208:211], v[152:155]
	v_mfma_f32_16x16x32_bf16 v[148:151], v[248:251], v[208:211], v[148:151]
	v_mfma_f32_16x16x32_bf16 v[144:147], v[252:255], v[208:211], v[144:147]
	s_waitcnt lgkmcnt(2)
	v_mfma_f32_16x16x32_bf16 v[132:135], v[244:247], v[188:191], v[132:135]
	ds_read_b128 v[208:211], v199 offset:9216
	s_waitcnt vmcnt(11)
	v_cvt_pk_bf16_f32 v7, v6, v7
	v_cvt_pk_bf16_f32 v6, v4, v5
	v_mfma_f32_16x16x32_bf16 v[124:127], v[216:219], v[188:191], v[124:127]
	ds_write_b64 v198, v[6:7] offset:43776
	v_mfma_f32_16x16x32_bf16 v[120:123], v[248:251], v[188:191], v[120:123]
	v_mfma_f32_16x16x32_bf16 v[140:143], v[252:255], v[188:191], v[140:143]
	buffer_load_dwordx4 v[4:7], v197, s[16:19], s39 offen
	s_waitcnt lgkmcnt(2)
	v_mfma_f32_16x16x32_bf16 v[136:139], v[244:247], v[192:195], v[136:139]
	ds_read_b128 v[188:191], v199 offset:11264
	v_mfma_f32_16x16x32_bf16 v[128:131], v[216:219], v[192:195], v[128:131]
	v_mfma_f32_16x16x32_bf16 v[116:119], v[248:251], v[192:195], v[116:119]
	v_mfma_f32_16x16x32_bf16 v[112:115], v[252:255], v[192:195], v[112:115]
	s_waitcnt lgkmcnt(2)
;     ...
;             G_TILE(G_A1, G_B1, true, G_B0, G_A0, t + 2, true, t + 3, (void)0);
	v_mfma_f32_16x16x32_bf16 v[100:103], v[244:247], v[208:211], v[100:103]
	ds_read_b128 v[192:195], v199 offset:13312
	v_cvt_pk_bf16_f32 v3, v2, v3
	v_cvt_pk_bf16_f32 v2, v0, v1
	v_mfma_f32_16x16x32_bf16 v[92:95], v[216:219], v[208:211], v[92:95]
	ds_write_b64 v198, v[2:3] offset:52480
	v_mfma_f32_16x16x32_bf16 v[88:91], v[248:251], v[208:211], v[88:91]
	v_mfma_f32_16x16x32_bf16 v[108:111], v[252:255], v[208:211], v[108:111]
	buffer_load_dwordx4 v[0:3], v197, s[16:19], s43 offen
	s_waitcnt lgkmcnt(2)
	v_mfma_f32_16x16x32_bf16 v[104:107], v[244:247], v[188:191], v[104:107]
	ds_read_b128 v[208:211], v199 offset:15360
	v_mfma_f32_16x16x32_bf16 v[96:99], v[216:219], v[188:191], v[96:99]
	v_mfma_f32_16x16x32_bf16 v[84:87], v[248:251], v[188:191], v[84:87]
	v_mfma_f32_16x16x32_bf16 v[80:83], v[252:255], v[188:191], v[80:83]
	s_waitcnt lgkmcnt(2)
	v_mfma_f32_16x16x32_bf16 v[72:75], v[244:247], v[192:195], v[72:75]
	ds_read_b128 v[236:239], v199 offset:17408
	s_waitcnt vmcnt(12)
	v_cvt_pk_bf16_f32 v11, v10, v11
	v_cvt_pk_bf16_f32 v10, v8, v9
	v_mfma_f32_16x16x32_bf16 v[64:67], v[216:219], v[192:195], v[64:67]
	ds_write_b64 v198, v[10:11] offset:61184
	v_mfma_f32_16x16x32_bf16 v[60:63], v[248:251], v[192:195], v[60:63]
	v_mfma_f32_16x16x32_bf16 v[76:79], v[252:255], v[192:195], v[76:79]
	buffer_load_dwordx4 v[8:11], v197, s[16:19], s45 offen
	s_waitcnt lgkmcnt(2)
	v_mfma_f32_16x16x32_bf16 v[68:71], v[244:247], v[208:211], v[68:71]
	v_mfma_f32_16x16x32_bf16 v[56:59], v[216:219], v[208:211], v[56:59]
	v_mfma_f32_16x16x32_bf16 v[52:55], v[248:251], v[208:211], v[52:55]
	v_mfma_f32_16x16x32_bf16 v[48:51], v[252:255], v[208:211], v[48:51]
	s_waitcnt lgkmcnt(1)
	s_waitcnt vmcnt(8)
	s_mov_b32 m0, s49
	s_waitcnt lgkmcnt(0)
	s_barrier
	ds_read_b64_tr_b16 v[178:179], v206 offset:34816
	ds_read_b64_tr_b16 v[176:177], v205 offset:34816
	ds_read_b64_tr_b16 v[180:181], v205 offset:34848
	ds_read_b64_tr_b16 v[184:185], v205 offset:34880
	ds_read_b64_tr_b16 v[188:189], v205 offset:34912
	ds_read_b128 v[192:195], v199 offset:36864
	ds_read_b64_tr_b16 v[182:183], v206 offset:34848
	ds_read_b64_tr_b16 v[186:187], v206 offset:34880
	ds_read_b64_tr_b16 v[190:191], v206 offset:34912
	ds_read_b128 v[208:211], v199 offset:38912
	ds_read_b128 v[212:215], v199 offset:40960
	buffer_load_dwordx4 v200, s[20:23], s36 offen lds
	s_mov_b32 m0, s68
	v_mfma_f32_16x16x32_bf16 v[44:47], v[244:247], v[236:239], v[44:47]
	v_mfma_f32_16x16x32_bf16 v[40:43], v[216:219], v[236:239], v[40:43]
	v_mfma_f32_16x16x32_bf16 v[36:39], v[248:251], v[236:239], v[36:39]
	v_mfma_f32_16x16x32_bf16 v[32:35], v[252:255], v[236:239], v[32:35]
	s_waitcnt lgkmcnt(5)
	v_mfma_f32_16x16x32_bf16 v[172:175], v[176:179], v[192:195], v[172:175]
	buffer_load_dwordx4 v201, s[20:23], s36 offen lds
	s_mov_b32 m0, s77
	s_add_i32 s38, s9, 0xfffa0000
	buffer_load_dwordx4 v202, s[20:23], s36 offen lds
	s_mov_b32 m0, s78
	s_waitcnt lgkmcnt(4)
	v_mfma_f32_16x16x32_bf16 v[168:171], v[180:183], v[192:195], v[168:171]
	buffer_load_dwordx4 v203, s[20:23], s36 offen lds
	s_mov_b32 m0, s79
	s_nop 0
	buffer_load_dwordx4 v204, s[20:23], s36 offen lds
	s_waitcnt lgkmcnt(3)
	v_mfma_f32_16x16x32_bf16 v[164:167], v[184:187], v[192:195], v[164:167]
	s_waitcnt lgkmcnt(2)
	v_mfma_f32_16x16x32_bf16 v[160:163], v[188:191], v[192:195], v[160:163]
	s_waitcnt lgkmcnt(1)
	v_mfma_f32_16x16x32_bf16 v[156:159], v[176:179], v[208:211], v[156:159]
	ds_read_b128 v[192:195], v199 offset:43008
	s_waitcnt vmcnt(12)
	v_cvt_pk_bf16_f32 v23, v22, v23
	v_cvt_pk_bf16_f32 v22, v20, v21
	v_mfma_f32_16x16x32_bf16 v[152:155], v[180:183], v[208:211], v[152:155]
	ds_write_b64 v198, v[22:23]
	v_mfma_f32_16x16x32_bf16 v[148:151], v[184:187], v[208:211], v[148:151]
	v_mfma_f32_16x16x32_bf16 v[144:147], v[188:191], v[208:211], v[144:147]
	buffer_load_dwordx4 v[20:23], v197, s[24:27], s38 offen
	s_waitcnt lgkmcnt(2)
	v_mfma_f32_16x16x32_bf16 v[132:135], v[176:179], v[212:215], v[132:135]
	ds_read_b128 v[208:211], v199 offset:45056
	v_mfma_f32_16x16x32_bf16 v[124:127], v[180:183], v[212:215], v[124:127]
	v_mfma_f32_16x16x32_bf16 v[120:123], v[184:187], v[212:215], v[120:123]
	v_mfma_f32_16x16x32_bf16 v[140:143], v[188:191], v[212:215], v[140:143]
	s_waitcnt lgkmcnt(2)
	v_mfma_f32_16x16x32_bf16 v[136:139], v[176:179], v[192:195], v[136:139]
	ds_read_b128 v[212:215], v199 offset:47104
	s_waitcnt vmcnt(12)
	v_cvt_pk_bf16_f32 v31, v30, v31
	v_cvt_pk_bf16_f32 v30, v28, v29
	v_mfma_f32_16x16x32_bf16 v[128:131], v[180:183], v[192:195], v[128:131]
	ds_write_b64 v198, v[30:31] offset:8704
	v_mfma_f32_16x16x32_bf16 v[116:119], v[184:187], v[192:195], v[116:119]
	v_mfma_f32_16x16x32_bf16 v[112:115], v[188:191], v[192:195], v[112:115]
	s_add_i32 s39, s9, 0xfffc0000
	buffer_load_dwordx4 v[28:31], v197, s[24:27], s39 offen
	s_waitcnt lgkmcnt(2)
	v_mfma_f32_16x16x32_bf16 v[100:103], v[176:179], v[208:211], v[100:103]
	ds_read_b128 v[192:195], v199 offset:49152
	v_mfma_f32_16x16x32_bf16 v[92:95], v[180:183], v[208:211], v[92:95]
	v_mfma_f32_16x16x32_bf16 v[88:91], v[184:187], v[208:211], v[88:91]
	v_mfma_f32_16x16x32_bf16 v[108:111], v[188:191], v[208:211], v[108:111]
	s_waitcnt lgkmcnt(2)
	v_mfma_f32_16x16x32_bf16 v[104:107], v[176:179], v[212:215], v[104:107]
	ds_read_b128 v[208:211], v199 offset:51200
	s_waitcnt vmcnt(12)
	v_cvt_pk_bf16_f32 v19, v18, v19
	v_cvt_pk_bf16_f32 v18, v16, v17
	v_mfma_f32_16x16x32_bf16 v[96:99], v[180:183], v[212:215], v[96:99]
	ds_write_b64 v198, v[18:19] offset:17408
	v_mfma_f32_16x16x32_bf16 v[84:87], v[184:187], v[212:215], v[84:87]
	v_mfma_f32_16x16x32_bf16 v[80:83], v[188:191], v[212:215], v[80:83]
	s_add_i32 s43, s9, 0xfffe0000
	buffer_load_dwordx4 v[16:19], v197, s[24:27], s43 offen
	s_waitcnt lgkmcnt(2)
; #define G_ENDTILE(VM) do { asm volatile("s_waitcnt vmcnt(" #VM ")" ::: "memory"); \
;         asm volatile("s_waitcnt lgkmcnt(0)" ::: "memory"); __builtin_amdgcn_s_barrier(); asm volatile("" ::: "memory"); } while (0)
;     ...
;         for (int t = 0; t < nt - 2; t += 2) {
;             G_TILE(G_A0, G_B0, true, G_B1, G_A1, t + 1, true, t + 2, (void)0);
;             G_ENDTILE(8);
;             G_TILE(G_A1, G_B1, true, G_B0, G_A0, t + 2, true, t + 3, (void)0);
;             G_ENDTILE(8);
;         }
	v_mfma_f32_16x16x32_bf16 v[72:75], v[176:179], v[192:195], v[72:75]
	ds_read_b128 v[212:215], v199 offset:53248
	v_mfma_f32_16x16x32_bf16 v[64:67], v[180:183], v[192:195], v[64:67]
	v_mfma_f32_16x16x32_bf16 v[60:63], v[184:187], v[192:195], v[60:63]
	v_mfma_f32_16x16x32_bf16 v[76:79], v[188:191], v[192:195], v[76:79]
	s_waitcnt lgkmcnt(2)
	v_mfma_f32_16x16x32_bf16 v[68:71], v[176:179], v[208:211], v[68:71]
	ds_read_b128 v[192:195], v199 offset:37888
	s_waitcnt vmcnt(12)
	v_cvt_pk_bf16_f32 v27, v26, v27
	v_cvt_pk_bf16_f32 v26, v24, v25
	v_mfma_f32_16x16x32_bf16 v[56:59], v[180:183], v[208:211], v[56:59]
	ds_write_b64 v198, v[26:27] offset:26112
	v_mfma_f32_16x16x32_bf16 v[52:55], v[184:187], v[208:211], v[52:55]
	v_mfma_f32_16x16x32_bf16 v[48:51], v[188:191], v[208:211], v[48:51]
	buffer_load_dwordx4 v[24:27], v197, s[24:27], s9 offen
	s_waitcnt lgkmcnt(2)
	v_mfma_f32_16x16x32_bf16 v[44:47], v[176:179], v[212:215], v[44:47]
	ds_read_b128 v[176:179], v199 offset:39936
	v_mfma_f32_16x16x32_bf16 v[40:43], v[180:183], v[212:215], v[40:43]
	ds_read_b64_tr_b16 v[244:245], v205 offset:52224
	ds_read_b64_tr_b16 v[248:249], v205 offset:52256
	ds_read_b64_tr_b16 v[216:217], v205 offset:52288
	ds_read_b64_tr_b16 v[220:221], v205 offset:52320
	ds_read_b64_tr_b16 v[246:247], v206 offset:52224
	ds_read_b64_tr_b16 v[250:251], v206 offset:52256
	ds_read_b64_tr_b16 v[218:219], v206 offset:52288
	ds_read_b64_tr_b16 v[222:223], v206 offset:52320
	v_mfma_f32_16x16x32_bf16 v[36:39], v[184:187], v[212:215], v[36:39]
	v_mfma_f32_16x16x32_bf16 v[32:35], v[188:191], v[212:215], v[32:35]
	s_waitcnt lgkmcnt(3)
	v_mfma_f32_16x16x32_bf16 v[172:175], v[244:247], v[192:195], v[172:175]
	ds_read_b128 v[184:187], v199 offset:41984
	s_waitcnt vmcnt(12)
	v_cvt_pk_bf16_f32 v15, v14, v15
	v_cvt_pk_bf16_f32 v14, v12, v13
	s_waitcnt lgkmcnt(3)
	v_mfma_f32_16x16x32_bf16 v[168:171], v[248:251], v[192:195], v[168:171]
	ds_write_b64 v198, v[14:15] offset:256
	s_waitcnt lgkmcnt(3)
	v_mfma_f32_16x16x32_bf16 v[164:167], v[216:219], v[192:195], v[164:167]
	s_waitcnt lgkmcnt(2)
	v_mfma_f32_16x16x32_bf16 v[160:163], v[220:223], v[192:195], v[160:163]
	buffer_load_dwordx4 v[12:15], v197, s[16:19], s38 offen
	v_mfma_f32_16x16x32_bf16 v[156:159], v[244:247], v[176:179], v[156:159]
	ds_read_b128 v[188:191], v199 offset:44032
	v_mfma_f32_16x16x32_bf16 v[152:155], v[248:251], v[176:179], v[152:155]
	v_mfma_f32_16x16x32_bf16 v[148:151], v[216:219], v[176:179], v[148:151]
	v_mfma_f32_16x16x32_bf16 v[144:147], v[220:223], v[176:179], v[144:147]
	s_waitcnt lgkmcnt(2)
	v_mfma_f32_16x16x32_bf16 v[132:135], v[244:247], v[184:187], v[132:135]
	ds_read_b128 v[176:179], v199 offset:46080
	s_waitcnt vmcnt(12)
	v_cvt_pk_bf16_f32 v7, v6, v7
	v_cvt_pk_bf16_f32 v6, v4, v5
	v_mfma_f32_16x16x32_bf16 v[124:127], v[248:251], v[184:187], v[124:127]
	ds_write_b64 v198, v[6:7] offset:8960
	v_mfma_f32_16x16x32_bf16 v[120:123], v[216:219], v[184:187], v[120:123]
	v_mfma_f32_16x16x32_bf16 v[140:143], v[220:223], v[184:187], v[140:143]
	buffer_load_dwordx4 v[4:7], v197, s[16:19], s39 offen
	s_waitcnt lgkmcnt(2)
	v_mfma_f32_16x16x32_bf16 v[136:139], v[244:247], v[188:191], v[136:139]
	ds_read_b128 v[184:187], v199 offset:48128
	v_mfma_f32_16x16x32_bf16 v[128:131], v[248:251], v[188:191], v[128:131]
	v_mfma_f32_16x16x32_bf16 v[116:119], v[216:219], v[188:191], v[116:119]
	v_mfma_f32_16x16x32_bf16 v[112:115], v[220:223], v[188:191], v[112:115]
	s_waitcnt lgkmcnt(2)
	v_mfma_f32_16x16x32_bf16 v[100:103], v[244:247], v[176:179], v[100:103]
	ds_read_b128 v[188:191], v199 offset:50176
	s_waitcnt vmcnt(12)
	v_cvt_pk_bf16_f32 v3, v2, v3
	v_cvt_pk_bf16_f32 v2, v0, v1
	v_mfma_f32_16x16x32_bf16 v[92:95], v[248:251], v[176:179], v[92:95]
	ds_write_b64 v198, v[2:3] offset:17664
	v_mfma_f32_16x16x32_bf16 v[88:91], v[216:219], v[176:179], v[88:91]
	v_mfma_f32_16x16x32_bf16 v[108:111], v[220:223], v[176:179], v[108:111]
	buffer_load_dwordx4 v[0:3], v197, s[16:19], s43 offen
	s_waitcnt lgkmcnt(2)
	v_mfma_f32_16x16x32_bf16 v[104:107], v[244:247], v[184:187], v[104:107]
	ds_read_b128 v[176:179], v199 offset:52224
	v_mfma_f32_16x16x32_bf16 v[96:99], v[248:251], v[184:187], v[96:99]
	v_mfma_f32_16x16x32_bf16 v[84:87], v[216:219], v[184:187], v[84:87]
	v_mfma_f32_16x16x32_bf16 v[80:83], v[220:223], v[184:187], v[80:83]
	s_waitcnt lgkmcnt(2)
	v_mfma_f32_16x16x32_bf16 v[72:75], v[244:247], v[188:191], v[72:75]
	ds_read_b128 v[252:255], v199 offset:54272
	s_waitcnt vmcnt(12)
	v_cvt_pk_bf16_f32 v11, v10, v11
	v_cvt_pk_bf16_f32 v10, v8, v9
	v_mfma_f32_16x16x32_bf16 v[64:67], v[248:251], v[188:191], v[64:67]
	ds_write_b64 v198, v[10:11] offset:26368
	v_mfma_f32_16x16x32_bf16 v[60:63], v[216:219], v[188:191], v[60:63]
	v_mfma_f32_16x16x32_bf16 v[76:79], v[220:223], v[188:191], v[76:79]
	buffer_load_dwordx4 v[8:11], v197, s[16:19], s9 offen
	s_waitcnt lgkmcnt(2)
	v_mfma_f32_16x16x32_bf16 v[68:71], v[244:247], v[176:179], v[68:71]
	v_mfma_f32_16x16x32_bf16 v[56:59], v[248:251], v[176:179], v[56:59]
	v_mfma_f32_16x16x32_bf16 v[52:55], v[216:219], v[176:179], v[52:55]
	v_mfma_f32_16x16x32_bf16 v[48:51], v[220:223], v[176:179], v[48:51]
	s_waitcnt lgkmcnt(1)
	s_waitcnt vmcnt(8)
	s_waitcnt lgkmcnt(0)
	s_barrier
	s_add_i32 s8, s8, 2
	s_add_i32 s9, s9, 0x100000
	s_addk_i32 s36, 0x100
	s_cmp_ge_i32 s8, s84
	s_cbranch_scc0 .LBB0_863
	v_mfma_f32_16x16x32_bf16 v[44:47], v[244:247], v[252:255], v[44:47]
	v_mfma_f32_16x16x32_bf16 v[40:43], v[248:251], v[252:255], v[40:43]
	v_mfma_f32_16x16x32_bf16 v[36:39], v[216:219], v[252:255], v[36:39]
	v_mfma_f32_16x16x32_bf16 v[32:35], v[220:223], v[252:255], v[32:35]
	s_branch .LBB0_865

;     ...
;     for (int ui = 0;; ++ui) {
; #pragma unroll
;         for (int m = 0; m < MF; ++m)
; #pragma unroll
;             for (int n = 0; n < 4; ++n) acc[m][n] = (f32x4){0.f, 0.f, 0.f, 0.f};
;         for (int t = 0; t < nt - 2; t += 2) {
;             G_TILE(G_A0, G_B0, true, G_B1, G_A1, t + 1, true, t + 2, (void)0);
.LBB0_897:
	s_andn2_b64 vcc, exec, s[28:29]
	v_mov_b32_e32 v159, 0
	s_cbranch_vccnz .LBB0_900
	v_mov_b32_e32 v32, 0
	s_mov_b32 s12, 0
	s_mov_b32 s13, 0x1e0000
	s_movk_i32 s45, 0x100
	v_mov_b32_e32 v33, v32
	v_mov_b32_e32 v34, v32
	s_waitcnt lgkmcnt(0)
	v_mov_b32_e32 v35, v32
	v_mov_b32_e32 v36, v32
	v_mov_b32_e32 v37, v32
	v_mov_b32_e32 v38, v32
	v_mov_b32_e32 v39, v32
	v_mov_b32_e32 v40, v32
	v_mov_b32_e32 v41, v32
	v_mov_b32_e32 v42, v32
	v_mov_b32_e32 v43, v32
	v_mov_b32_e32 v44, v32
	v_mov_b32_e32 v45, v32
	v_mov_b32_e32 v46, v32
	v_mov_b32_e32 v47, v32
	v_mov_b32_e32 v48, v32
	v_mov_b32_e32 v49, v32
	v_mov_b32_e32 v50, v32
	v_mov_b32_e32 v51, v32
	v_mov_b32_e32 v52, v32
	v_mov_b32_e32 v53, v32
	v_mov_b32_e32 v54, v32
	v_mov_b32_e32 v55, v32
	v_mov_b32_e32 v56, v32
	v_mov_b32_e32 v57, v32
	v_mov_b32_e32 v58, v32
	v_mov_b32_e32 v59, v32
	v_mov_b32_e32 v60, v32
	v_mov_b32_e32 v61, v32
	v_mov_b32_e32 v62, v32
	v_mov_b32_e32 v63, v32
	v_mov_b32_e32 v64, v32
	v_mov_b32_e32 v65, v32
	v_mov_b32_e32 v66, v32
	v_mov_b32_e32 v67, v32
	v_mov_b32_e32 v68, v32
	v_mov_b32_e32 v69, v32
	v_mov_b32_e32 v70, v32
	v_mov_b32_e32 v71, v32
	v_mov_b32_e32 v72, v32
	v_mov_b32_e32 v73, v32
	v_mov_b32_e32 v74, v32
	v_mov_b32_e32 v75, v32
	v_mov_b32_e32 v76, v32
	v_mov_b32_e32 v77, v32
	v_mov_b32_e32 v78, v32
	v_mov_b32_e32 v79, v32
	v_mov_b32_e32 v80, v32
	v_mov_b32_e32 v81, v32
	v_mov_b32_e32 v82, v32
	v_mov_b32_e32 v83, v32
	v_mov_b32_e32 v84, v32
	v_mov_b32_e32 v85, v32
	v_mov_b32_e32 v86, v32
	v_mov_b32_e32 v87, v32
	v_mov_b32_e32 v88, v32
	v_mov_b32_e32 v89, v32
	v_mov_b32_e32 v90, v32
	v_mov_b32_e32 v91, v32
	v_mov_b32_e32 v92, v32
	v_mov_b32_e32 v93, v32
	v_mov_b32_e32 v94, v32
	v_mov_b32_e32 v95, v32
	v_mov_b32_e32 v96, v32
	v_mov_b32_e32 v97, v32
	v_mov_b32_e32 v98, v32
	v_mov_b32_e32 v99, v32
	v_mov_b32_e32 v100, v32
	v_mov_b32_e32 v101, v32
	v_mov_b32_e32 v102, v32
	v_mov_b32_e32 v103, v32
	v_mov_b32_e32 v104, v32
	v_mov_b32_e32 v105, v32
	v_mov_b32_e32 v106, v32
	v_mov_b32_e32 v107, v32
	v_mov_b32_e32 v108, v32
	v_mov_b32_e32 v109, v32
	v_mov_b32_e32 v110, v32
	v_mov_b32_e32 v111, v32
	v_mov_b32_e32 v112, v32
	v_mov_b32_e32 v113, v32
	v_mov_b32_e32 v114, v32
	v_mov_b32_e32 v115, v32
	v_mov_b32_e32 v116, v32
	v_mov_b32_e32 v117, v32
	v_mov_b32_e32 v118, v32
	v_mov_b32_e32 v119, v32
	v_mov_b32_e32 v120, v32
	v_mov_b32_e32 v121, v32
	v_mov_b32_e32 v122, v32
	v_mov_b32_e32 v123, v32
	v_mov_b32_e32 v124, v32
	v_mov_b32_e32 v125, v32
	v_mov_b32_e32 v126, v32
	v_mov_b32_e32 v127, v32
	v_mov_b32_e32 v128, v32
	v_mov_b32_e32 v129, v32
	v_mov_b32_e32 v130, v32
	v_mov_b32_e32 v131, v32
	v_mov_b32_e32 v132, v32
	v_mov_b32_e32 v133, v32
	v_mov_b32_e32 v134, v32
	v_mov_b32_e32 v135, v32
	v_mov_b32_e32 v136, v32
	v_mov_b32_e32 v137, v32
	v_mov_b32_e32 v138, v32
	v_mov_b32_e32 v139, v32
	v_mov_b32_e32 v140, v32
	v_mov_b32_e32 v141, v32
	v_mov_b32_e32 v142, v32
	v_mov_b32_e32 v143, v32
	v_mov_b32_e32 v144, v32
	v_mov_b32_e32 v145, v32
	v_mov_b32_e32 v146, v32
	v_mov_b32_e32 v147, v32
	v_mov_b32_e32 v148, v32
	v_mov_b32_e32 v149, v32
	v_mov_b32_e32 v150, v32
	v_mov_b32_e32 v151, v32
	v_mov_b32_e32 v152, v32
	v_mov_b32_e32 v153, v32
	v_mov_b32_e32 v154, v32
	v_mov_b32_e32 v155, v32
	v_mov_b32_e32 v156, v32
	v_mov_b32_e32 v157, v32
	v_mov_b32_e32 v158, v32
	v_mov_b32_e32 v159, v32
	v_mov_b32_e32 v202, 0
	v_mov_b32_e32 v203, 0
	v_mov_b32_e32 v204, 0
	v_mov_b32_e32 v205, 0
	v_mov_b32_e32 v206, 0
	v_mov_b32_e32 v207, 0
	v_mov_b32_e32 v208, 0
	v_mov_b32_e32 v209, 0
	v_mov_b32_e32 v244, 0
	v_mov_b32_e32 v245, 0
	v_mov_b32_e32 v246, 0
	v_mov_b32_e32 v247, 0
	v_mov_b32_e32 v248, 0
	v_mov_b32_e32 v249, 0
	v_mov_b32_e32 v250, 0
	v_mov_b32_e32 v251, 0
	v_mov_b32_e32 v252, 0
	v_mov_b32_e32 v253, 0
	v_mov_b32_e32 v254, 0
	v_mov_b32_e32 v255, 0
.LBB0_899:
	s_mov_b32 m0, s64
	s_add_i32 s69, s45, 0xffffff80
	ds_read_b64_tr_b16 v[170:171], v166
	ds_read_b64_tr_b16 v[172:173], v167
	ds_read_b64_tr_b16 v[176:177], v167 offset:32
	ds_read_b128 v[178:181], v162
	ds_read_b64_tr_b16 v[174:175], v166 offset:32
	ds_read_b64_tr_b16 v[182:183], v166 offset:64
	ds_read_b64_tr_b16 v[186:187], v166 offset:96
	ds_read_b64_tr_b16 v[184:185], v167 offset:64
	ds_read_b64_tr_b16 v[188:189], v167 offset:96
	ds_read_b128 v[190:193], v162 offset:2048
	ds_read_b128 v[198:201], v162 offset:4096
	buffer_load_dwordx4 v163, s[20:23], s69 offen lds
	s_mov_b32 m0, s63
	v_mfma_f32_16x16x32_bf16 v[44:47], v[244:247], v[252:255], v[44:47]
	v_mfma_f32_16x16x32_bf16 v[40:43], v[248:251], v[252:255], v[40:43]
	v_mfma_f32_16x16x32_bf16 v[36:39], v[202:205], v[252:255], v[36:39]
	v_mfma_f32_16x16x32_bf16 v[32:35], v[206:209], v[252:255], v[32:35]
	s_waitcnt lgkmcnt(7)
	v_mfma_f32_16x16x32_bf16 v[156:159], v[170:173], v[178:181], v[156:159]
	buffer_load_dwordx4 v165, s[20:23], s69 offen lds
	s_mov_b32 m0, s62
	s_nop 0
	buffer_load_dwordx4 v164, s[20:23], s69 offen lds
	s_mov_b32 m0, s31
	s_waitcnt lgkmcnt(6)
	v_mfma_f32_16x16x32_bf16 v[152:155], v[174:177], v[178:181], v[152:155]
	buffer_load_dwordx4 v168, s[20:23], s69 offen lds
	s_add_i32 s69, s13, 0xfff20000
	s_waitcnt lgkmcnt(3)
	v_mfma_f32_16x16x32_bf16 v[148:151], v[182:185], v[178:181], v[148:151]
	s_waitcnt lgkmcnt(2)
	v_mfma_f32_16x16x32_bf16 v[144:147], v[186:189], v[178:181], v[144:147]
	s_waitcnt lgkmcnt(1)
	v_mfma_f32_16x16x32_bf16 v[140:143], v[170:173], v[190:193], v[140:143]
	ds_read_b128 v[178:181], v162 offset:6144
	s_waitcnt vmcnt(11)
	v_cvt_pk_bf16_f32 v15, v14, v15
	v_cvt_pk_bf16_f32 v14, v12, v13
	v_mfma_f32_16x16x32_bf16 v[136:139], v[174:177], v[190:193], v[136:139]
	ds_write_b64 v161, v[14:15] offset:34816
	v_mfma_f32_16x16x32_bf16 v[132:135], v[182:185], v[190:193], v[132:135]
	v_mfma_f32_16x16x32_bf16 v[128:131], v[186:189], v[190:193], v[128:131]
	buffer_load_dwordx4 v[12:15], v160, s[24:27], s69 offen
	s_waitcnt lgkmcnt(2)
	v_mfma_f32_16x16x32_bf16 v[124:127], v[170:173], v[198:201], v[124:127]
	ds_read_b128 v[190:193], v162 offset:8192
	v_mfma_f32_16x16x32_bf16 v[120:123], v[174:177], v[198:201], v[120:123]
	v_mfma_f32_16x16x32_bf16 v[116:119], v[182:185], v[198:201], v[116:119]
	v_mfma_f32_16x16x32_bf16 v[112:115], v[186:189], v[198:201], v[112:115]
	s_waitcnt lgkmcnt(2)
	v_mfma_f32_16x16x32_bf16 v[108:111], v[170:173], v[178:181], v[108:111]
	ds_read_b128 v[198:201], v162 offset:10240
	s_waitcnt vmcnt(11)
	v_cvt_pk_bf16_f32 v3, v2, v3
	v_cvt_pk_bf16_f32 v2, v0, v1
	v_mfma_f32_16x16x32_bf16 v[104:107], v[174:177], v[178:181], v[104:107]
	ds_write_b64 v161, v[2:3] offset:43520
	v_mfma_f32_16x16x32_bf16 v[100:103], v[182:185], v[178:181], v[100:103]
	v_mfma_f32_16x16x32_bf16 v[96:99], v[186:189], v[178:181], v[96:99]
	s_add_i32 s74, s13, 0xfff40000
	buffer_load_dwordx4 v[0:3], v160, s[24:27], s74 offen
	s_waitcnt lgkmcnt(2)
	v_mfma_f32_16x16x32_bf16 v[92:95], v[170:173], v[190:193], v[92:95]
	ds_read_b128 v[178:181], v162 offset:12288
	v_mfma_f32_16x16x32_bf16 v[88:91], v[174:177], v[190:193], v[88:91]
	v_mfma_f32_16x16x32_bf16 v[84:87], v[182:185], v[190:193], v[84:87]
	v_mfma_f32_16x16x32_bf16 v[80:83], v[186:189], v[190:193], v[80:83]
	s_waitcnt lgkmcnt(2)
	v_mfma_f32_16x16x32_bf16 v[76:79], v[170:173], v[198:201], v[76:79]
	ds_read_b128 v[190:193], v162 offset:14336
	s_waitcnt vmcnt(11)
	v_cvt_pk_bf16_f32 v31, v30, v31
	v_cvt_pk_bf16_f32 v30, v28, v29
	v_mfma_f32_16x16x32_bf16 v[72:75], v[174:177], v[198:201], v[72:75]
	ds_write_b64 v161, v[30:31] offset:52224
	v_mfma_f32_16x16x32_bf16 v[68:71], v[182:185], v[198:201], v[68:71]
	v_mfma_f32_16x16x32_bf16 v[64:67], v[186:189], v[198:201], v[64:67]
	s_add_i32 s75, s13, 0xfff60000
	buffer_load_dwordx4 v[28:31], v160, s[24:27], s75 offen
	s_waitcnt lgkmcnt(2)
	v_mfma_f32_16x16x32_bf16 v[60:63], v[170:173], v[178:181], v[60:63]
	ds_read_b128 v[198:201], v162 offset:1024
	v_mfma_f32_16x16x32_bf16 v[56:59], v[174:177], v[178:181], v[56:59]
	v_mfma_f32_16x16x32_bf16 v[52:55], v[182:185], v[178:181], v[52:55]
	v_mfma_f32_16x16x32_bf16 v[48:51], v[186:189], v[178:181], v[48:51]
	s_waitcnt lgkmcnt(2)
	v_mfma_f32_16x16x32_bf16 v[44:47], v[170:173], v[190:193], v[44:47]
	ds_read_b128 v[170:173], v162 offset:3072
	s_waitcnt vmcnt(11)
	v_cvt_pk_bf16_f32 v27, v26, v27
	v_cvt_pk_bf16_f32 v26, v24, v25
	v_mfma_f32_16x16x32_bf16 v[40:43], v[174:177], v[190:193], v[40:43]
	ds_read_b64_tr_b16 v[244:245], v166 offset:17408
	ds_read_b64_tr_b16 v[248:249], v166 offset:17440
	ds_read_b64_tr_b16 v[202:203], v166 offset:17472
	ds_read_b64_tr_b16 v[206:207], v166 offset:17504
	ds_read_b64_tr_b16 v[246:247], v167 offset:17408
	ds_read_b64_tr_b16 v[250:251], v167 offset:17440
	ds_read_b64_tr_b16 v[204:205], v167 offset:17472
	ds_read_b64_tr_b16 v[208:209], v167 offset:17504
	ds_write_b64 v161, v[26:27] offset:60928
	v_mfma_f32_16x16x32_bf16 v[36:39], v[182:185], v[190:193], v[36:39]
	v_mfma_f32_16x16x32_bf16 v[32:35], v[186:189], v[190:193], v[32:35]
	s_add_i32 s76, s13, 0xfff80000
	buffer_load_dwordx4 v[24:27], v160, s[24:27], s76 offen
	s_waitcnt lgkmcnt(4)
	v_mfma_f32_16x16x32_bf16 v[156:159], v[244:247], v[198:201], v[156:159]
	ds_read_b128 v[182:185], v162 offset:5120
	s_waitcnt lgkmcnt(4)
	v_mfma_f32_16x16x32_bf16 v[152:155], v[248:251], v[198:201], v[152:155]
	s_waitcnt lgkmcnt(3)
	v_mfma_f32_16x16x32_bf16 v[148:151], v[202:205], v[198:201], v[148:151]
	s_waitcnt lgkmcnt(2)
	v_mfma_f32_16x16x32_bf16 v[144:147], v[206:209], v[198:201], v[144:147]
	v_mfma_f32_16x16x32_bf16 v[140:143], v[244:247], v[170:173], v[140:143]
	ds_read_b128 v[186:189], v162 offset:7168
	s_waitcnt vmcnt(11)
	v_cvt_pk_bf16_f32 v23, v22, v23
	v_cvt_pk_bf16_f32 v22, v20, v21
	v_mfma_f32_16x16x32_bf16 v[136:139], v[248:251], v[170:173], v[136:139]
	ds_write_b64 v161, v[22:23] offset:35072
	v_mfma_f32_16x16x32_bf16 v[132:135], v[202:205], v[170:173], v[132:135]
	v_mfma_f32_16x16x32_bf16 v[128:131], v[206:209], v[170:173], v[128:131]
	buffer_load_dwordx4 v[20:23], v160, s[16:19], s69 offen
	s_waitcnt lgkmcnt(2)
	v_mfma_f32_16x16x32_bf16 v[124:127], v[244:247], v[182:185], v[124:127]
	ds_read_b128 v[170:173], v162 offset:9216
	v_mfma_f32_16x16x32_bf16 v[120:123], v[248:251], v[182:185], v[120:123]
	v_mfma_f32_16x16x32_bf16 v[116:119], v[202:205], v[182:185], v[116:119]
	v_mfma_f32_16x16x32_bf16 v[112:115], v[206:209], v[182:185], v[112:115]
	s_waitcnt lgkmcnt(2)
	v_mfma_f32_16x16x32_bf16 v[108:111], v[244:247], v[186:189], v[108:111]
	ds_read_b128 v[182:185], v162 offset:11264
	s_waitcnt vmcnt(11)
	v_cvt_pk_bf16_f32 v7, v6, v7
	v_cvt_pk_bf16_f32 v6, v4, v5
	v_mfma_f32_16x16x32_bf16 v[104:107], v[248:251], v[186:189], v[104:107]
	ds_write_b64 v161, v[6:7] offset:43776
	v_mfma_f32_16x16x32_bf16 v[100:103], v[202:205], v[186:189], v[100:103]
	v_mfma_f32_16x16x32_bf16 v[96:99], v[206:209], v[186:189], v[96:99]
	buffer_load_dwordx4 v[4:7], v160, s[16:19], s74 offen
	s_waitcnt lgkmcnt(2)
	v_mfma_f32_16x16x32_bf16 v[92:95], v[244:247], v[170:173], v[92:95]
	ds_read_b128 v[186:189], v162 offset:13312
	v_mfma_f32_16x16x32_bf16 v[88:91], v[248:251], v[170:173], v[88:91]
	v_mfma_f32_16x16x32_bf16 v[84:87], v[202:205], v[170:173], v[84:87]
	v_mfma_f32_16x16x32_bf16 v[80:83], v[206:209], v[170:173], v[80:83]
	s_waitcnt lgkmcnt(2)
	v_mfma_f32_16x16x32_bf16 v[76:79], v[244:247], v[182:185], v[76:79]
	ds_read_b128 v[252:255], v162 offset:15360
	s_waitcnt vmcnt(11)
	v_cvt_pk_bf16_f32 v11, v10, v11
	v_cvt_pk_bf16_f32 v10, v8, v9
	v_mfma_f32_16x16x32_bf16 v[72:75], v[248:251], v[182:185], v[72:75]
	ds_write_b64 v161, v[10:11] offset:52480
	v_mfma_f32_16x16x32_bf16 v[68:71], v[202:205], v[182:185], v[68:71]
	v_mfma_f32_16x16x32_bf16 v[64:67], v[206:209], v[182:185], v[64:67]
	buffer_load_dwordx4 v[8:11], v160, s[16:19], s75 offen
	s_waitcnt lgkmcnt(2)
	v_mfma_f32_16x16x32_bf16 v[60:63], v[244:247], v[186:189], v[60:63]
	v_mfma_f32_16x16x32_bf16 v[56:59], v[248:251], v[186:189], v[56:59]
	v_mfma_f32_16x16x32_bf16 v[52:55], v[202:205], v[186:189], v[52:55]
	v_mfma_f32_16x16x32_bf16 v[48:51], v[206:209], v[186:189], v[48:51]
	s_waitcnt lgkmcnt(1)
	s_waitcnt vmcnt(11)
	v_cvt_pk_bf16_f32 v19, v18, v19
	v_cvt_pk_bf16_f32 v18, v16, v17
	ds_write_b64 v161, v[18:19] offset:61184
	buffer_load_dwordx4 v[16:19], v160, s[16:19], s76 offen
	s_waitcnt vmcnt(8)
	s_mov_b32 m0, s56
	s_waitcnt lgkmcnt(0)
	s_barrier
;     ...
;             G_TILE(G_A1, G_B1, true, G_B0, G_A0, t + 2, true, t + 3, (void)0);
	ds_read_b64_tr_b16 v[170:171], v166 offset:34816
	ds_read_b64_tr_b16 v[172:173], v167 offset:34816
	ds_read_b64_tr_b16 v[176:177], v167 offset:34848
	ds_read_b128 v[178:181], v162 offset:32768
	ds_read_b64_tr_b16 v[174:175], v166 offset:34848
	ds_read_b64_tr_b16 v[182:183], v166 offset:34880
	ds_read_b64_tr_b16 v[186:187], v166 offset:34912
	ds_read_b64_tr_b16 v[184:185], v167 offset:34880
	ds_read_b64_tr_b16 v[188:189], v167 offset:34912
	ds_read_b128 v[190:193], v162 offset:34816
	ds_read_b128 v[198:201], v162 offset:36864
	buffer_load_dwordx4 v163, s[20:23], s45 offen lds
	s_mov_b32 m0, s57
	v_mfma_f32_16x16x32_bf16 v[44:47], v[244:247], v[252:255], v[44:47]
	v_mfma_f32_16x16x32_bf16 v[40:43], v[248:251], v[252:255], v[40:43]
	v_mfma_f32_16x16x32_bf16 v[36:39], v[202:205], v[252:255], v[36:39]
	v_mfma_f32_16x16x32_bf16 v[32:35], v[206:209], v[252:255], v[32:35]
	s_waitcnt lgkmcnt(7)
	v_mfma_f32_16x16x32_bf16 v[156:159], v[170:173], v[178:181], v[156:159]
	buffer_load_dwordx4 v165, s[20:23], s45 offen lds
	s_mov_b32 m0, s58
	s_add_i32 s69, s13, 0xfffa0000
	buffer_load_dwordx4 v164, s[20:23], s45 offen lds
	s_mov_b32 m0, s59
	s_waitcnt lgkmcnt(6)
	v_mfma_f32_16x16x32_bf16 v[152:155], v[174:177], v[178:181], v[152:155]
	buffer_load_dwordx4 v168, s[20:23], s45 offen lds
	s_waitcnt lgkmcnt(3)
	v_mfma_f32_16x16x32_bf16 v[148:151], v[182:185], v[178:181], v[148:151]
	s_waitcnt lgkmcnt(2)
	v_mfma_f32_16x16x32_bf16 v[144:147], v[186:189], v[178:181], v[144:147]
	s_waitcnt lgkmcnt(1)
	v_mfma_f32_16x16x32_bf16 v[140:143], v[170:173], v[190:193], v[140:143]
	ds_read_b128 v[178:181], v162 offset:38912
	s_waitcnt vmcnt(11)
	v_cvt_pk_bf16_f32 v15, v14, v15
	v_cvt_pk_bf16_f32 v14, v12, v13
	v_mfma_f32_16x16x32_bf16 v[136:139], v[174:177], v[190:193], v[136:139]
	ds_write_b64 v161, v[14:15]
	v_mfma_f32_16x16x32_bf16 v[132:135], v[182:185], v[190:193], v[132:135]
	v_mfma_f32_16x16x32_bf16 v[128:131], v[186:189], v[190:193], v[128:131]
	buffer_load_dwordx4 v[12:15], v160, s[24:27], s69 offen
	s_waitcnt lgkmcnt(2)
	v_mfma_f32_16x16x32_bf16 v[124:127], v[170:173], v[198:201], v[124:127]
	ds_read_b128 v[190:193], v162 offset:40960
	v_mfma_f32_16x16x32_bf16 v[120:123], v[174:177], v[198:201], v[120:123]
	v_mfma_f32_16x16x32_bf16 v[116:119], v[182:185], v[198:201], v[116:119]
	v_mfma_f32_16x16x32_bf16 v[112:115], v[186:189], v[198:201], v[112:115]
	s_waitcnt lgkmcnt(2)
	v_mfma_f32_16x16x32_bf16 v[108:111], v[170:173], v[178:181], v[108:111]
	ds_read_b128 v[198:201], v162 offset:43008
	s_waitcnt vmcnt(11)
	v_cvt_pk_bf16_f32 v3, v2, v3
	v_cvt_pk_bf16_f32 v2, v0, v1
	v_mfma_f32_16x16x32_bf16 v[104:107], v[174:177], v[178:181], v[104:107]
	ds_write_b64 v161, v[2:3] offset:8704
	v_mfma_f32_16x16x32_bf16 v[100:103], v[182:185], v[178:181], v[100:103]
	v_mfma_f32_16x16x32_bf16 v[96:99], v[186:189], v[178:181], v[96:99]
	s_add_i32 s74, s13, 0xfffc0000
	buffer_load_dwordx4 v[0:3], v160, s[24:27], s74 offen
	s_waitcnt lgkmcnt(2)
	v_mfma_f32_16x16x32_bf16 v[92:95], v[170:173], v[190:193], v[92:95]
	ds_read_b128 v[178:181], v162 offset:45056
	v_mfma_f32_16x16x32_bf16 v[88:91], v[174:177], v[190:193], v[88:91]
	v_mfma_f32_16x16x32_bf16 v[84:87], v[182:185], v[190:193], v[84:87]
	v_mfma_f32_16x16x32_bf16 v[80:83], v[186:189], v[190:193], v[80:83]
	s_waitcnt lgkmcnt(2)
	v_mfma_f32_16x16x32_bf16 v[76:79], v[170:173], v[198:201], v[76:79]
	ds_read_b128 v[190:193], v162 offset:47104
	s_waitcnt vmcnt(11)
	v_cvt_pk_bf16_f32 v31, v30, v31
	v_cvt_pk_bf16_f32 v30, v28, v29
	v_mfma_f32_16x16x32_bf16 v[72:75], v[174:177], v[198:201], v[72:75]
	ds_write_b64 v161, v[30:31] offset:17408
	v_mfma_f32_16x16x32_bf16 v[68:71], v[182:185], v[198:201], v[68:71]
	v_mfma_f32_16x16x32_bf16 v[64:67], v[186:189], v[198:201], v[64:67]
	s_add_i32 s75, s13, 0xfffe0000
	buffer_load_dwordx4 v[28:31], v160, s[24:27], s75 offen
	s_waitcnt lgkmcnt(2)
	v_mfma_f32_16x16x32_bf16 v[60:63], v[170:173], v[178:181], v[60:63]
	ds_read_b128 v[198:201], v162 offset:33792
	v_mfma_f32_16x16x32_bf16 v[56:59], v[174:177], v[178:181], v[56:59]
	v_mfma_f32_16x16x32_bf16 v[52:55], v[182:185], v[178:181], v[52:55]
	v_mfma_f32_16x16x32_bf16 v[48:51], v[186:189], v[178:181], v[48:51]
	s_waitcnt lgkmcnt(2)
	v_mfma_f32_16x16x32_bf16 v[44:47], v[170:173], v[190:193], v[44:47]
	ds_read_b128 v[170:173], v162 offset:35840
	s_waitcnt vmcnt(11)
; #define G_DMA_A(kt, AO) do { G_DMA1(kt, AO, 0); G_DMA1(kt, AO, 1); G_DMA1(kt, AO, 2); G_DMA1(kt, AO, 3); if (MF == 9) G_DMA5(kt, AO); } while (0)
; #define G_ISSUE_B(kt) do { const unsigned _sb = (unsigned)(kt) * 4u * kstepB; \
;         _Pragma("unroll") for (int _i = 0; _i < 8; ++_i) sb[_i] = bload16(_i < 4 ? rsB0 : rsB1, vob, _sb + (_i & 3) * kstepB); } while (0)
; #define G_WRITE_B(BO) do { \
;         _Pragma("unroll") for (int _i = 0; _i < 8; ++_i) *(LAS u32x2*)(b_wr + (BO) + (_i & 3) * (16 * G_BSTRIDE) + (_i >> 2) * SLAB1) = pack4(__builtin_bit_cast(f32x4, sb[_i])); } while (0)
; #define G_ENDTILE(VM) do { asm volatile("s_waitcnt vmcnt(" #VM ")" ::: "memory"); \
;         asm volatile("s_waitcnt lgkmcnt(0)" ::: "memory"); __builtin_amdgcn_s_barrier(); asm volatile("" ::: "memory"); } while (0)
;     ...
;     __builtin_amdgcn_s_barrier();
;     G_DMA_A(0, G_A0); G_ISSUE_B(0); G_WRITE_B(G_B0);
;     __builtin_amdgcn_sched_barrier(0);
;     G_ISSUE_B(1);
;     __builtin_amdgcn_sched_barrier(0);
;     G_ENDTILE(8);
;     for (int ui = 0;; ++ui) {
; #pragma unroll
;         for (int m = 0; m < MF; ++m)
; #pragma unroll
;             for (int n = 0; n < 4; ++n) acc[m][n] = (f32x4){0.f, 0.f, 0.f, 0.f};
;         for (int t = 0; t < nt - 2; t += 2) {
;             G_TILE(G_A0, G_B0, true, G_B1, G_A1, t + 1, true, t + 2, (void)0);
;             G_ENDTILE(8);
;             G_TILE(G_A1, G_B1, true, G_B0, G_A0, t + 2, true, t + 3, (void)0);
;             G_ENDTILE(8);
;         }
	v_cvt_pk_bf16_f32 v27, v26, v27
	v_cvt_pk_bf16_f32 v26, v24, v25
	v_mfma_f32_16x16x32_bf16 v[40:43], v[174:177], v[190:193], v[40:43]
	ds_read_b64_tr_b16 v[244:245], v166 offset:52224
	ds_read_b64_tr_b16 v[248:249], v166 offset:52256
	ds_read_b64_tr_b16 v[202:203], v166 offset:52288
	ds_read_b64_tr_b16 v[206:207], v166 offset:52320
	ds_read_b64_tr_b16 v[246:247], v167 offset:52224
	ds_read_b64_tr_b16 v[250:251], v167 offset:52256
	ds_read_b64_tr_b16 v[204:205], v167 offset:52288
	ds_read_b64_tr_b16 v[208:209], v167 offset:52320
	ds_write_b64 v161, v[26:27] offset:26112
	v_mfma_f32_16x16x32_bf16 v[36:39], v[182:185], v[190:193], v[36:39]
	v_mfma_f32_16x16x32_bf16 v[32:35], v[186:189], v[190:193], v[32:35]
	buffer_load_dwordx4 v[24:27], v160, s[24:27], s13 offen
	s_waitcnt lgkmcnt(4)
	v_mfma_f32_16x16x32_bf16 v[156:159], v[244:247], v[198:201], v[156:159]
	ds_read_b128 v[182:185], v162 offset:37888
	s_waitcnt lgkmcnt(4)
	v_mfma_f32_16x16x32_bf16 v[152:155], v[248:251], v[198:201], v[152:155]
	s_waitcnt lgkmcnt(3)
	v_mfma_f32_16x16x32_bf16 v[148:151], v[202:205], v[198:201], v[148:151]
	s_waitcnt lgkmcnt(2)
	v_mfma_f32_16x16x32_bf16 v[144:147], v[206:209], v[198:201], v[144:147]
	v_mfma_f32_16x16x32_bf16 v[140:143], v[244:247], v[170:173], v[140:143]
	ds_read_b128 v[186:189], v162 offset:39936
	s_waitcnt vmcnt(11)
	v_cvt_pk_bf16_f32 v23, v22, v23
	v_cvt_pk_bf16_f32 v22, v20, v21
	v_mfma_f32_16x16x32_bf16 v[136:139], v[248:251], v[170:173], v[136:139]
	ds_write_b64 v161, v[22:23] offset:256
	v_mfma_f32_16x16x32_bf16 v[132:135], v[202:205], v[170:173], v[132:135]
	v_mfma_f32_16x16x32_bf16 v[128:131], v[206:209], v[170:173], v[128:131]
	buffer_load_dwordx4 v[20:23], v160, s[16:19], s69 offen
	s_waitcnt lgkmcnt(2)
	v_mfma_f32_16x16x32_bf16 v[124:127], v[244:247], v[182:185], v[124:127]
	ds_read_b128 v[170:173], v162 offset:41984
	v_mfma_f32_16x16x32_bf16 v[120:123], v[248:251], v[182:185], v[120:123]
	v_mfma_f32_16x16x32_bf16 v[116:119], v[202:205], v[182:185], v[116:119]
	v_mfma_f32_16x16x32_bf16 v[112:115], v[206:209], v[182:185], v[112:115]
	s_waitcnt lgkmcnt(2)
	v_mfma_f32_16x16x32_bf16 v[108:111], v[244:247], v[186:189], v[108:111]
	ds_read_b128 v[182:185], v162 offset:44032
	s_waitcnt vmcnt(11)
	v_cvt_pk_bf16_f32 v7, v6, v7
	v_cvt_pk_bf16_f32 v6, v4, v5
	v_mfma_f32_16x16x32_bf16 v[104:107], v[248:251], v[186:189], v[104:107]
	ds_write_b64 v161, v[6:7] offset:8960
	v_mfma_f32_16x16x32_bf16 v[100:103], v[202:205], v[186:189], v[100:103]
	v_mfma_f32_16x16x32_bf16 v[96:99], v[206:209], v[186:189], v[96:99]
	buffer_load_dwordx4 v[4:7], v160, s[16:19], s74 offen
	s_waitcnt lgkmcnt(2)
	v_mfma_f32_16x16x32_bf16 v[92:95], v[244:247], v[170:173], v[92:95]
	ds_read_b128 v[186:189], v162 offset:46080
	v_mfma_f32_16x16x32_bf16 v[88:91], v[248:251], v[170:173], v[88:91]
	v_mfma_f32_16x16x32_bf16 v[84:87], v[202:205], v[170:173], v[84:87]
	v_mfma_f32_16x16x32_bf16 v[80:83], v[206:209], v[170:173], v[80:83]
	s_waitcnt lgkmcnt(2)
	v_mfma_f32_16x16x32_bf16 v[76:79], v[244:247], v[182:185], v[76:79]
	ds_read_b128 v[252:255], v162 offset:48128
	s_waitcnt vmcnt(11)
	v_cvt_pk_bf16_f32 v11, v10, v11
	v_cvt_pk_bf16_f32 v10, v8, v9
	v_mfma_f32_16x16x32_bf16 v[72:75], v[248:251], v[182:185], v[72:75]
	ds_write_b64 v161, v[10:11] offset:17664
	v_mfma_f32_16x16x32_bf16 v[68:71], v[202:205], v[182:185], v[68:71]
	v_mfma_f32_16x16x32_bf16 v[64:67], v[206:209], v[182:185], v[64:67]
	buffer_load_dwordx4 v[8:11], v160, s[16:19], s75 offen
	s_waitcnt lgkmcnt(2)
	v_mfma_f32_16x16x32_bf16 v[60:63], v[244:247], v[186:189], v[60:63]
	v_mfma_f32_16x16x32_bf16 v[56:59], v[248:251], v[186:189], v[56:59]
	v_mfma_f32_16x16x32_bf16 v[52:55], v[202:205], v[186:189], v[52:55]
	v_mfma_f32_16x16x32_bf16 v[48:51], v[206:209], v[186:189], v[48:51]
	s_waitcnt lgkmcnt(1)
	s_waitcnt vmcnt(11)
	v_cvt_pk_bf16_f32 v19, v18, v19
	v_cvt_pk_bf16_f32 v18, v16, v17
	ds_write_b64 v161, v[18:19] offset:26368
	buffer_load_dwordx4 v[16:19], v160, s[16:19], s13 offen
	s_waitcnt vmcnt(8)
	s_waitcnt lgkmcnt(0)
	s_barrier
	s_add_i32 s12, s12, 2
	s_add_i32 s13, s13, 0x100000
	s_addk_i32 s45, 0x100
	s_cmp_ge_i32 s12, s30
	s_cbranch_scc0 .LBB0_899
	v_mfma_f32_16x16x32_bf16 v[44:47], v[244:247], v[252:255], v[44:47]
	v_mfma_f32_16x16x32_bf16 v[40:43], v[248:251], v[252:255], v[40:43]
	v_mfma_f32_16x16x32_bf16 v[36:39], v[202:205], v[252:255], v[36:39]
	v_mfma_f32_16x16x32_bf16 v[32:35], v[206:209], v[252:255], v[32:35]
	s_branch .LBB0_901

;     ...
;         for (int m = 0; m < MF; ++m)
; #pragma unroll
;             for (int n = 0; n < 4; ++n) acc[m][n] = (f32x4){0.f, 0.f, 0.f, 0.f};
;         for (int t = 0; t < nt - 2; t += 2) {
;             G_TILE(G_A0, G_B0, true, G_B1, G_A1, t + 1, true, t + 2, (void)0);
.LBB0_1036:
	s_andn2_b64 vcc, exec, s[26:27]
	v_mov_b32_e32 v159, 0
	s_cbranch_vccnz .LBB0_1039
	v_mov_b32_e32 v32, 0
	s_mov_b32 s0, 0
	s_mov_b32 s1, 0x1e0000
	s_movk_i32 s4, 0x100
	v_mov_b32_e32 v33, v32
	v_mov_b32_e32 v34, v32
	v_mov_b32_e32 v35, v32
	v_mov_b32_e32 v36, v32
	v_mov_b32_e32 v37, v32
	v_mov_b32_e32 v38, v32
	v_mov_b32_e32 v39, v32
	v_mov_b32_e32 v40, v32
	v_mov_b32_e32 v41, v32
	v_mov_b32_e32 v42, v32
	v_mov_b32_e32 v43, v32
	v_mov_b32_e32 v44, v32
	v_mov_b32_e32 v45, v32
	v_mov_b32_e32 v46, v32
	v_mov_b32_e32 v47, v32
	v_mov_b32_e32 v48, v32
	v_mov_b32_e32 v49, v32
	v_mov_b32_e32 v50, v32
	v_mov_b32_e32 v51, v32
	v_mov_b32_e32 v52, v32
	v_mov_b32_e32 v53, v32
	v_mov_b32_e32 v54, v32
	v_mov_b32_e32 v55, v32
	v_mov_b32_e32 v56, v32
	v_mov_b32_e32 v57, v32
	v_mov_b32_e32 v58, v32
	v_mov_b32_e32 v59, v32
	v_mov_b32_e32 v60, v32
	v_mov_b32_e32 v61, v32
	v_mov_b32_e32 v62, v32
	v_mov_b32_e32 v63, v32
	v_mov_b32_e32 v64, v32
	v_mov_b32_e32 v65, v32
	v_mov_b32_e32 v66, v32
	v_mov_b32_e32 v67, v32
	v_mov_b32_e32 v68, v32
	v_mov_b32_e32 v69, v32
	v_mov_b32_e32 v70, v32
	v_mov_b32_e32 v71, v32
	v_mov_b32_e32 v72, v32
	v_mov_b32_e32 v73, v32
	v_mov_b32_e32 v74, v32
	v_mov_b32_e32 v75, v32
	v_mov_b32_e32 v76, v32
	v_mov_b32_e32 v77, v32
	v_mov_b32_e32 v78, v32
	v_mov_b32_e32 v79, v32
	v_mov_b32_e32 v80, v32
	v_mov_b32_e32 v81, v32
	v_mov_b32_e32 v82, v32
	v_mov_b32_e32 v83, v32
	v_mov_b32_e32 v84, v32
	v_mov_b32_e32 v85, v32
	v_mov_b32_e32 v86, v32
	v_mov_b32_e32 v87, v32
	v_mov_b32_e32 v88, v32
	v_mov_b32_e32 v89, v32
	v_mov_b32_e32 v90, v32
	v_mov_b32_e32 v91, v32
	v_mov_b32_e32 v92, v32
	v_mov_b32_e32 v93, v32
	v_mov_b32_e32 v94, v32
	v_mov_b32_e32 v95, v32
	v_mov_b32_e32 v96, v32
	v_mov_b32_e32 v97, v32
	v_mov_b32_e32 v98, v32
	v_mov_b32_e32 v99, v32
	v_mov_b32_e32 v100, v32
	v_mov_b32_e32 v101, v32
	v_mov_b32_e32 v102, v32
	v_mov_b32_e32 v103, v32
	v_mov_b32_e32 v104, v32
	v_mov_b32_e32 v105, v32
	v_mov_b32_e32 v106, v32
	v_mov_b32_e32 v107, v32
	v_mov_b32_e32 v108, v32
	v_mov_b32_e32 v109, v32
	v_mov_b32_e32 v110, v32
	v_mov_b32_e32 v111, v32
	v_mov_b32_e32 v112, v32
	v_mov_b32_e32 v113, v32
	v_mov_b32_e32 v114, v32
	v_mov_b32_e32 v115, v32
	v_mov_b32_e32 v116, v32
	v_mov_b32_e32 v117, v32
	v_mov_b32_e32 v118, v32
	v_mov_b32_e32 v119, v32
	v_mov_b32_e32 v120, v32
	v_mov_b32_e32 v121, v32
	v_mov_b32_e32 v122, v32
	v_mov_b32_e32 v123, v32
	v_mov_b32_e32 v124, v32
	v_mov_b32_e32 v125, v32
	v_mov_b32_e32 v126, v32
	v_mov_b32_e32 v127, v32
	v_mov_b32_e32 v128, v32
	v_mov_b32_e32 v129, v32
	v_mov_b32_e32 v130, v32
	v_mov_b32_e32 v131, v32
	v_mov_b32_e32 v132, v32
	v_mov_b32_e32 v133, v32
	v_mov_b32_e32 v134, v32
	v_mov_b32_e32 v135, v32
	v_mov_b32_e32 v136, v32
	v_mov_b32_e32 v137, v32
	v_mov_b32_e32 v138, v32
	v_mov_b32_e32 v139, v32
	v_mov_b32_e32 v140, v32
	v_mov_b32_e32 v141, v32
	v_mov_b32_e32 v142, v32
	v_mov_b32_e32 v143, v32
	v_mov_b32_e32 v144, v32
	v_mov_b32_e32 v145, v32
	v_mov_b32_e32 v146, v32
	v_mov_b32_e32 v147, v32
	v_mov_b32_e32 v148, v32
	v_mov_b32_e32 v149, v32
	v_mov_b32_e32 v150, v32
	v_mov_b32_e32 v151, v32
	v_mov_b32_e32 v152, v32
	v_mov_b32_e32 v153, v32
	v_mov_b32_e32 v154, v32
	v_mov_b32_e32 v155, v32
	v_mov_b32_e32 v156, v32
	v_mov_b32_e32 v157, v32
	v_mov_b32_e32 v158, v32
	v_mov_b32_e32 v159, v32
	v_mov_b32_e32 v198, 0
	v_mov_b32_e32 v199, 0
	v_mov_b32_e32 v200, 0
	v_mov_b32_e32 v201, 0
	v_mov_b32_e32 v202, 0
	v_mov_b32_e32 v203, 0
	v_mov_b32_e32 v204, 0
	v_mov_b32_e32 v205, 0
	v_mov_b32_e32 v244, 0
	v_mov_b32_e32 v245, 0
	v_mov_b32_e32 v246, 0
	v_mov_b32_e32 v247, 0
	v_mov_b32_e32 v248, 0
	v_mov_b32_e32 v249, 0
	v_mov_b32_e32 v250, 0
	v_mov_b32_e32 v251, 0
	v_mov_b32_e32 v252, 0
	v_mov_b32_e32 v253, 0
	v_mov_b32_e32 v254, 0
	v_mov_b32_e32 v255, 0
.LBB0_1038:
	s_mov_b32 m0, s64
	s_add_i32 s5, s4, 0xffffff80
	ds_read_b64_tr_b16 v[160:161], v178
	ds_read_b64_tr_b16 v[162:163], v179
	ds_read_b64_tr_b16 v[166:167], v179 offset:32
	ds_read_b128 v[168:171], v175
	ds_read_b64_tr_b16 v[164:165], v178 offset:32
	ds_read_b64_tr_b16 v[182:183], v178 offset:64
	ds_read_b64_tr_b16 v[186:187], v178 offset:96
	ds_read_b64_tr_b16 v[184:185], v179 offset:64
	ds_read_b64_tr_b16 v[188:189], v179 offset:96
	ds_read_b128 v[190:193], v175 offset:2048
	ds_read_b128 v[194:197], v175 offset:4096
	buffer_load_dwordx4 v176, s[16:19], s5 offen lds
	s_mov_b32 m0, s63
	v_mfma_f32_16x16x32_bf16 v[44:47], v[244:247], v[252:255], v[44:47]
	v_mfma_f32_16x16x32_bf16 v[40:43], v[248:251], v[252:255], v[40:43]
	v_mfma_f32_16x16x32_bf16 v[36:39], v[198:201], v[252:255], v[36:39]
	v_mfma_f32_16x16x32_bf16 v[32:35], v[202:205], v[252:255], v[32:35]
	s_waitcnt lgkmcnt(7)
	v_mfma_f32_16x16x32_bf16 v[156:159], v[160:163], v[168:171], v[156:159]
	buffer_load_dwordx4 v177, s[16:19], s5 offen lds
	s_mov_b32 m0, s62
	s_nop 0
	buffer_load_dwordx4 v180, s[16:19], s5 offen lds
	s_mov_b32 m0, s61
	s_waitcnt lgkmcnt(6)
	v_mfma_f32_16x16x32_bf16 v[152:155], v[164:167], v[168:171], v[152:155]
	buffer_load_dwordx4 v181, s[16:19], s5 offen lds
	s_add_i32 s5, s1, 0xfff20000
	s_waitcnt lgkmcnt(3)
	v_mfma_f32_16x16x32_bf16 v[148:151], v[182:185], v[168:171], v[148:151]
	s_waitcnt lgkmcnt(2)
	v_mfma_f32_16x16x32_bf16 v[144:147], v[186:189], v[168:171], v[144:147]
	s_waitcnt lgkmcnt(1)
	v_mfma_f32_16x16x32_bf16 v[140:143], v[160:163], v[190:193], v[140:143]
	ds_read_b128 v[168:171], v175 offset:6144
	s_waitcnt vmcnt(11)
	v_cvt_pk_bf16_f32 v15, v14, v15
	v_cvt_pk_bf16_f32 v14, v12, v13
	v_mfma_f32_16x16x32_bf16 v[136:139], v[164:167], v[190:193], v[136:139]
	ds_write_b64 v174, v[14:15] offset:34816
	v_mfma_f32_16x16x32_bf16 v[132:135], v[182:185], v[190:193], v[132:135]
	v_mfma_f32_16x16x32_bf16 v[128:131], v[186:189], v[190:193], v[128:131]
	buffer_load_dwordx4 v[12:15], v173, s[8:11], s5 offen
	s_waitcnt lgkmcnt(2)
	v_mfma_f32_16x16x32_bf16 v[124:127], v[160:163], v[194:197], v[124:127]
	ds_read_b128 v[190:193], v175 offset:8192
	v_mfma_f32_16x16x32_bf16 v[120:123], v[164:167], v[194:197], v[120:123]
	v_mfma_f32_16x16x32_bf16 v[116:119], v[182:185], v[194:197], v[116:119]
	v_mfma_f32_16x16x32_bf16 v[112:115], v[186:189], v[194:197], v[112:115]
	s_waitcnt lgkmcnt(2)
	v_mfma_f32_16x16x32_bf16 v[108:111], v[160:163], v[168:171], v[108:111]
	ds_read_b128 v[194:197], v175 offset:10240
	s_waitcnt vmcnt(10)
	v_cvt_pk_bf16_f32 v31, v30, v31
	v_cvt_pk_bf16_f32 v30, v28, v29
	v_mfma_f32_16x16x32_bf16 v[104:107], v[164:167], v[168:171], v[104:107]
	ds_write_b64 v174, v[30:31] offset:43520
	v_mfma_f32_16x16x32_bf16 v[100:103], v[182:185], v[168:171], v[100:103]
	v_mfma_f32_16x16x32_bf16 v[96:99], v[186:189], v[168:171], v[96:99]
	s_add_i32 s20, s1, 0xfff40000
	buffer_load_dwordx4 v[28:31], v173, s[8:11], s20 offen
	s_waitcnt lgkmcnt(2)
	v_mfma_f32_16x16x32_bf16 v[92:95], v[160:163], v[190:193], v[92:95]
	ds_read_b128 v[168:171], v175 offset:12288
	v_mfma_f32_16x16x32_bf16 v[88:91], v[164:167], v[190:193], v[88:91]
	v_mfma_f32_16x16x32_bf16 v[84:87], v[182:185], v[190:193], v[84:87]
	v_mfma_f32_16x16x32_bf16 v[80:83], v[186:189], v[190:193], v[80:83]
	s_waitcnt lgkmcnt(2)
	v_mfma_f32_16x16x32_bf16 v[76:79], v[160:163], v[194:197], v[76:79]
	ds_read_b128 v[190:193], v175 offset:14336
	v_cvt_pk_bf16_f32 v7, v6, v7
	v_cvt_pk_bf16_f32 v6, v4, v5
	v_mfma_f32_16x16x32_bf16 v[72:75], v[164:167], v[194:197], v[72:75]
	ds_write_b64 v174, v[6:7] offset:52224
	v_mfma_f32_16x16x32_bf16 v[68:71], v[182:185], v[194:197], v[68:71]
	v_mfma_f32_16x16x32_bf16 v[64:67], v[186:189], v[194:197], v[64:67]
	s_add_i32 s21, s1, 0xfff60000
	buffer_load_dwordx4 v[4:7], v173, s[8:11], s21 offen
	s_waitcnt lgkmcnt(2)
	v_mfma_f32_16x16x32_bf16 v[60:63], v[160:163], v[168:171], v[60:63]
	ds_read_b128 v[194:197], v175 offset:1024
	v_mfma_f32_16x16x32_bf16 v[56:59], v[164:167], v[168:171], v[56:59]
	v_mfma_f32_16x16x32_bf16 v[52:55], v[182:185], v[168:171], v[52:55]
	v_mfma_f32_16x16x32_bf16 v[48:51], v[186:189], v[168:171], v[48:51]
	s_waitcnt lgkmcnt(2)
	v_mfma_f32_16x16x32_bf16 v[44:47], v[160:163], v[190:193], v[44:47]
	ds_read_b128 v[160:163], v175 offset:3072
	s_waitcnt vmcnt(11)
	v_cvt_pk_bf16_f32 v27, v26, v27
	v_cvt_pk_bf16_f32 v26, v24, v25
	v_mfma_f32_16x16x32_bf16 v[40:43], v[164:167], v[190:193], v[40:43]
	ds_read_b64_tr_b16 v[244:245], v178 offset:17408
	ds_read_b64_tr_b16 v[248:249], v178 offset:17440
	ds_read_b64_tr_b16 v[198:199], v178 offset:17472
	ds_read_b64_tr_b16 v[202:203], v178 offset:17504
	ds_read_b64_tr_b16 v[246:247], v179 offset:17408
	ds_read_b64_tr_b16 v[250:251], v179 offset:17440
	ds_read_b64_tr_b16 v[200:201], v179 offset:17472
	ds_read_b64_tr_b16 v[204:205], v179 offset:17504
	ds_write_b64 v174, v[26:27] offset:60928
	v_mfma_f32_16x16x32_bf16 v[36:39], v[182:185], v[190:193], v[36:39]
	v_mfma_f32_16x16x32_bf16 v[32:35], v[186:189], v[190:193], v[32:35]
	s_add_i32 s22, s1, 0xfff80000
	buffer_load_dwordx4 v[24:27], v173, s[8:11], s22 offen
	s_waitcnt lgkmcnt(4)
	v_mfma_f32_16x16x32_bf16 v[156:159], v[244:247], v[194:197], v[156:159]
	ds_read_b128 v[182:185], v175 offset:5120
	s_waitcnt lgkmcnt(4)
	v_mfma_f32_16x16x32_bf16 v[152:155], v[248:251], v[194:197], v[152:155]
	s_waitcnt lgkmcnt(3)
	v_mfma_f32_16x16x32_bf16 v[148:151], v[198:201], v[194:197], v[148:151]
	s_waitcnt lgkmcnt(2)
	v_mfma_f32_16x16x32_bf16 v[144:147], v[202:205], v[194:197], v[144:147]
	v_mfma_f32_16x16x32_bf16 v[140:143], v[244:247], v[160:163], v[140:143]
	ds_read_b128 v[186:189], v175 offset:7168
	s_waitcnt vmcnt(11)
	v_cvt_pk_bf16_f32 v23, v22, v23
	v_cvt_pk_bf16_f32 v22, v20, v21
	v_mfma_f32_16x16x32_bf16 v[136:139], v[248:251], v[160:163], v[136:139]
	ds_write_b64 v174, v[22:23] offset:35072
	v_mfma_f32_16x16x32_bf16 v[132:135], v[198:201], v[160:163], v[132:135]
	v_mfma_f32_16x16x32_bf16 v[128:131], v[202:205], v[160:163], v[128:131]
	buffer_load_dwordx4 v[20:23], v173, s[12:15], s5 offen
	s_waitcnt lgkmcnt(2)
	v_mfma_f32_16x16x32_bf16 v[124:127], v[244:247], v[182:185], v[124:127]
	ds_read_b128 v[160:163], v175 offset:9216
	v_mfma_f32_16x16x32_bf16 v[120:123], v[248:251], v[182:185], v[120:123]
	v_mfma_f32_16x16x32_bf16 v[116:119], v[198:201], v[182:185], v[116:119]
	v_mfma_f32_16x16x32_bf16 v[112:115], v[202:205], v[182:185], v[112:115]
	s_waitcnt lgkmcnt(2)
	v_mfma_f32_16x16x32_bf16 v[108:111], v[244:247], v[186:189], v[108:111]
	ds_read_b128 v[182:185], v175 offset:11264
	s_waitcnt vmcnt(10)
	v_cvt_pk_bf16_f32 v11, v10, v11
	v_cvt_pk_bf16_f32 v10, v8, v9
	v_mfma_f32_16x16x32_bf16 v[104:107], v[248:251], v[186:189], v[104:107]
	ds_write_b64 v174, v[10:11] offset:43776
	v_mfma_f32_16x16x32_bf16 v[100:103], v[198:201], v[186:189], v[100:103]
	v_mfma_f32_16x16x32_bf16 v[96:99], v[202:205], v[186:189], v[96:99]
	buffer_load_dwordx4 v[8:11], v173, s[12:15], s20 offen
	s_waitcnt lgkmcnt(2)
	v_mfma_f32_16x16x32_bf16 v[92:95], v[244:247], v[160:163], v[92:95]
	ds_read_b128 v[186:189], v175 offset:13312
	v_mfma_f32_16x16x32_bf16 v[88:91], v[248:251], v[160:163], v[88:91]
	v_mfma_f32_16x16x32_bf16 v[84:87], v[198:201], v[160:163], v[84:87]
	v_mfma_f32_16x16x32_bf16 v[80:83], v[202:205], v[160:163], v[80:83]
	s_waitcnt lgkmcnt(2)
	v_mfma_f32_16x16x32_bf16 v[76:79], v[244:247], v[182:185], v[76:79]
	ds_read_b128 v[252:255], v175 offset:15360
	v_cvt_pk_bf16_f32 v3, v2, v3
	v_cvt_pk_bf16_f32 v2, v0, v1
	v_mfma_f32_16x16x32_bf16 v[72:75], v[248:251], v[182:185], v[72:75]
	ds_write_b64 v174, v[2:3] offset:52480
	v_mfma_f32_16x16x32_bf16 v[68:71], v[198:201], v[182:185], v[68:71]
	v_mfma_f32_16x16x32_bf16 v[64:67], v[202:205], v[182:185], v[64:67]
	buffer_load_dwordx4 v[0:3], v173, s[12:15], s21 offen
	s_waitcnt lgkmcnt(2)
	v_mfma_f32_16x16x32_bf16 v[60:63], v[244:247], v[186:189], v[60:63]
	v_mfma_f32_16x16x32_bf16 v[56:59], v[248:251], v[186:189], v[56:59]
	v_mfma_f32_16x16x32_bf16 v[52:55], v[198:201], v[186:189], v[52:55]
	v_mfma_f32_16x16x32_bf16 v[48:51], v[202:205], v[186:189], v[48:51]
	s_waitcnt lgkmcnt(1)
	s_waitcnt vmcnt(11)
	v_cvt_pk_bf16_f32 v19, v18, v19
	v_cvt_pk_bf16_f32 v18, v16, v17
	ds_write_b64 v174, v[18:19] offset:61184
	buffer_load_dwordx4 v[16:19], v173, s[12:15], s22 offen
	s_waitcnt vmcnt(8)
	s_mov_b32 m0, s45
	s_waitcnt lgkmcnt(0)
	s_barrier
	ds_read_b64_tr_b16 v[160:161], v178 offset:34816
	ds_read_b64_tr_b16 v[162:163], v179 offset:34816
	ds_read_b64_tr_b16 v[166:167], v179 offset:34848
	ds_read_b128 v[168:171], v175 offset:32768
	ds_read_b64_tr_b16 v[164:165], v178 offset:34848
	ds_read_b64_tr_b16 v[182:183], v178 offset:34880
	ds_read_b64_tr_b16 v[186:187], v178 offset:34912
	ds_read_b64_tr_b16 v[184:185], v179 offset:34880
	ds_read_b64_tr_b16 v[188:189], v179 offset:34912
	ds_read_b128 v[190:193], v175 offset:34816
	ds_read_b128 v[194:197], v175 offset:36864
	buffer_load_dwordx4 v176, s[16:19], s4 offen lds
	s_mov_b32 m0, s53
	v_mfma_f32_16x16x32_bf16 v[44:47], v[244:247], v[252:255], v[44:47]
	v_mfma_f32_16x16x32_bf16 v[40:43], v[248:251], v[252:255], v[40:43]
	v_mfma_f32_16x16x32_bf16 v[36:39], v[198:201], v[252:255], v[36:39]
	v_mfma_f32_16x16x32_bf16 v[32:35], v[202:205], v[252:255], v[32:35]
	s_waitcnt lgkmcnt(7)
	v_mfma_f32_16x16x32_bf16 v[156:159], v[160:163], v[168:171], v[156:159]
	buffer_load_dwordx4 v177, s[16:19], s4 offen lds
	s_mov_b32 m0, s54
	s_add_i32 s5, s1, 0xfffa0000
	buffer_load_dwordx4 v180, s[16:19], s4 offen lds
	s_mov_b32 m0, s55
	s_waitcnt lgkmcnt(6)
	v_mfma_f32_16x16x32_bf16 v[152:155], v[164:167], v[168:171], v[152:155]
	buffer_load_dwordx4 v181, s[16:19], s4 offen lds
	s_waitcnt lgkmcnt(3)
	v_mfma_f32_16x16x32_bf16 v[148:151], v[182:185], v[168:171], v[148:151]
	s_waitcnt lgkmcnt(2)
	v_mfma_f32_16x16x32_bf16 v[144:147], v[186:189], v[168:171], v[144:147]
	s_waitcnt lgkmcnt(1)
	v_mfma_f32_16x16x32_bf16 v[140:143], v[160:163], v[190:193], v[140:143]
	ds_read_b128 v[168:171], v175 offset:38912
	s_waitcnt vmcnt(11)
	v_cvt_pk_bf16_f32 v15, v14, v15
	v_cvt_pk_bf16_f32 v14, v12, v13
	v_mfma_f32_16x16x32_bf16 v[136:139], v[164:167], v[190:193], v[136:139]
	ds_write_b64 v174, v[14:15]
	v_mfma_f32_16x16x32_bf16 v[132:135], v[182:185], v[190:193], v[132:135]
	v_mfma_f32_16x16x32_bf16 v[128:131], v[186:189], v[190:193], v[128:131]
	buffer_load_dwordx4 v[12:15], v173, s[8:11], s5 offen
	s_waitcnt lgkmcnt(2)
	v_mfma_f32_16x16x32_bf16 v[124:127], v[160:163], v[194:197], v[124:127]
	ds_read_b128 v[190:193], v175 offset:40960
	v_mfma_f32_16x16x32_bf16 v[120:123], v[164:167], v[194:197], v[120:123]
	v_mfma_f32_16x16x32_bf16 v[116:119], v[182:185], v[194:197], v[116:119]
	v_mfma_f32_16x16x32_bf16 v[112:115], v[186:189], v[194:197], v[112:115]
	s_waitcnt lgkmcnt(2)
	v_mfma_f32_16x16x32_bf16 v[108:111], v[160:163], v[168:171], v[108:111]
	ds_read_b128 v[194:197], v175 offset:43008
	s_waitcnt vmcnt(11)
	v_cvt_pk_bf16_f32 v31, v30, v31
	v_cvt_pk_bf16_f32 v30, v28, v29
	v_mfma_f32_16x16x32_bf16 v[104:107], v[164:167], v[168:171], v[104:107]
	ds_write_b64 v174, v[30:31] offset:8704
	v_mfma_f32_16x16x32_bf16 v[100:103], v[182:185], v[168:171], v[100:103]
	v_mfma_f32_16x16x32_bf16 v[96:99], v[186:189], v[168:171], v[96:99]
	s_add_i32 s20, s1, 0xfffc0000
	buffer_load_dwordx4 v[28:31], v173, s[8:11], s20 offen
	s_waitcnt lgkmcnt(2)
	v_mfma_f32_16x16x32_bf16 v[92:95], v[160:163], v[190:193], v[92:95]
	ds_read_b128 v[168:171], v175 offset:45056
	v_mfma_f32_16x16x32_bf16 v[88:91], v[164:167], v[190:193], v[88:91]
	v_mfma_f32_16x16x32_bf16 v[84:87], v[182:185], v[190:193], v[84:87]
	v_mfma_f32_16x16x32_bf16 v[80:83], v[186:189], v[190:193], v[80:83]
	s_waitcnt lgkmcnt(2)
	v_mfma_f32_16x16x32_bf16 v[76:79], v[160:163], v[194:197], v[76:79]
	ds_read_b128 v[190:193], v175 offset:47104
	s_waitcnt vmcnt(11)
	v_cvt_pk_bf16_f32 v7, v6, v7
	v_cvt_pk_bf16_f32 v6, v4, v5
	v_mfma_f32_16x16x32_bf16 v[72:75], v[164:167], v[194:197], v[72:75]
	ds_write_b64 v174, v[6:7] offset:17408
	v_mfma_f32_16x16x32_bf16 v[68:71], v[182:185], v[194:197], v[68:71]
	v_mfma_f32_16x16x32_bf16 v[64:67], v[186:189], v[194:197], v[64:67]
	s_add_i32 s21, s1, 0xfffe0000
	buffer_load_dwordx4 v[4:7], v173, s[8:11], s21 offen
	s_waitcnt lgkmcnt(2)
	v_mfma_f32_16x16x32_bf16 v[60:63], v[160:163], v[168:171], v[60:63]
	ds_read_b128 v[194:197], v175 offset:33792
	v_mfma_f32_16x16x32_bf16 v[56:59], v[164:167], v[168:171], v[56:59]
	v_mfma_f32_16x16x32_bf16 v[52:55], v[182:185], v[168:171], v[52:55]
	v_mfma_f32_16x16x32_bf16 v[48:51], v[186:189], v[168:171], v[48:51]
	s_waitcnt lgkmcnt(2)
	v_mfma_f32_16x16x32_bf16 v[44:47], v[160:163], v[190:193], v[44:47]
	ds_read_b128 v[160:163], v175 offset:35840
	s_waitcnt vmcnt(11)
; #define G_DMA_A(kt, AO) do { G_DMA1(kt, AO, 0); G_DMA1(kt, AO, 1); G_DMA1(kt, AO, 2); G_DMA1(kt, AO, 3); if (MF == 9) G_DMA5(kt, AO); } while (0)
; #define G_ISSUE_B(kt) do { const unsigned _sb = (unsigned)(kt) * 4u * kstepB; \
;         _Pragma("unroll") for (int _i = 0; _i < 8; ++_i) sb[_i] = bload16(_i < 4 ? rsB0 : rsB1, vob, _sb + (_i & 3) * kstepB); } while (0)
; #define G_WRITE_B(BO) do { \
;         _Pragma("unroll") for (int _i = 0; _i < 8; ++_i) *(LAS u32x2*)(b_wr + (BO) + (_i & 3) * (16 * G_BSTRIDE) + (_i >> 2) * SLAB1) = pack4(__builtin_bit_cast(f32x4, sb[_i])); } while (0)
; #define G_ENDTILE(VM) do { asm volatile("s_waitcnt vmcnt(" #VM ")" ::: "memory"); \
;         asm volatile("s_waitcnt lgkmcnt(0)" ::: "memory"); __builtin_amdgcn_s_barrier(); asm volatile("" ::: "memory"); } while (0)
;     ...
;     __builtin_amdgcn_s_barrier();
;     G_DMA_A(0, G_A0); G_ISSUE_B(0); G_WRITE_B(G_B0);
;     __builtin_amdgcn_sched_barrier(0);
;     G_ISSUE_B(1);
;     __builtin_amdgcn_sched_barrier(0);
;     G_ENDTILE(8);
;     for (int ui = 0;; ++ui) {
; #pragma unroll
;         for (int m = 0; m < MF; ++m)
; #pragma unroll
;             for (int n = 0; n < 4; ++n) acc[m][n] = (f32x4){0.f, 0.f, 0.f, 0.f};
;         for (int t = 0; t < nt - 2; t += 2) {
;             G_TILE(G_A0, G_B0, true, G_B1, G_A1, t + 1, true, t + 2, (void)0);
;             G_ENDTILE(8);
;             G_TILE(G_A1, G_B1, true, G_B0, G_A0, t + 2, true, t + 3, (void)0);
;             G_ENDTILE(8);
;         }
	v_cvt_pk_bf16_f32 v27, v26, v27
	v_cvt_pk_bf16_f32 v26, v24, v25
	v_mfma_f32_16x16x32_bf16 v[40:43], v[164:167], v[190:193], v[40:43]
	ds_read_b64_tr_b16 v[244:245], v178 offset:52224
	ds_read_b64_tr_b16 v[248:249], v178 offset:52256
	ds_read_b64_tr_b16 v[198:199], v178 offset:52288
	ds_read_b64_tr_b16 v[202:203], v178 offset:52320
	ds_read_b64_tr_b16 v[246:247], v179 offset:52224
	ds_read_b64_tr_b16 v[250:251], v179 offset:52256
	ds_read_b64_tr_b16 v[200:201], v179 offset:52288
	ds_read_b64_tr_b16 v[204:205], v179 offset:52320
	ds_write_b64 v174, v[26:27] offset:26112
	v_mfma_f32_16x16x32_bf16 v[36:39], v[182:185], v[190:193], v[36:39]
	v_mfma_f32_16x16x32_bf16 v[32:35], v[186:189], v[190:193], v[32:35]
	buffer_load_dwordx4 v[24:27], v173, s[8:11], s1 offen
	s_waitcnt lgkmcnt(4)
	v_mfma_f32_16x16x32_bf16 v[156:159], v[244:247], v[194:197], v[156:159]
	ds_read_b128 v[182:185], v175 offset:37888
	s_waitcnt lgkmcnt(4)
	v_mfma_f32_16x16x32_bf16 v[152:155], v[248:251], v[194:197], v[152:155]
	s_waitcnt lgkmcnt(3)
	v_mfma_f32_16x16x32_bf16 v[148:151], v[198:201], v[194:197], v[148:151]
	s_waitcnt lgkmcnt(2)
	v_mfma_f32_16x16x32_bf16 v[144:147], v[202:205], v[194:197], v[144:147]
	v_mfma_f32_16x16x32_bf16 v[140:143], v[244:247], v[160:163], v[140:143]
	ds_read_b128 v[186:189], v175 offset:39936
	s_waitcnt vmcnt(11)
	v_cvt_pk_bf16_f32 v23, v22, v23
	v_cvt_pk_bf16_f32 v22, v20, v21
	v_mfma_f32_16x16x32_bf16 v[136:139], v[248:251], v[160:163], v[136:139]
	ds_write_b64 v174, v[22:23] offset:256
	v_mfma_f32_16x16x32_bf16 v[132:135], v[198:201], v[160:163], v[132:135]
	v_mfma_f32_16x16x32_bf16 v[128:131], v[202:205], v[160:163], v[128:131]
	buffer_load_dwordx4 v[20:23], v173, s[12:15], s5 offen
	s_waitcnt lgkmcnt(2)
	v_mfma_f32_16x16x32_bf16 v[124:127], v[244:247], v[182:185], v[124:127]
	ds_read_b128 v[160:163], v175 offset:41984
	v_mfma_f32_16x16x32_bf16 v[120:123], v[248:251], v[182:185], v[120:123]
	v_mfma_f32_16x16x32_bf16 v[116:119], v[198:201], v[182:185], v[116:119]
	v_mfma_f32_16x16x32_bf16 v[112:115], v[202:205], v[182:185], v[112:115]
	s_waitcnt lgkmcnt(2)
	v_mfma_f32_16x16x32_bf16 v[108:111], v[244:247], v[186:189], v[108:111]
	ds_read_b128 v[182:185], v175 offset:44032
	s_waitcnt vmcnt(11)
	v_cvt_pk_bf16_f32 v11, v10, v11
	v_cvt_pk_bf16_f32 v10, v8, v9
	v_mfma_f32_16x16x32_bf16 v[104:107], v[248:251], v[186:189], v[104:107]
	ds_write_b64 v174, v[10:11] offset:8960
	v_mfma_f32_16x16x32_bf16 v[100:103], v[198:201], v[186:189], v[100:103]
	v_mfma_f32_16x16x32_bf16 v[96:99], v[202:205], v[186:189], v[96:99]
	buffer_load_dwordx4 v[8:11], v173, s[12:15], s20 offen
	s_waitcnt lgkmcnt(2)
	v_mfma_f32_16x16x32_bf16 v[92:95], v[244:247], v[160:163], v[92:95]
	ds_read_b128 v[186:189], v175 offset:46080
	v_mfma_f32_16x16x32_bf16 v[88:91], v[248:251], v[160:163], v[88:91]
	v_mfma_f32_16x16x32_bf16 v[84:87], v[198:201], v[160:163], v[84:87]
	v_mfma_f32_16x16x32_bf16 v[80:83], v[202:205], v[160:163], v[80:83]
	s_waitcnt lgkmcnt(2)
	v_mfma_f32_16x16x32_bf16 v[76:79], v[244:247], v[182:185], v[76:79]
	ds_read_b128 v[252:255], v175 offset:48128
	s_waitcnt vmcnt(11)
	v_cvt_pk_bf16_f32 v3, v2, v3
	v_cvt_pk_bf16_f32 v2, v0, v1
	v_mfma_f32_16x16x32_bf16 v[72:75], v[248:251], v[182:185], v[72:75]
	ds_write_b64 v174, v[2:3] offset:17664
	v_mfma_f32_16x16x32_bf16 v[68:71], v[198:201], v[182:185], v[68:71]
	v_mfma_f32_16x16x32_bf16 v[64:67], v[202:205], v[182:185], v[64:67]
	buffer_load_dwordx4 v[0:3], v173, s[12:15], s21 offen
	s_waitcnt lgkmcnt(2)
	v_mfma_f32_16x16x32_bf16 v[60:63], v[244:247], v[186:189], v[60:63]
	v_mfma_f32_16x16x32_bf16 v[56:59], v[248:251], v[186:189], v[56:59]
	v_mfma_f32_16x16x32_bf16 v[52:55], v[198:201], v[186:189], v[52:55]
	v_mfma_f32_16x16x32_bf16 v[48:51], v[202:205], v[186:189], v[48:51]
	s_waitcnt lgkmcnt(1)
	s_waitcnt vmcnt(11)
	v_cvt_pk_bf16_f32 v19, v18, v19
	v_cvt_pk_bf16_f32 v18, v16, v17
	ds_write_b64 v174, v[18:19] offset:26368
	buffer_load_dwordx4 v[16:19], v173, s[12:15], s1 offen
	s_waitcnt vmcnt(8)
	s_waitcnt lgkmcnt(0)
	s_barrier
	s_add_i32 s0, s0, 2
	s_add_i32 s1, s1, 0x100000
	s_addk_i32 s4, 0x100
	s_cmp_ge_i32 s0, s60
	s_cbranch_scc0 .LBB0_1038
	v_mfma_f32_16x16x32_bf16 v[44:47], v[244:247], v[252:255], v[44:47]
	v_mfma_f32_16x16x32_bf16 v[40:43], v[248:251], v[252:255], v[40:43]
	v_mfma_f32_16x16x32_bf16 v[36:39], v[198:201], v[252:255], v[36:39]
	v_mfma_f32_16x16x32_bf16 v[32:35], v[202:205], v[252:255], v[32:35]
	s_branch .LBB0_1040
